# weight-slab quantiser: counted vmcnt ladder so row groups are consumed as they arrive (12 inlined copies waited for the whole slab with vmcnt(0))
# baseline (speedup 1.0000x reference)
; __device__ __forceinline__ unsigned cvt_pk_bf16(float lo, float hi) { unsigned r; asm volatile("v_cvt_pk_bf16_f32 %0, %1, %2" : "=v"(r) : "v"(lo), "v"(hi)); return r; }
; __device__ __forceinline__ void do_slabs_impl(LAS unsigned char* lds, unsigned char* ws, const float* w_up, const float* w_dn, const float* w_in, int vcu, int G, int wave, int j0, int j1) {
;     ...
;         if (cur.valid) {
;             f32x4 mx = (f32x4){0.f, 0.f, 0.f, 0.f};
; #pragma unroll
;             for (int i = 0; i < 32; ++i) { const int k = wave * 256 + i * 8 + kq; const f32x4 x = v[i];
;                 mx[0] = fmaxf(mx[0], fabsf(x[0])); mx[1] = fmaxf(mx[1], fabsf(x[1])); mx[2] = fmaxf(mx[2], fabsf(x[2])); mx[3] = fmaxf(mx[3], fabsf(x[3]));
;                 const unsigned p01 = cvt_pk_bf16(x[0], x[1]), p23 = cvt_pk_bf16(x[2], x[3]);
;                 const int ks = k ^ (((c4 >> 3) & 3) << 3);
;                 slab[(c4 + 0) * PITCH + ks] = (bf16)(p01 & 0xffffu); slab[(c4 + 1) * PITCH + ks] = (bf16)(p01 >> 16); slab[(c4 + 2) * PITCH + ks] = (bf16)(p23 & 0xffffu); slab[(c4 + 3) * PITCH + ks] = (bf16)(p23 >> 16); }
.LBB0_395:
	s_cmp_lg_u32 s20, 0
	s_cselect_b64 s[36:37], -1, 0
	s_cmp_eq_u32 s20, 0
	s_cbranch_scc1 .LBB0_399
	s_waitcnt vmcnt(31)
	v_cvt_pk_bf16_f32 v128, v0, v1
	v_cvt_pk_bf16_f32 v129, v2, v3
	ds_write_b16 v144, v128
	ds_write_b16_d16_hi v144, v128 offset:4112
	ds_write_b16 v144, v129 offset:8224
	ds_write_b16_d16_hi v144, v129 offset:12336
	s_waitcnt vmcnt(30)
	v_cvt_pk_bf16_f32 v136, v4, v5
	v_cvt_pk_bf16_f32 v137, v6, v7
	ds_write_b16 v145, v136
	ds_write_b16_d16_hi v145, v136 offset:4112
	ds_write_b16 v145, v137 offset:8224
	ds_write_b16_d16_hi v145, v137 offset:12336
	s_waitcnt vmcnt(29)
	v_cvt_pk_bf16_f32 v136, v8, v9
	v_cvt_pk_bf16_f32 v137, v10, v11
	ds_write_b16 v146, v136
	ds_write_b16_d16_hi v146, v136 offset:4112
	ds_write_b16 v146, v137 offset:8224
	ds_write_b16_d16_hi v146, v137 offset:12336
	s_waitcnt vmcnt(28)
	v_cvt_pk_bf16_f32 v136, v12, v13
	v_cvt_pk_bf16_f32 v137, v14, v15
	ds_write_b16 v147, v136
	ds_write_b16_d16_hi v147, v136 offset:4112
	ds_write_b16 v147, v137 offset:8224
	ds_write_b16_d16_hi v147, v137 offset:12336
	s_waitcnt vmcnt(27)
	v_cvt_pk_bf16_f32 v136, v16, v17
	v_cvt_pk_bf16_f32 v137, v18, v19
	ds_write_b16 v148, v136
	ds_write_b16_d16_hi v148, v136 offset:4112
	ds_write_b16 v148, v137 offset:8224
	ds_write_b16_d16_hi v148, v137 offset:12336
	s_waitcnt vmcnt(26)
	v_cvt_pk_bf16_f32 v136, v20, v21
	v_cvt_pk_bf16_f32 v137, v22, v23
	ds_write_b16 v149, v136
	ds_write_b16_d16_hi v149, v136 offset:4112
	ds_write_b16 v149, v137 offset:8224
	ds_write_b16_d16_hi v149, v137 offset:12336
	s_waitcnt vmcnt(25)
	v_cvt_pk_bf16_f32 v136, v24, v25
	v_cvt_pk_bf16_f32 v137, v26, v27
	ds_write_b16 v150, v136
	ds_write_b16_d16_hi v150, v136 offset:4112
	ds_write_b16 v150, v137 offset:8224
	ds_write_b16_d16_hi v150, v137 offset:12336
	s_waitcnt vmcnt(24)
	v_cvt_pk_bf16_f32 v136, v28, v29
	v_cvt_pk_bf16_f32 v137, v30, v31
	ds_write_b16 v151, v136
	ds_write_b16_d16_hi v151, v136 offset:4112
	ds_write_b16 v151, v137 offset:8224
	ds_write_b16_d16_hi v151, v137 offset:12336
	s_waitcnt vmcnt(23)
	v_cvt_pk_bf16_f32 v136, v32, v33
	v_cvt_pk_bf16_f32 v137, v34, v35
	ds_write_b16 v152, v136
	ds_write_b16_d16_hi v152, v136 offset:4112
	ds_write_b16 v152, v137 offset:8224
	ds_write_b16_d16_hi v152, v137 offset:12336
	s_waitcnt vmcnt(22)
	v_cvt_pk_bf16_f32 v136, v36, v37
	v_cvt_pk_bf16_f32 v137, v38, v39
	ds_write_b16 v153, v136
	ds_write_b16_d16_hi v153, v136 offset:4112
	ds_write_b16 v153, v137 offset:8224
	ds_write_b16_d16_hi v153, v137 offset:12336
	s_waitcnt vmcnt(21)
	v_cvt_pk_bf16_f32 v136, v40, v41
	v_cvt_pk_bf16_f32 v137, v42, v43
	ds_write_b16 v154, v136
	ds_write_b16_d16_hi v154, v136 offset:4112
	ds_write_b16 v154, v137 offset:8224
	ds_write_b16_d16_hi v154, v137 offset:12336
	s_waitcnt vmcnt(20)
	v_cvt_pk_bf16_f32 v136, v44, v45
	v_cvt_pk_bf16_f32 v137, v46, v47
	ds_write_b16 v155, v136
	ds_write_b16_d16_hi v155, v136 offset:4112
	ds_write_b16 v155, v137 offset:8224
	ds_write_b16_d16_hi v155, v137 offset:12336
	s_waitcnt vmcnt(19)
	v_cvt_pk_bf16_f32 v136, v48, v49
	v_cvt_pk_bf16_f32 v137, v50, v51
	ds_write_b16 v156, v136
	ds_write_b16_d16_hi v156, v136 offset:4112
	ds_write_b16 v156, v137 offset:8224
	ds_write_b16_d16_hi v156, v137 offset:12336
	s_waitcnt vmcnt(18)
	v_cvt_pk_bf16_f32 v136, v52, v53
	v_cvt_pk_bf16_f32 v137, v54, v55
	ds_write_b16 v157, v136
	ds_write_b16_d16_hi v157, v136 offset:4112
	ds_write_b16 v157, v137 offset:8224
	ds_write_b16_d16_hi v157, v137 offset:12336
	s_waitcnt vmcnt(17)
	v_cvt_pk_bf16_f32 v136, v56, v57
	v_cvt_pk_bf16_f32 v137, v58, v59
	ds_write_b16 v158, v136
	ds_write_b16_d16_hi v158, v136 offset:4112
	ds_write_b16 v158, v137 offset:8224
	ds_write_b16_d16_hi v158, v137 offset:12336
	s_waitcnt vmcnt(16)
	v_cvt_pk_bf16_f32 v136, v60, v61
	v_cvt_pk_bf16_f32 v137, v62, v63
	ds_write_b16 v159, v136
	ds_write_b16_d16_hi v159, v136 offset:4112
	ds_write_b16 v159, v137 offset:8224
	ds_write_b16_d16_hi v159, v137 offset:12336
	s_waitcnt vmcnt(15)
	v_cvt_pk_bf16_f32 v136, v64, v65
	v_cvt_pk_bf16_f32 v137, v66, v67
	v_max3_f32 v130, |v2|, 0, |v6|
	ds_write_b16 v160, v136
	ds_write_b16_d16_hi v160, v136 offset:4112
	ds_write_b16 v160, v137 offset:8224
	ds_write_b16_d16_hi v160, v137 offset:12336
	s_waitcnt vmcnt(14)
	v_cvt_pk_bf16_f32 v136, v68, v69
	v_cvt_pk_bf16_f32 v137, v70, v71
	v_max3_f32 v130, v130, |v10|, |v14|
	ds_write_b16 v161, v136
	ds_write_b16_d16_hi v161, v136 offset:4112
	ds_write_b16 v161, v137 offset:8224
	ds_write_b16_d16_hi v161, v137 offset:12336
	s_waitcnt vmcnt(13)
	v_cvt_pk_bf16_f32 v136, v72, v73
	v_cvt_pk_bf16_f32 v137, v74, v75
	v_max3_f32 v130, v130, |v18|, |v22|
	ds_write_b16 v162, v136
	ds_write_b16_d16_hi v162, v136 offset:4112
	ds_write_b16 v162, v137 offset:8224
	ds_write_b16_d16_hi v162, v137 offset:12336
	s_waitcnt vmcnt(12)
	v_cvt_pk_bf16_f32 v136, v76, v77
	v_cvt_pk_bf16_f32 v137, v78, v79
	v_max3_f32 v128, |v0|, 0, |v4|
	v_max3_f32 v130, v130, |v26|, |v30|
	ds_write_b16 v163, v136
	ds_write_b16_d16_hi v163, v136 offset:4112
	ds_write_b16 v163, v137 offset:8224
	ds_write_b16_d16_hi v163, v137 offset:12336
	s_waitcnt vmcnt(11)
	v_cvt_pk_bf16_f32 v136, v80, v81
	v_cvt_pk_bf16_f32 v137, v82, v83
	v_max3_f32 v128, v128, |v8|, |v12|
	v_max3_f32 v130, v130, |v34|, |v38|
	ds_write_b16 v164, v136
	ds_write_b16_d16_hi v164, v136 offset:4112
	ds_write_b16 v164, v137 offset:8224
	ds_write_b16_d16_hi v164, v137 offset:12336
	s_waitcnt vmcnt(10)
	v_cvt_pk_bf16_f32 v136, v84, v85
	v_cvt_pk_bf16_f32 v137, v86, v87
	v_max3_f32 v128, v128, |v16|, |v20|
	v_max3_f32 v130, v130, |v42|, |v46|
	ds_write_b16 v165, v136
	ds_write_b16_d16_hi v165, v136 offset:4112
	ds_write_b16 v165, v137 offset:8224
	ds_write_b16_d16_hi v165, v137 offset:12336
	s_waitcnt vmcnt(9)
; #define LAS __attribute__((address_space(3)))
; __device__ __forceinline__ unsigned cvt_pk_bf16(float lo, float hi) { unsigned r; asm volatile("v_cvt_pk_bf16_f32 %0, %1, %2" : "=v"(r) : "v"(lo), "v"(hi)); return r; }
; __device__ __forceinline__ void do_slabs_impl(LAS unsigned char* lds, unsigned char* ws, const float* w_up, const float* w_dn, const float* w_in, int vcu, int G, int wave, int j0, int j1) {
;     ...
;             for (int i = 0; i < 32; ++i) { const int k = wave * 256 + i * 8 + kq; const f32x4 x = v[i];
;                 mx[0] = fmaxf(mx[0], fabsf(x[0])); mx[1] = fmaxf(mx[1], fabsf(x[1])); mx[2] = fmaxf(mx[2], fabsf(x[2])); mx[3] = fmaxf(mx[3], fabsf(x[3]));
;                 const unsigned p01 = cvt_pk_bf16(x[0], x[1]), p23 = cvt_pk_bf16(x[2], x[3]);
;                 const int ks = k ^ (((c4 >> 3) & 3) << 3);
;                 slab[(c4 + 0) * PITCH + ks] = (bf16)(p01 & 0xffffu); slab[(c4 + 1) * PITCH + ks] = (bf16)(p01 >> 16); slab[(c4 + 2) * PITCH + ks] = (bf16)(p23 & 0xffffu); slab[(c4 + 3) * PITCH + ks] = (bf16)(p23 >> 16); }
; #pragma unroll
;             for (int q = 0; q < 4; ++q) { float m = mx[q]; m = fmaxf(m, __shfl_xor(m, 8)); m = fmaxf(m, __shfl_xor(m, 16)); m = fmaxf(m, __shfl_xor(m, 32)); mx[q] = m; }
;             if (lane < 8) { LAS float* d = red + wave * 32 + c4; d[0] = mx[0]; d[1] = mx[1]; d[2] = mx[2]; d[3] = mx[3]; }
	v_cvt_pk_bf16_f32 v136, v88, v89
	v_cvt_pk_bf16_f32 v137, v90, v91
	v_max3_f32 v128, v128, |v24|, |v28|
	v_max3_f32 v130, v130, |v50|, |v54|
	ds_write_b16 v166, v136
	ds_write_b16_d16_hi v166, v136 offset:4112
	ds_write_b16 v166, v137 offset:8224
	ds_write_b16_d16_hi v166, v137 offset:12336
	s_waitcnt vmcnt(8)
	v_cvt_pk_bf16_f32 v136, v92, v93
	v_cvt_pk_bf16_f32 v137, v94, v95
	v_max3_f32 v129, |v1|, 0, |v5|
	v_max3_f32 v128, v128, |v32|, |v36|
	v_max3_f32 v130, v130, |v58|, |v62|
	ds_write_b16 v167, v136
	ds_write_b16_d16_hi v167, v136 offset:4112
	ds_write_b16 v167, v137 offset:8224
	ds_write_b16_d16_hi v167, v137 offset:12336
	s_waitcnt vmcnt(7)
	v_cvt_pk_bf16_f32 v136, v96, v97
	v_cvt_pk_bf16_f32 v137, v98, v99
	v_max3_f32 v129, v129, |v9|, |v13|
	v_max3_f32 v128, v128, |v40|, |v44|
	v_max3_f32 v130, v130, |v66|, |v70|
	ds_write_b16 v168, v136
	ds_write_b16_d16_hi v168, v136 offset:4112
	ds_write_b16 v168, v137 offset:8224
	ds_write_b16_d16_hi v168, v137 offset:12336
	s_waitcnt vmcnt(6)
	v_cvt_pk_bf16_f32 v136, v100, v101
	v_cvt_pk_bf16_f32 v137, v102, v103
	v_max3_f32 v129, v129, |v17|, |v21|
	v_max3_f32 v128, v128, |v48|, |v52|
	v_max3_f32 v130, v130, |v74|, |v78|
	ds_write_b16 v169, v136
	ds_write_b16_d16_hi v169, v136 offset:4112
	ds_write_b16 v169, v137 offset:8224
	ds_write_b16_d16_hi v169, v137 offset:12336
	s_waitcnt vmcnt(5)
	v_cvt_pk_bf16_f32 v136, v104, v105
	v_cvt_pk_bf16_f32 v137, v106, v107
	v_max3_f32 v129, v129, |v25|, |v29|
	v_max3_f32 v128, v128, |v56|, |v60|
	v_max3_f32 v130, v130, |v82|, |v86|
	ds_write_b16 v170, v136
	ds_write_b16_d16_hi v170, v136 offset:4112
	ds_write_b16 v170, v137 offset:8224
	ds_write_b16_d16_hi v170, v137 offset:12336
	s_waitcnt vmcnt(4)
	v_cvt_pk_bf16_f32 v136, v108, v109
	v_cvt_pk_bf16_f32 v137, v110, v111
	v_max3_f32 v129, v129, |v33|, |v37|
	v_max3_f32 v128, v128, |v64|, |v68|
	v_max3_f32 v130, v130, |v90|, |v94|
	ds_write_b16 v171, v136
	ds_write_b16_d16_hi v171, v136 offset:4112
	ds_write_b16 v171, v137 offset:8224
	ds_write_b16_d16_hi v171, v137 offset:12336
	s_waitcnt vmcnt(3)
	v_cvt_pk_bf16_f32 v136, v112, v113
	v_cvt_pk_bf16_f32 v137, v114, v115
	v_max3_f32 v129, v129, |v41|, |v45|
	v_max3_f32 v128, v128, |v72|, |v76|
	v_max3_f32 v130, v130, |v98|, |v102|
	ds_write_b16 v172, v136
	ds_write_b16_d16_hi v172, v136 offset:4112
	ds_write_b16 v172, v137 offset:8224
	ds_write_b16_d16_hi v172, v137 offset:12336
	s_waitcnt vmcnt(2)
	v_cvt_pk_bf16_f32 v136, v116, v117
	v_cvt_pk_bf16_f32 v137, v118, v119
	v_max3_f32 v129, v129, |v49|, |v53|
	v_max3_f32 v128, v128, |v80|, |v84|
	v_max3_f32 v130, v130, |v106|, |v110|
	ds_write_b16 v173, v136
	ds_write_b16_d16_hi v173, v136 offset:4112
	ds_write_b16 v173, v137 offset:8224
	ds_write_b16_d16_hi v173, v137 offset:12336
	s_waitcnt vmcnt(1)
	v_cvt_pk_bf16_f32 v136, v120, v121
	v_cvt_pk_bf16_f32 v137, v122, v123
	v_max3_f32 v129, v129, |v57|, |v61|
	v_max3_f32 v128, v128, |v88|, |v92|
	v_max3_f32 v130, v130, |v114|, |v118|
	ds_write_b16 v174, v136
	ds_write_b16_d16_hi v174, v136 offset:4112
	ds_write_b16 v174, v137 offset:8224
	ds_write_b16_d16_hi v174, v137 offset:12336
	v_and_b32_e32 v137, 64, v177
	v_max3_f32 v131, |v3|, 0, |v7|
	v_max3_f32 v129, v129, |v65|, |v69|
	v_max3_f32 v128, v128, |v96|, |v100|
	s_waitcnt vmcnt(0)
	v_max3_f32 v136, v130, |v122|, |v126|
	v_xor_b32_e32 v130, 8, v177
	v_add_u32_e32 v137, 64, v137
	v_max3_f32 v131, v131, |v11|, |v15|
	v_max3_f32 v129, v129, |v73|, |v77|
	v_max3_f32 v128, v128, |v104|, |v108|
	v_cmp_lt_i32_e32 vcc, v130, v137
	v_max3_f32 v131, v131, |v19|, |v23|
	v_max3_f32 v129, v129, |v81|, |v85|
	v_max3_f32 v128, v128, |v112|, |v116|
	v_cndmask_b32_e32 v130, v177, v130, vcc
	v_max3_f32 v131, v131, |v27|, |v31|
	v_max3_f32 v129, v129, |v89|, |v93|
	v_max3_f32 v128, v128, |v120|, |v124|
	v_lshlrev_b32_e32 v130, 2, v130
	v_max3_f32 v131, v131, |v35|, |v39|
	v_max3_f32 v129, v129, |v97|, |v101|
	ds_bpermute_b32 v139, v130, v128
	v_max3_f32 v131, v131, |v43|, |v47|
	v_max3_f32 v129, v129, |v105|, |v109|
	v_xor_b32_e32 v138, 16, v177
	v_max3_f32 v131, v131, |v51|, |v55|
	v_max3_f32 v129, v129, |v113|, |v117|
	v_cmp_lt_i32_e32 vcc, v138, v137
	v_xor_b32_e32 v182, 32, v177
	v_max3_f32 v131, v131, |v59|, |v63|
	v_max3_f32 v129, v129, |v121|, |v125|
	v_cndmask_b32_e32 v138, v177, v138, vcc
	v_cmp_lt_i32_e32 vcc, v182, v137
	v_max3_f32 v131, v131, |v67|, |v71|
	v_max3_f32 v131, v131, |v75|, |v79|
	v_cndmask_b32_e32 v137, v177, v182, vcc
	ds_bpermute_b32 v182, v130, v129
	s_waitcnt lgkmcnt(0)
	v_max_f32_e32 v139, v139, v139
	v_max3_f32 v131, v131, |v83|, |v87|
	v_lshlrev_b32_e32 v138, 2, v138
	v_max_f32_e32 v128, v128, v139
	v_max3_f32 v131, v131, |v91|, |v95|
	ds_bpermute_b32 v139, v138, v128
	v_max3_f32 v131, v131, |v99|, |v103|
	v_max3_f32 v131, v131, |v107|, |v111|
	v_lshlrev_b32_e32 v183, 2, v137
	v_max_f32_e32 v137, v182, v182
	v_max3_f32 v131, v131, |v115|, |v119|
	v_max_f32_e32 v137, v129, v137
	v_max3_f32 v131, v131, |v123|, |v127|
	ds_bpermute_b32 v182, v138, v137
	s_waitcnt lgkmcnt(1)
	v_max_f32_e32 v129, v139, v139
	ds_bpermute_b32 v139, v130, v136
	ds_bpermute_b32 v184, v130, v131
	v_max_f32_e32 v128, v128, v129
	s_waitcnt lgkmcnt(2)
	v_max_f32_e32 v182, v182, v182
	v_max_f32_e32 v130, v137, v182
	s_waitcnt lgkmcnt(1)
	v_max_f32_e32 v137, v139, v139
	s_waitcnt lgkmcnt(0)
	v_max_f32_e32 v139, v184, v184
	v_max_f32_e32 v136, v136, v137
	v_max_f32_e32 v139, v131, v139
	ds_bpermute_b32 v137, v138, v136
	ds_bpermute_b32 v138, v138, v139
	ds_bpermute_b32 v129, v183, v128
	ds_bpermute_b32 v131, v183, v130
	v_cvt_pk_bf16_f32 v180, v124, v125
	s_waitcnt lgkmcnt(3)
	v_max_f32_e32 v137, v137, v137
	s_waitcnt lgkmcnt(2)
	v_max_f32_e32 v138, v138, v138
	v_max_f32_e32 v136, v136, v137
	v_max_f32_e32 v138, v139, v138
	ds_bpermute_b32 v137, v183, v136
	ds_bpermute_b32 v139, v183, v138
	v_cvt_pk_bf16_f32 v181, v126, v127
	ds_write_b16 v175, v180
	ds_write_b16_d16_hi v175, v180 offset:4112
	ds_write_b16 v175, v181 offset:8224
	ds_write_b16_d16_hi v175, v181 offset:12336
	s_and_saveexec_b64 s[38:39], s[4:5]
	s_cbranch_execz .LBB0_398
	s_waitcnt lgkmcnt(4)
	v_max_f32_e32 v139, v139, v139
	v_max_f32_e32 v138, v138, v138
	v_max_f32_e32 v137, v137, v137
	v_max_f32_e32 v136, v136, v136
	v_max_f32_e32 v131, v131, v131
	v_max_f32_e32 v130, v130, v130
	v_max_f32_e32 v129, v129, v129
	v_max_f32_e32 v128, v128, v128
	v_max_f32_e32 v139, v138, v139
	v_max_f32_e32 v138, v136, v137
	v_max_f32_e32 v137, v130, v131
	v_max_f32_e32 v136, v128, v129
	ds_write_b128 v176, v[136:139]

; __device__ __forceinline__ unsigned cvt_pk_bf16(float lo, float hi) { unsigned r; asm volatile("v_cvt_pk_bf16_f32 %0, %1, %2" : "=v"(r) : "v"(lo), "v"(hi)); return r; }
; __device__ __forceinline__ void do_slabs_impl(LAS unsigned char* lds, unsigned char* ws, const float* w_up, const float* w_dn, const float* w_in, int vcu, int G, int wave, int j0, int j1) {
;     ...
;         if (cur.valid) {
;             f32x4 mx = (f32x4){0.f, 0.f, 0.f, 0.f};
; #pragma unroll
;             for (int i = 0; i < 32; ++i) { const int k = wave * 256 + i * 8 + kq; const f32x4 x = v[i];
;                 mx[0] = fmaxf(mx[0], fabsf(x[0])); mx[1] = fmaxf(mx[1], fabsf(x[1])); mx[2] = fmaxf(mx[2], fabsf(x[2])); mx[3] = fmaxf(mx[3], fabsf(x[3]));
;                 const unsigned p01 = cvt_pk_bf16(x[0], x[1]), p23 = cvt_pk_bf16(x[2], x[3]);
;                 const int ks = k ^ (((c4 >> 3) & 3) << 3);
;                 slab[(c4 + 0) * PITCH + ks] = (bf16)(p01 & 0xffffu); slab[(c4 + 1) * PITCH + ks] = (bf16)(p01 >> 16); slab[(c4 + 2) * PITCH + ks] = (bf16)(p23 & 0xffffu); slab[(c4 + 3) * PITCH + ks] = (bf16)(p23 >> 16); }
.LBB0_613:
	s_cmp_lg_u32 s47, 0
	s_cselect_b64 s[42:43], -1, 0
	s_cmp_eq_u32 s47, 0
	s_cbranch_scc1 .LBB0_617
	s_waitcnt vmcnt(31)
	v_cvt_pk_bf16_f32 v128, v0, v1
	v_cvt_pk_bf16_f32 v129, v2, v3
	ds_write_b16 v144, v128
	ds_write_b16_d16_hi v144, v128 offset:4112
	ds_write_b16 v144, v129 offset:8224
	ds_write_b16_d16_hi v144, v129 offset:12336
	s_waitcnt vmcnt(30)
	v_cvt_pk_bf16_f32 v136, v4, v5
	v_cvt_pk_bf16_f32 v137, v6, v7
	ds_write_b16 v145, v136
	ds_write_b16_d16_hi v145, v136 offset:4112
	ds_write_b16 v145, v137 offset:8224
	ds_write_b16_d16_hi v145, v137 offset:12336
	s_waitcnt vmcnt(29)
	v_cvt_pk_bf16_f32 v136, v8, v9
	v_cvt_pk_bf16_f32 v137, v10, v11
	ds_write_b16 v146, v136
	ds_write_b16_d16_hi v146, v136 offset:4112
	ds_write_b16 v146, v137 offset:8224
	ds_write_b16_d16_hi v146, v137 offset:12336
	s_waitcnt vmcnt(28)
	v_cvt_pk_bf16_f32 v136, v12, v13
	v_cvt_pk_bf16_f32 v137, v14, v15
	ds_write_b16 v147, v136
	ds_write_b16_d16_hi v147, v136 offset:4112
	ds_write_b16 v147, v137 offset:8224
	ds_write_b16_d16_hi v147, v137 offset:12336
	s_waitcnt vmcnt(27)
	v_cvt_pk_bf16_f32 v136, v16, v17
	v_cvt_pk_bf16_f32 v137, v18, v19
	ds_write_b16 v148, v136
	ds_write_b16_d16_hi v148, v136 offset:4112
	ds_write_b16 v148, v137 offset:8224
	ds_write_b16_d16_hi v148, v137 offset:12336
	s_waitcnt vmcnt(26)
	v_cvt_pk_bf16_f32 v136, v20, v21
	v_cvt_pk_bf16_f32 v137, v22, v23
	ds_write_b16 v149, v136
	ds_write_b16_d16_hi v149, v136 offset:4112
	ds_write_b16 v149, v137 offset:8224
	ds_write_b16_d16_hi v149, v137 offset:12336
	s_waitcnt vmcnt(25)
	v_cvt_pk_bf16_f32 v136, v24, v25
	v_cvt_pk_bf16_f32 v137, v26, v27
	ds_write_b16 v150, v136
	ds_write_b16_d16_hi v150, v136 offset:4112
	ds_write_b16 v150, v137 offset:8224
	ds_write_b16_d16_hi v150, v137 offset:12336
	s_waitcnt vmcnt(24)
	v_cvt_pk_bf16_f32 v136, v28, v29
	v_cvt_pk_bf16_f32 v137, v30, v31
	ds_write_b16 v151, v136
	ds_write_b16_d16_hi v151, v136 offset:4112
	ds_write_b16 v151, v137 offset:8224
	ds_write_b16_d16_hi v151, v137 offset:12336
	s_waitcnt vmcnt(23)
	v_cvt_pk_bf16_f32 v136, v32, v33
	v_cvt_pk_bf16_f32 v137, v34, v35
	ds_write_b16 v152, v136
	ds_write_b16_d16_hi v152, v136 offset:4112
	ds_write_b16 v152, v137 offset:8224
	ds_write_b16_d16_hi v152, v137 offset:12336
	s_waitcnt vmcnt(22)
	v_cvt_pk_bf16_f32 v136, v36, v37
	v_cvt_pk_bf16_f32 v137, v38, v39
	ds_write_b16 v153, v136
	ds_write_b16_d16_hi v153, v136 offset:4112
	ds_write_b16 v153, v137 offset:8224
	ds_write_b16_d16_hi v153, v137 offset:12336
	s_waitcnt vmcnt(21)
	v_cvt_pk_bf16_f32 v136, v40, v41
	v_cvt_pk_bf16_f32 v137, v42, v43
	ds_write_b16 v154, v136
	ds_write_b16_d16_hi v154, v136 offset:4112
	ds_write_b16 v154, v137 offset:8224
	ds_write_b16_d16_hi v154, v137 offset:12336
	s_waitcnt vmcnt(20)
	v_cvt_pk_bf16_f32 v136, v44, v45
	v_cvt_pk_bf16_f32 v137, v46, v47
	ds_write_b16 v155, v136
	ds_write_b16_d16_hi v155, v136 offset:4112
	ds_write_b16 v155, v137 offset:8224
	ds_write_b16_d16_hi v155, v137 offset:12336
	s_waitcnt vmcnt(19)
	v_cvt_pk_bf16_f32 v136, v48, v49
	v_cvt_pk_bf16_f32 v137, v50, v51
	ds_write_b16 v156, v136
	ds_write_b16_d16_hi v156, v136 offset:4112
	ds_write_b16 v156, v137 offset:8224
	ds_write_b16_d16_hi v156, v137 offset:12336
	s_waitcnt vmcnt(18)
	v_cvt_pk_bf16_f32 v136, v52, v53
	v_cvt_pk_bf16_f32 v137, v54, v55
	ds_write_b16 v157, v136
	ds_write_b16_d16_hi v157, v136 offset:4112
	ds_write_b16 v157, v137 offset:8224
	ds_write_b16_d16_hi v157, v137 offset:12336
	s_waitcnt vmcnt(17)
	v_cvt_pk_bf16_f32 v136, v56, v57
	v_cvt_pk_bf16_f32 v137, v58, v59
	ds_write_b16 v158, v136
	ds_write_b16_d16_hi v158, v136 offset:4112
	ds_write_b16 v158, v137 offset:8224
	ds_write_b16_d16_hi v158, v137 offset:12336
	s_waitcnt vmcnt(16)
	v_cvt_pk_bf16_f32 v136, v60, v61
	v_cvt_pk_bf16_f32 v137, v62, v63
	ds_write_b16 v159, v136
	ds_write_b16_d16_hi v159, v136 offset:4112
	ds_write_b16 v159, v137 offset:8224
	ds_write_b16_d16_hi v159, v137 offset:12336
	s_waitcnt vmcnt(15)
	v_cvt_pk_bf16_f32 v136, v64, v65
	v_cvt_pk_bf16_f32 v137, v66, v67
	v_max3_f32 v130, |v2|, 0, |v6|
	ds_write_b16 v160, v136
	ds_write_b16_d16_hi v160, v136 offset:4112
	ds_write_b16 v160, v137 offset:8224
	ds_write_b16_d16_hi v160, v137 offset:12336
	s_waitcnt vmcnt(14)
	v_cvt_pk_bf16_f32 v136, v68, v69
	v_cvt_pk_bf16_f32 v137, v70, v71
	v_max3_f32 v130, v130, |v10|, |v14|
	ds_write_b16 v161, v136
	ds_write_b16_d16_hi v161, v136 offset:4112
	ds_write_b16 v161, v137 offset:8224
	ds_write_b16_d16_hi v161, v137 offset:12336
	s_waitcnt vmcnt(13)
	v_cvt_pk_bf16_f32 v136, v72, v73
	v_cvt_pk_bf16_f32 v137, v74, v75
	v_max3_f32 v130, v130, |v18|, |v22|
	ds_write_b16 v162, v136
	ds_write_b16_d16_hi v162, v136 offset:4112
	ds_write_b16 v162, v137 offset:8224
	ds_write_b16_d16_hi v162, v137 offset:12336
	s_waitcnt vmcnt(12)
	v_cvt_pk_bf16_f32 v136, v76, v77
	v_cvt_pk_bf16_f32 v137, v78, v79
	v_max3_f32 v128, |v0|, 0, |v4|
	v_max3_f32 v130, v130, |v26|, |v30|
	ds_write_b16 v163, v136
	ds_write_b16_d16_hi v163, v136 offset:4112
	ds_write_b16 v163, v137 offset:8224
	ds_write_b16_d16_hi v163, v137 offset:12336
	s_waitcnt vmcnt(11)
	v_cvt_pk_bf16_f32 v136, v80, v81
	v_cvt_pk_bf16_f32 v137, v82, v83
	v_max3_f32 v128, v128, |v8|, |v12|
	v_max3_f32 v130, v130, |v34|, |v38|
	ds_write_b16 v164, v136
	ds_write_b16_d16_hi v164, v136 offset:4112
	ds_write_b16 v164, v137 offset:8224
	ds_write_b16_d16_hi v164, v137 offset:12336
	s_waitcnt vmcnt(10)
	v_cvt_pk_bf16_f32 v136, v84, v85
	v_cvt_pk_bf16_f32 v137, v86, v87
	v_max3_f32 v128, v128, |v16|, |v20|
	v_max3_f32 v130, v130, |v42|, |v46|
	ds_write_b16 v165, v136
	ds_write_b16_d16_hi v165, v136 offset:4112
	ds_write_b16 v165, v137 offset:8224
	ds_write_b16_d16_hi v165, v137 offset:12336
	s_waitcnt vmcnt(9)
; #define LAS __attribute__((address_space(3)))
; __device__ __forceinline__ unsigned cvt_pk_bf16(float lo, float hi) { unsigned r; asm volatile("v_cvt_pk_bf16_f32 %0, %1, %2" : "=v"(r) : "v"(lo), "v"(hi)); return r; }
; __device__ __forceinline__ void do_slabs_impl(LAS unsigned char* lds, unsigned char* ws, const float* w_up, const float* w_dn, const float* w_in, int vcu, int G, int wave, int j0, int j1) {
;     ...
;             for (int i = 0; i < 32; ++i) { const int k = wave * 256 + i * 8 + kq; const f32x4 x = v[i];
;                 mx[0] = fmaxf(mx[0], fabsf(x[0])); mx[1] = fmaxf(mx[1], fabsf(x[1])); mx[2] = fmaxf(mx[2], fabsf(x[2])); mx[3] = fmaxf(mx[3], fabsf(x[3]));
;                 const unsigned p01 = cvt_pk_bf16(x[0], x[1]), p23 = cvt_pk_bf16(x[2], x[3]);
;                 const int ks = k ^ (((c4 >> 3) & 3) << 3);
;                 slab[(c4 + 0) * PITCH + ks] = (bf16)(p01 & 0xffffu); slab[(c4 + 1) * PITCH + ks] = (bf16)(p01 >> 16); slab[(c4 + 2) * PITCH + ks] = (bf16)(p23 & 0xffffu); slab[(c4 + 3) * PITCH + ks] = (bf16)(p23 >> 16); }
; #pragma unroll
;             for (int q = 0; q < 4; ++q) { float m = mx[q]; m = fmaxf(m, __shfl_xor(m, 8)); m = fmaxf(m, __shfl_xor(m, 16)); m = fmaxf(m, __shfl_xor(m, 32)); mx[q] = m; }
;             if (lane < 8) { LAS float* d = red + wave * 32 + c4; d[0] = mx[0]; d[1] = mx[1]; d[2] = mx[2]; d[3] = mx[3]; }
	v_cvt_pk_bf16_f32 v136, v88, v89
	v_cvt_pk_bf16_f32 v137, v90, v91
	v_max3_f32 v128, v128, |v24|, |v28|
	v_max3_f32 v130, v130, |v50|, |v54|
	ds_write_b16 v166, v136
	ds_write_b16_d16_hi v166, v136 offset:4112
	ds_write_b16 v166, v137 offset:8224
	ds_write_b16_d16_hi v166, v137 offset:12336
	s_waitcnt vmcnt(8)
	v_cvt_pk_bf16_f32 v136, v92, v93
	v_cvt_pk_bf16_f32 v137, v94, v95
	v_max3_f32 v129, |v1|, 0, |v5|
	v_max3_f32 v128, v128, |v32|, |v36|
	v_max3_f32 v130, v130, |v58|, |v62|
	ds_write_b16 v167, v136
	ds_write_b16_d16_hi v167, v136 offset:4112
	ds_write_b16 v167, v137 offset:8224
	ds_write_b16_d16_hi v167, v137 offset:12336
	s_waitcnt vmcnt(7)
	v_cvt_pk_bf16_f32 v136, v96, v97
	v_cvt_pk_bf16_f32 v137, v98, v99
	v_max3_f32 v129, v129, |v9|, |v13|
	v_max3_f32 v128, v128, |v40|, |v44|
	v_max3_f32 v130, v130, |v66|, |v70|
	ds_write_b16 v168, v136
	ds_write_b16_d16_hi v168, v136 offset:4112
	ds_write_b16 v168, v137 offset:8224
	ds_write_b16_d16_hi v168, v137 offset:12336
	s_waitcnt vmcnt(6)
	v_cvt_pk_bf16_f32 v136, v100, v101
	v_cvt_pk_bf16_f32 v137, v102, v103
	v_max3_f32 v129, v129, |v17|, |v21|
	v_max3_f32 v128, v128, |v48|, |v52|
	v_max3_f32 v130, v130, |v74|, |v78|
	ds_write_b16 v169, v136
	ds_write_b16_d16_hi v169, v136 offset:4112
	ds_write_b16 v169, v137 offset:8224
	ds_write_b16_d16_hi v169, v137 offset:12336
	s_waitcnt vmcnt(5)
	v_cvt_pk_bf16_f32 v136, v104, v105
	v_cvt_pk_bf16_f32 v137, v106, v107
	v_max3_f32 v129, v129, |v25|, |v29|
	v_max3_f32 v128, v128, |v56|, |v60|
	v_max3_f32 v130, v130, |v82|, |v86|
	ds_write_b16 v170, v136
	ds_write_b16_d16_hi v170, v136 offset:4112
	ds_write_b16 v170, v137 offset:8224
	ds_write_b16_d16_hi v170, v137 offset:12336
	s_waitcnt vmcnt(4)
	v_cvt_pk_bf16_f32 v136, v108, v109
	v_cvt_pk_bf16_f32 v137, v110, v111
	v_max3_f32 v129, v129, |v33|, |v37|
	v_max3_f32 v128, v128, |v64|, |v68|
	v_max3_f32 v130, v130, |v90|, |v94|
	ds_write_b16 v171, v136
	ds_write_b16_d16_hi v171, v136 offset:4112
	ds_write_b16 v171, v137 offset:8224
	ds_write_b16_d16_hi v171, v137 offset:12336
	s_waitcnt vmcnt(3)
	v_cvt_pk_bf16_f32 v136, v112, v113
	v_cvt_pk_bf16_f32 v137, v114, v115
	v_max3_f32 v129, v129, |v41|, |v45|
	v_max3_f32 v128, v128, |v72|, |v76|
	v_max3_f32 v130, v130, |v98|, |v102|
	ds_write_b16 v172, v136
	ds_write_b16_d16_hi v172, v136 offset:4112
	ds_write_b16 v172, v137 offset:8224
	ds_write_b16_d16_hi v172, v137 offset:12336
	s_waitcnt vmcnt(2)
	v_cvt_pk_bf16_f32 v136, v116, v117
	v_cvt_pk_bf16_f32 v137, v118, v119
	v_max3_f32 v129, v129, |v49|, |v53|
	v_max3_f32 v128, v128, |v80|, |v84|
	v_max3_f32 v130, v130, |v106|, |v110|
	ds_write_b16 v173, v136
	ds_write_b16_d16_hi v173, v136 offset:4112
	ds_write_b16 v173, v137 offset:8224
	ds_write_b16_d16_hi v173, v137 offset:12336
	s_waitcnt vmcnt(1)
	v_cvt_pk_bf16_f32 v136, v120, v121
	v_cvt_pk_bf16_f32 v137, v122, v123
	v_max3_f32 v129, v129, |v57|, |v61|
	v_max3_f32 v128, v128, |v88|, |v92|
	v_max3_f32 v130, v130, |v114|, |v118|
	ds_write_b16 v174, v136
	ds_write_b16_d16_hi v174, v136 offset:4112
	ds_write_b16 v174, v137 offset:8224
	ds_write_b16_d16_hi v174, v137 offset:12336
	v_and_b32_e32 v137, 64, v177
	v_max3_f32 v131, |v3|, 0, |v7|
	v_max3_f32 v129, v129, |v65|, |v69|
	v_max3_f32 v128, v128, |v96|, |v100|
	s_waitcnt vmcnt(0)
	v_max3_f32 v136, v130, |v122|, |v126|
	v_xor_b32_e32 v130, 8, v177
	v_add_u32_e32 v137, 64, v137
	v_max3_f32 v131, v131, |v11|, |v15|
	v_max3_f32 v129, v129, |v73|, |v77|
	v_max3_f32 v128, v128, |v104|, |v108|
	v_cmp_lt_i32_e32 vcc, v130, v137
	v_max3_f32 v131, v131, |v19|, |v23|
	v_max3_f32 v129, v129, |v81|, |v85|
	v_max3_f32 v128, v128, |v112|, |v116|
	v_cndmask_b32_e32 v130, v177, v130, vcc
	v_max3_f32 v131, v131, |v27|, |v31|
	v_max3_f32 v129, v129, |v89|, |v93|
	v_max3_f32 v128, v128, |v120|, |v124|
	v_lshlrev_b32_e32 v130, 2, v130
	v_max3_f32 v131, v131, |v35|, |v39|
	v_max3_f32 v129, v129, |v97|, |v101|
	ds_bpermute_b32 v139, v130, v128
	v_max3_f32 v131, v131, |v43|, |v47|
	v_max3_f32 v129, v129, |v105|, |v109|
	v_xor_b32_e32 v138, 16, v177
	v_max3_f32 v131, v131, |v51|, |v55|
	v_max3_f32 v129, v129, |v113|, |v117|
	v_cmp_lt_i32_e32 vcc, v138, v137
	v_xor_b32_e32 v182, 32, v177
	v_max3_f32 v131, v131, |v59|, |v63|
	v_max3_f32 v129, v129, |v121|, |v125|
	v_cndmask_b32_e32 v138, v177, v138, vcc
	v_cmp_lt_i32_e32 vcc, v182, v137
	v_max3_f32 v131, v131, |v67|, |v71|
	v_max3_f32 v131, v131, |v75|, |v79|
	v_cndmask_b32_e32 v137, v177, v182, vcc
	ds_bpermute_b32 v182, v130, v129
	s_waitcnt lgkmcnt(1)
	v_max_f32_e32 v139, v139, v139
	v_max3_f32 v131, v131, |v83|, |v87|
	v_lshlrev_b32_e32 v138, 2, v138
	v_max_f32_e32 v128, v128, v139
	v_max3_f32 v131, v131, |v91|, |v95|
	ds_bpermute_b32 v139, v138, v128
	v_max3_f32 v131, v131, |v99|, |v103|
	v_max3_f32 v131, v131, |v107|, |v111|
	v_lshlrev_b32_e32 v183, 2, v137
	s_waitcnt lgkmcnt(1)
	v_max_f32_e32 v137, v182, v182
	v_max3_f32 v131, v131, |v115|, |v119|
	v_max_f32_e32 v137, v129, v137
	v_max3_f32 v131, v131, |v123|, |v127|
	ds_bpermute_b32 v182, v138, v137
	s_waitcnt lgkmcnt(1)
	v_max_f32_e32 v129, v139, v139
	ds_bpermute_b32 v139, v130, v136
	ds_bpermute_b32 v184, v130, v131
	v_max_f32_e32 v128, v128, v129
	s_waitcnt lgkmcnt(2)
	v_max_f32_e32 v182, v182, v182
	v_max_f32_e32 v130, v137, v182
	s_waitcnt lgkmcnt(1)
	v_max_f32_e32 v137, v139, v139
	s_waitcnt lgkmcnt(0)
	v_max_f32_e32 v139, v184, v184
	v_max_f32_e32 v136, v136, v137
	v_max_f32_e32 v139, v131, v139
	ds_bpermute_b32 v137, v138, v136
	ds_bpermute_b32 v138, v138, v139
	ds_bpermute_b32 v129, v183, v128
	ds_bpermute_b32 v131, v183, v130
	v_cvt_pk_bf16_f32 v180, v124, v125
	s_waitcnt lgkmcnt(3)
	v_max_f32_e32 v137, v137, v137
	s_waitcnt lgkmcnt(2)
	v_max_f32_e32 v138, v138, v138
	v_max_f32_e32 v136, v136, v137
	v_max_f32_e32 v138, v139, v138
	ds_bpermute_b32 v137, v183, v136
	ds_bpermute_b32 v139, v183, v138
	v_cvt_pk_bf16_f32 v181, v126, v127
	ds_write_b16 v175, v180
	ds_write_b16_d16_hi v175, v180 offset:4112
	ds_write_b16 v175, v181 offset:8224
	ds_write_b16_d16_hi v175, v181 offset:12336
	s_and_saveexec_b64 s[44:45], s[4:5]
	s_cbranch_execz .LBB0_616
	s_waitcnt lgkmcnt(4)
	v_max_f32_e32 v139, v139, v139
	v_max_f32_e32 v138, v138, v138
	v_max_f32_e32 v137, v137, v137
	v_max_f32_e32 v136, v136, v136
	v_max_f32_e32 v131, v131, v131
	v_max_f32_e32 v130, v130, v130
	v_max_f32_e32 v129, v129, v129
	v_max_f32_e32 v128, v128, v128
	v_max_f32_e32 v139, v138, v139
	v_max_f32_e32 v138, v136, v137
	v_max_f32_e32 v137, v130, v131
	v_max_f32_e32 v136, v128, v129
	ds_write_b128 v176, v[136:139]

; __device__ __forceinline__ unsigned cvt_pk_bf16(float lo, float hi) { unsigned r; asm volatile("v_cvt_pk_bf16_f32 %0, %1, %2" : "=v"(r) : "v"(lo), "v"(hi)); return r; }
; __device__ __forceinline__ void do_slabs_impl(LAS unsigned char* lds, unsigned char* ws, const float* w_up, const float* w_dn, const float* w_in, int vcu, int G, int wave, int j0, int j1) {
;     ...
;         if (cur.valid) {
;             f32x4 mx = (f32x4){0.f, 0.f, 0.f, 0.f};
; #pragma unroll
;             for (int i = 0; i < 32; ++i) { const int k = wave * 256 + i * 8 + kq; const f32x4 x = v[i];
;                 mx[0] = fmaxf(mx[0], fabsf(x[0])); mx[1] = fmaxf(mx[1], fabsf(x[1])); mx[2] = fmaxf(mx[2], fabsf(x[2])); mx[3] = fmaxf(mx[3], fabsf(x[3]));
;                 const unsigned p01 = cvt_pk_bf16(x[0], x[1]), p23 = cvt_pk_bf16(x[2], x[3]);
;                 const int ks = k ^ (((c4 >> 3) & 3) << 3);
;                 slab[(c4 + 0) * PITCH + ks] = (bf16)(p01 & 0xffffu); slab[(c4 + 1) * PITCH + ks] = (bf16)(p01 >> 16); slab[(c4 + 2) * PITCH + ks] = (bf16)(p23 & 0xffffu); slab[(c4 + 3) * PITCH + ks] = (bf16)(p23 >> 16); }
.LBB0_648:
	s_cmp_lg_u32 s43, 0
	s_cselect_b64 s[38:39], -1, 0
	s_cmp_eq_u32 s43, 0
	s_cbranch_scc1 .LBB0_652
	s_waitcnt vmcnt(31)
	v_cvt_pk_bf16_f32 v128, v0, v1
	v_cvt_pk_bf16_f32 v129, v2, v3
	ds_write_b16 v144, v128
	ds_write_b16_d16_hi v144, v128 offset:4112
	ds_write_b16 v144, v129 offset:8224
	ds_write_b16_d16_hi v144, v129 offset:12336
	s_waitcnt vmcnt(30)
	v_cvt_pk_bf16_f32 v136, v4, v5
	v_cvt_pk_bf16_f32 v137, v6, v7
	ds_write_b16 v145, v136
	ds_write_b16_d16_hi v145, v136 offset:4112
	ds_write_b16 v145, v137 offset:8224
	ds_write_b16_d16_hi v145, v137 offset:12336
	s_waitcnt vmcnt(29)
	v_cvt_pk_bf16_f32 v136, v8, v9
	v_cvt_pk_bf16_f32 v137, v10, v11
	ds_write_b16 v146, v136
	ds_write_b16_d16_hi v146, v136 offset:4112
	ds_write_b16 v146, v137 offset:8224
	ds_write_b16_d16_hi v146, v137 offset:12336
	s_waitcnt vmcnt(28)
	v_cvt_pk_bf16_f32 v136, v12, v13
	v_cvt_pk_bf16_f32 v137, v14, v15
	ds_write_b16 v147, v136
	ds_write_b16_d16_hi v147, v136 offset:4112
	ds_write_b16 v147, v137 offset:8224
	ds_write_b16_d16_hi v147, v137 offset:12336
	s_waitcnt vmcnt(27)
	v_cvt_pk_bf16_f32 v136, v16, v17
	v_cvt_pk_bf16_f32 v137, v18, v19
	ds_write_b16 v148, v136
	ds_write_b16_d16_hi v148, v136 offset:4112
	ds_write_b16 v148, v137 offset:8224
	ds_write_b16_d16_hi v148, v137 offset:12336
	s_waitcnt vmcnt(26)
	v_cvt_pk_bf16_f32 v136, v20, v21
	v_cvt_pk_bf16_f32 v137, v22, v23
	ds_write_b16 v149, v136
	ds_write_b16_d16_hi v149, v136 offset:4112
	ds_write_b16 v149, v137 offset:8224
	ds_write_b16_d16_hi v149, v137 offset:12336
	s_waitcnt vmcnt(25)
	v_cvt_pk_bf16_f32 v136, v24, v25
	v_cvt_pk_bf16_f32 v137, v26, v27
	ds_write_b16 v150, v136
	ds_write_b16_d16_hi v150, v136 offset:4112
	ds_write_b16 v150, v137 offset:8224
	ds_write_b16_d16_hi v150, v137 offset:12336
	s_waitcnt vmcnt(24)
	v_cvt_pk_bf16_f32 v136, v28, v29
	v_cvt_pk_bf16_f32 v137, v30, v31
	ds_write_b16 v151, v136
	ds_write_b16_d16_hi v151, v136 offset:4112
	ds_write_b16 v151, v137 offset:8224
	ds_write_b16_d16_hi v151, v137 offset:12336
	s_waitcnt vmcnt(23)
	v_cvt_pk_bf16_f32 v136, v32, v33
	v_cvt_pk_bf16_f32 v137, v34, v35
	ds_write_b16 v152, v136
	ds_write_b16_d16_hi v152, v136 offset:4112
	ds_write_b16 v152, v137 offset:8224
	ds_write_b16_d16_hi v152, v137 offset:12336
	s_waitcnt vmcnt(22)
	v_cvt_pk_bf16_f32 v136, v36, v37
	v_cvt_pk_bf16_f32 v137, v38, v39
	ds_write_b16 v153, v136
	ds_write_b16_d16_hi v153, v136 offset:4112
	ds_write_b16 v153, v137 offset:8224
	ds_write_b16_d16_hi v153, v137 offset:12336
	s_waitcnt vmcnt(21)
	v_cvt_pk_bf16_f32 v136, v40, v41
	v_cvt_pk_bf16_f32 v137, v42, v43
	ds_write_b16 v154, v136
	ds_write_b16_d16_hi v154, v136 offset:4112
	ds_write_b16 v154, v137 offset:8224
	ds_write_b16_d16_hi v154, v137 offset:12336
	s_waitcnt vmcnt(20)
	v_cvt_pk_bf16_f32 v136, v44, v45
	v_cvt_pk_bf16_f32 v137, v46, v47
	ds_write_b16 v155, v136
	ds_write_b16_d16_hi v155, v136 offset:4112
	ds_write_b16 v155, v137 offset:8224
	ds_write_b16_d16_hi v155, v137 offset:12336
	s_waitcnt vmcnt(19)
	v_cvt_pk_bf16_f32 v136, v48, v49
	v_cvt_pk_bf16_f32 v137, v50, v51
	ds_write_b16 v156, v136
	ds_write_b16_d16_hi v156, v136 offset:4112
	ds_write_b16 v156, v137 offset:8224
	ds_write_b16_d16_hi v156, v137 offset:12336
	s_waitcnt vmcnt(18)
	v_cvt_pk_bf16_f32 v136, v52, v53
	v_cvt_pk_bf16_f32 v137, v54, v55
	ds_write_b16 v157, v136
	ds_write_b16_d16_hi v157, v136 offset:4112
	ds_write_b16 v157, v137 offset:8224
	ds_write_b16_d16_hi v157, v137 offset:12336
	s_waitcnt vmcnt(17)
	v_cvt_pk_bf16_f32 v136, v56, v57
	v_cvt_pk_bf16_f32 v137, v58, v59
	ds_write_b16 v158, v136
	ds_write_b16_d16_hi v158, v136 offset:4112
	ds_write_b16 v158, v137 offset:8224
	ds_write_b16_d16_hi v158, v137 offset:12336
	s_waitcnt vmcnt(16)
	v_cvt_pk_bf16_f32 v136, v60, v61
	v_cvt_pk_bf16_f32 v137, v62, v63
	ds_write_b16 v159, v136
	ds_write_b16_d16_hi v159, v136 offset:4112
	ds_write_b16 v159, v137 offset:8224
	ds_write_b16_d16_hi v159, v137 offset:12336
	s_waitcnt vmcnt(15)
	v_cvt_pk_bf16_f32 v136, v64, v65
	v_cvt_pk_bf16_f32 v137, v66, v67
	v_max3_f32 v130, |v2|, 0, |v6|
	ds_write_b16 v160, v136
	ds_write_b16_d16_hi v160, v136 offset:4112
	ds_write_b16 v160, v137 offset:8224
	ds_write_b16_d16_hi v160, v137 offset:12336
	s_waitcnt vmcnt(14)
	v_cvt_pk_bf16_f32 v136, v68, v69
	v_cvt_pk_bf16_f32 v137, v70, v71
	v_max3_f32 v130, v130, |v10|, |v14|
	ds_write_b16 v161, v136
	ds_write_b16_d16_hi v161, v136 offset:4112
	ds_write_b16 v161, v137 offset:8224
	ds_write_b16_d16_hi v161, v137 offset:12336
	s_waitcnt vmcnt(13)
	v_cvt_pk_bf16_f32 v136, v72, v73
	v_cvt_pk_bf16_f32 v137, v74, v75
	v_max3_f32 v130, v130, |v18|, |v22|
	ds_write_b16 v162, v136
	ds_write_b16_d16_hi v162, v136 offset:4112
	ds_write_b16 v162, v137 offset:8224
	ds_write_b16_d16_hi v162, v137 offset:12336
	s_waitcnt vmcnt(12)
	v_cvt_pk_bf16_f32 v136, v76, v77
	v_cvt_pk_bf16_f32 v137, v78, v79
	v_max3_f32 v128, |v0|, 0, |v4|
	v_max3_f32 v130, v130, |v26|, |v30|
	ds_write_b16 v163, v136
	ds_write_b16_d16_hi v163, v136 offset:4112
	ds_write_b16 v163, v137 offset:8224
	ds_write_b16_d16_hi v163, v137 offset:12336
	s_waitcnt vmcnt(11)
	v_cvt_pk_bf16_f32 v136, v80, v81
	v_cvt_pk_bf16_f32 v137, v82, v83
	v_max3_f32 v128, v128, |v8|, |v12|
	v_max3_f32 v130, v130, |v34|, |v38|
	ds_write_b16 v164, v136
	ds_write_b16_d16_hi v164, v136 offset:4112
	ds_write_b16 v164, v137 offset:8224
	ds_write_b16_d16_hi v164, v137 offset:12336
	s_waitcnt vmcnt(10)
	v_cvt_pk_bf16_f32 v136, v84, v85
	v_cvt_pk_bf16_f32 v137, v86, v87
	v_max3_f32 v128, v128, |v16|, |v20|
	v_max3_f32 v130, v130, |v42|, |v46|
	ds_write_b16 v165, v136
	ds_write_b16_d16_hi v165, v136 offset:4112
	ds_write_b16 v165, v137 offset:8224
	ds_write_b16_d16_hi v165, v137 offset:12336
	s_waitcnt vmcnt(9)
; #define LAS __attribute__((address_space(3)))
; __device__ __forceinline__ unsigned cvt_pk_bf16(float lo, float hi) { unsigned r; asm volatile("v_cvt_pk_bf16_f32 %0, %1, %2" : "=v"(r) : "v"(lo), "v"(hi)); return r; }
; __device__ __forceinline__ void do_slabs_impl(LAS unsigned char* lds, unsigned char* ws, const float* w_up, const float* w_dn, const float* w_in, int vcu, int G, int wave, int j0, int j1) {
;     ...
;             for (int i = 0; i < 32; ++i) { const int k = wave * 256 + i * 8 + kq; const f32x4 x = v[i];
;                 mx[0] = fmaxf(mx[0], fabsf(x[0])); mx[1] = fmaxf(mx[1], fabsf(x[1])); mx[2] = fmaxf(mx[2], fabsf(x[2])); mx[3] = fmaxf(mx[3], fabsf(x[3]));
;                 const unsigned p01 = cvt_pk_bf16(x[0], x[1]), p23 = cvt_pk_bf16(x[2], x[3]);
;                 const int ks = k ^ (((c4 >> 3) & 3) << 3);
;                 slab[(c4 + 0) * PITCH + ks] = (bf16)(p01 & 0xffffu); slab[(c4 + 1) * PITCH + ks] = (bf16)(p01 >> 16); slab[(c4 + 2) * PITCH + ks] = (bf16)(p23 & 0xffffu); slab[(c4 + 3) * PITCH + ks] = (bf16)(p23 >> 16); }
; #pragma unroll
;             for (int q = 0; q < 4; ++q) { float m = mx[q]; m = fmaxf(m, __shfl_xor(m, 8)); m = fmaxf(m, __shfl_xor(m, 16)); m = fmaxf(m, __shfl_xor(m, 32)); mx[q] = m; }
;             if (lane < 8) { LAS float* d = red + wave * 32 + c4; d[0] = mx[0]; d[1] = mx[1]; d[2] = mx[2]; d[3] = mx[3]; }
	v_cvt_pk_bf16_f32 v136, v88, v89
	v_cvt_pk_bf16_f32 v137, v90, v91
	v_max3_f32 v128, v128, |v24|, |v28|
	v_max3_f32 v130, v130, |v50|, |v54|
	ds_write_b16 v166, v136
	ds_write_b16_d16_hi v166, v136 offset:4112
	ds_write_b16 v166, v137 offset:8224
	ds_write_b16_d16_hi v166, v137 offset:12336
	s_waitcnt vmcnt(8)
	v_cvt_pk_bf16_f32 v136, v92, v93
	v_cvt_pk_bf16_f32 v137, v94, v95
	v_max3_f32 v129, |v1|, 0, |v5|
	v_max3_f32 v128, v128, |v32|, |v36|
	v_max3_f32 v130, v130, |v58|, |v62|
	ds_write_b16 v167, v136
	ds_write_b16_d16_hi v167, v136 offset:4112
	ds_write_b16 v167, v137 offset:8224
	ds_write_b16_d16_hi v167, v137 offset:12336
	s_waitcnt vmcnt(7)
	v_cvt_pk_bf16_f32 v136, v96, v97
	v_cvt_pk_bf16_f32 v137, v98, v99
	v_max3_f32 v129, v129, |v9|, |v13|
	v_max3_f32 v128, v128, |v40|, |v44|
	v_max3_f32 v130, v130, |v66|, |v70|
	ds_write_b16 v168, v136
	ds_write_b16_d16_hi v168, v136 offset:4112
	ds_write_b16 v168, v137 offset:8224
	ds_write_b16_d16_hi v168, v137 offset:12336
	s_waitcnt vmcnt(6)
	v_cvt_pk_bf16_f32 v136, v100, v101
	v_cvt_pk_bf16_f32 v137, v102, v103
	v_max3_f32 v129, v129, |v17|, |v21|
	v_max3_f32 v128, v128, |v48|, |v52|
	v_max3_f32 v130, v130, |v74|, |v78|
	ds_write_b16 v169, v136
	ds_write_b16_d16_hi v169, v136 offset:4112
	ds_write_b16 v169, v137 offset:8224
	ds_write_b16_d16_hi v169, v137 offset:12336
	s_waitcnt vmcnt(5)
	v_cvt_pk_bf16_f32 v136, v104, v105
	v_cvt_pk_bf16_f32 v137, v106, v107
	v_max3_f32 v129, v129, |v25|, |v29|
	v_max3_f32 v128, v128, |v56|, |v60|
	v_max3_f32 v130, v130, |v82|, |v86|
	ds_write_b16 v170, v136
	ds_write_b16_d16_hi v170, v136 offset:4112
	ds_write_b16 v170, v137 offset:8224
	ds_write_b16_d16_hi v170, v137 offset:12336
	s_waitcnt vmcnt(4)
	v_cvt_pk_bf16_f32 v136, v108, v109
	v_cvt_pk_bf16_f32 v137, v110, v111
	v_max3_f32 v129, v129, |v33|, |v37|
	v_max3_f32 v128, v128, |v64|, |v68|
	v_max3_f32 v130, v130, |v90|, |v94|
	ds_write_b16 v171, v136
	ds_write_b16_d16_hi v171, v136 offset:4112
	ds_write_b16 v171, v137 offset:8224
	ds_write_b16_d16_hi v171, v137 offset:12336
	s_waitcnt vmcnt(3)
	v_cvt_pk_bf16_f32 v136, v112, v113
	v_cvt_pk_bf16_f32 v137, v114, v115
	v_max3_f32 v129, v129, |v41|, |v45|
	v_max3_f32 v128, v128, |v72|, |v76|
	v_max3_f32 v130, v130, |v98|, |v102|
	ds_write_b16 v172, v136
	ds_write_b16_d16_hi v172, v136 offset:4112
	ds_write_b16 v172, v137 offset:8224
	ds_write_b16_d16_hi v172, v137 offset:12336
	s_waitcnt vmcnt(2)
	v_cvt_pk_bf16_f32 v136, v116, v117
	v_cvt_pk_bf16_f32 v137, v118, v119
	v_max3_f32 v129, v129, |v49|, |v53|
	v_max3_f32 v128, v128, |v80|, |v84|
	v_max3_f32 v130, v130, |v106|, |v110|
	ds_write_b16 v173, v136
	ds_write_b16_d16_hi v173, v136 offset:4112
	ds_write_b16 v173, v137 offset:8224
	ds_write_b16_d16_hi v173, v137 offset:12336
	s_waitcnt vmcnt(1)
	v_cvt_pk_bf16_f32 v136, v120, v121
	v_cvt_pk_bf16_f32 v137, v122, v123
	v_max3_f32 v129, v129, |v57|, |v61|
	v_max3_f32 v128, v128, |v88|, |v92|
	v_max3_f32 v130, v130, |v114|, |v118|
	ds_write_b16 v174, v136
	ds_write_b16_d16_hi v174, v136 offset:4112
	ds_write_b16 v174, v137 offset:8224
	ds_write_b16_d16_hi v174, v137 offset:12336
	v_and_b32_e32 v137, 64, v177
	v_max3_f32 v131, |v3|, 0, |v7|
	v_max3_f32 v129, v129, |v65|, |v69|
	v_max3_f32 v128, v128, |v96|, |v100|
	s_waitcnt vmcnt(0)
	v_max3_f32 v136, v130, |v122|, |v126|
	v_xor_b32_e32 v130, 8, v177
	v_add_u32_e32 v137, 64, v137
	v_max3_f32 v131, v131, |v11|, |v15|
	v_max3_f32 v129, v129, |v73|, |v77|
	v_max3_f32 v128, v128, |v104|, |v108|
	v_cmp_lt_i32_e32 vcc, v130, v137
	v_max3_f32 v131, v131, |v19|, |v23|
	v_max3_f32 v129, v129, |v81|, |v85|
	v_max3_f32 v128, v128, |v112|, |v116|
	v_cndmask_b32_e32 v130, v177, v130, vcc
	v_max3_f32 v131, v131, |v27|, |v31|
	v_max3_f32 v129, v129, |v89|, |v93|
	v_max3_f32 v128, v128, |v120|, |v124|
	v_lshlrev_b32_e32 v130, 2, v130
	v_max3_f32 v131, v131, |v35|, |v39|
	v_max3_f32 v129, v129, |v97|, |v101|
	ds_bpermute_b32 v139, v130, v128
	v_max3_f32 v131, v131, |v43|, |v47|
	v_max3_f32 v129, v129, |v105|, |v109|
	v_xor_b32_e32 v138, 16, v177
	v_max3_f32 v131, v131, |v51|, |v55|
	v_max3_f32 v129, v129, |v113|, |v117|
	v_cmp_lt_i32_e32 vcc, v138, v137
	v_xor_b32_e32 v182, 32, v177
	v_max3_f32 v131, v131, |v59|, |v63|
	v_max3_f32 v129, v129, |v121|, |v125|
	v_cndmask_b32_e32 v138, v177, v138, vcc
	v_cmp_lt_i32_e32 vcc, v182, v137
	v_max3_f32 v131, v131, |v67|, |v71|
	v_max3_f32 v131, v131, |v75|, |v79|
	v_cndmask_b32_e32 v137, v177, v182, vcc
	ds_bpermute_b32 v182, v130, v129
	s_waitcnt lgkmcnt(1)
	v_max_f32_e32 v139, v139, v139
	v_max3_f32 v131, v131, |v83|, |v87|
	v_lshlrev_b32_e32 v138, 2, v138
	v_max_f32_e32 v128, v128, v139
	v_max3_f32 v131, v131, |v91|, |v95|
	ds_bpermute_b32 v139, v138, v128
	v_max3_f32 v131, v131, |v99|, |v103|
	v_max3_f32 v131, v131, |v107|, |v111|
	v_lshlrev_b32_e32 v183, 2, v137
	s_waitcnt lgkmcnt(1)
	v_max_f32_e32 v137, v182, v182
	v_max3_f32 v131, v131, |v115|, |v119|
	v_max_f32_e32 v137, v129, v137
	v_max3_f32 v131, v131, |v123|, |v127|
	ds_bpermute_b32 v182, v138, v137
	s_waitcnt lgkmcnt(1)
	v_max_f32_e32 v129, v139, v139
	ds_bpermute_b32 v139, v130, v136
	ds_bpermute_b32 v184, v130, v131
	v_max_f32_e32 v128, v128, v129
	s_waitcnt lgkmcnt(2)
	v_max_f32_e32 v182, v182, v182
	v_max_f32_e32 v130, v137, v182
	s_waitcnt lgkmcnt(1)
	v_max_f32_e32 v137, v139, v139
	s_waitcnt lgkmcnt(0)
	v_max_f32_e32 v139, v184, v184
	v_max_f32_e32 v136, v136, v137
	v_max_f32_e32 v139, v131, v139
	ds_bpermute_b32 v137, v138, v136
	ds_bpermute_b32 v138, v138, v139
	ds_bpermute_b32 v129, v183, v128
	ds_bpermute_b32 v131, v183, v130
	v_cvt_pk_bf16_f32 v180, v124, v125
	s_waitcnt lgkmcnt(3)
	v_max_f32_e32 v137, v137, v137
	s_waitcnt lgkmcnt(2)
	v_max_f32_e32 v138, v138, v138
	v_max_f32_e32 v136, v136, v137
	v_max_f32_e32 v138, v139, v138
	ds_bpermute_b32 v137, v183, v136
	ds_bpermute_b32 v139, v183, v138
	v_cvt_pk_bf16_f32 v181, v126, v127
	ds_write_b16 v175, v180
	ds_write_b16_d16_hi v175, v180 offset:4112
	ds_write_b16 v175, v181 offset:8224
	ds_write_b16_d16_hi v175, v181 offset:12336
	s_and_saveexec_b64 s[40:41], s[4:5]
	s_cbranch_execz .LBB0_651
	s_waitcnt lgkmcnt(4)
	v_max_f32_e32 v139, v139, v139
	v_max_f32_e32 v138, v138, v138
	v_max_f32_e32 v137, v137, v137
	v_max_f32_e32 v136, v136, v136
	v_max_f32_e32 v131, v131, v131
	v_max_f32_e32 v130, v130, v130
	v_max_f32_e32 v129, v129, v129
	v_max_f32_e32 v128, v128, v128
	v_max_f32_e32 v139, v138, v139
	v_max_f32_e32 v138, v136, v137
	v_max_f32_e32 v137, v130, v131
	v_max_f32_e32 v136, v128, v129
	ds_write_b128 v176, v[136:139]

; __device__ __forceinline__ unsigned cvt_pk_bf16(float lo, float hi) { unsigned r; asm volatile("v_cvt_pk_bf16_f32 %0, %1, %2" : "=v"(r) : "v"(lo), "v"(hi)); return r; }
; __device__ __forceinline__ void do_slabs_impl(LAS unsigned char* lds, unsigned char* ws, const float* w_up, const float* w_dn, const float* w_in, int vcu, int G, int wave, int j0, int j1) {
;     ...
;         if (cur.valid) {
;             f32x4 mx = (f32x4){0.f, 0.f, 0.f, 0.f};
; #pragma unroll
;             for (int i = 0; i < 32; ++i) { const int k = wave * 256 + i * 8 + kq; const f32x4 x = v[i];
;                 mx[0] = fmaxf(mx[0], fabsf(x[0])); mx[1] = fmaxf(mx[1], fabsf(x[1])); mx[2] = fmaxf(mx[2], fabsf(x[2])); mx[3] = fmaxf(mx[3], fabsf(x[3]));
;                 const unsigned p01 = cvt_pk_bf16(x[0], x[1]), p23 = cvt_pk_bf16(x[2], x[3]);
;                 const int ks = k ^ (((c4 >> 3) & 3) << 3);
;                 slab[(c4 + 0) * PITCH + ks] = (bf16)(p01 & 0xffffu); slab[(c4 + 1) * PITCH + ks] = (bf16)(p01 >> 16); slab[(c4 + 2) * PITCH + ks] = (bf16)(p23 & 0xffffu); slab[(c4 + 3) * PITCH + ks] = (bf16)(p23 >> 16); }
.LBB0_683:
	s_cmp_lg_u32 s24, 0
	s_cselect_b64 s[36:37], -1, 0
	s_cmp_eq_u32 s24, 0
	s_cbranch_scc1 .LBB0_687
	s_waitcnt vmcnt(31)
	v_cvt_pk_bf16_f32 v128, v0, v1
	v_cvt_pk_bf16_f32 v129, v2, v3
	ds_write_b16 v144, v128
	ds_write_b16_d16_hi v144, v128 offset:4112
	ds_write_b16 v144, v129 offset:8224
	ds_write_b16_d16_hi v144, v129 offset:12336
	s_waitcnt vmcnt(30)
	v_cvt_pk_bf16_f32 v136, v4, v5
	v_cvt_pk_bf16_f32 v137, v6, v7
	ds_write_b16 v145, v136
	ds_write_b16_d16_hi v145, v136 offset:4112
	ds_write_b16 v145, v137 offset:8224
	ds_write_b16_d16_hi v145, v137 offset:12336
	s_waitcnt vmcnt(29)
	v_cvt_pk_bf16_f32 v136, v8, v9
	v_cvt_pk_bf16_f32 v137, v10, v11
	ds_write_b16 v146, v136
	ds_write_b16_d16_hi v146, v136 offset:4112
	ds_write_b16 v146, v137 offset:8224
	ds_write_b16_d16_hi v146, v137 offset:12336
	s_waitcnt vmcnt(28)
	v_cvt_pk_bf16_f32 v136, v12, v13
	v_cvt_pk_bf16_f32 v137, v14, v15
	ds_write_b16 v147, v136
	ds_write_b16_d16_hi v147, v136 offset:4112
	ds_write_b16 v147, v137 offset:8224
	ds_write_b16_d16_hi v147, v137 offset:12336
	s_waitcnt vmcnt(27)
	v_cvt_pk_bf16_f32 v136, v16, v17
	v_cvt_pk_bf16_f32 v137, v18, v19
	ds_write_b16 v148, v136
	ds_write_b16_d16_hi v148, v136 offset:4112
	ds_write_b16 v148, v137 offset:8224
	ds_write_b16_d16_hi v148, v137 offset:12336
	s_waitcnt vmcnt(26)
	v_cvt_pk_bf16_f32 v136, v20, v21
	v_cvt_pk_bf16_f32 v137, v22, v23
	ds_write_b16 v149, v136
	ds_write_b16_d16_hi v149, v136 offset:4112
	ds_write_b16 v149, v137 offset:8224
	ds_write_b16_d16_hi v149, v137 offset:12336
	s_waitcnt vmcnt(25)
	v_cvt_pk_bf16_f32 v136, v24, v25
	v_cvt_pk_bf16_f32 v137, v26, v27
	ds_write_b16 v150, v136
	ds_write_b16_d16_hi v150, v136 offset:4112
	ds_write_b16 v150, v137 offset:8224
	ds_write_b16_d16_hi v150, v137 offset:12336
	s_waitcnt vmcnt(24)
	v_cvt_pk_bf16_f32 v136, v28, v29
	v_cvt_pk_bf16_f32 v137, v30, v31
	ds_write_b16 v151, v136
	ds_write_b16_d16_hi v151, v136 offset:4112
	ds_write_b16 v151, v137 offset:8224
	ds_write_b16_d16_hi v151, v137 offset:12336
	s_waitcnt vmcnt(23)
	v_cvt_pk_bf16_f32 v136, v32, v33
	v_cvt_pk_bf16_f32 v137, v34, v35
	ds_write_b16 v152, v136
	ds_write_b16_d16_hi v152, v136 offset:4112
	ds_write_b16 v152, v137 offset:8224
	ds_write_b16_d16_hi v152, v137 offset:12336
	s_waitcnt vmcnt(22)
	v_cvt_pk_bf16_f32 v136, v36, v37
	v_cvt_pk_bf16_f32 v137, v38, v39
	ds_write_b16 v153, v136
	ds_write_b16_d16_hi v153, v136 offset:4112
	ds_write_b16 v153, v137 offset:8224
	ds_write_b16_d16_hi v153, v137 offset:12336
	s_waitcnt vmcnt(21)
	v_cvt_pk_bf16_f32 v136, v40, v41
	v_cvt_pk_bf16_f32 v137, v42, v43
	ds_write_b16 v154, v136
	ds_write_b16_d16_hi v154, v136 offset:4112
	ds_write_b16 v154, v137 offset:8224
	ds_write_b16_d16_hi v154, v137 offset:12336
	s_waitcnt vmcnt(20)
	v_cvt_pk_bf16_f32 v136, v44, v45
	v_cvt_pk_bf16_f32 v137, v46, v47
	ds_write_b16 v155, v136
	ds_write_b16_d16_hi v155, v136 offset:4112
	ds_write_b16 v155, v137 offset:8224
	ds_write_b16_d16_hi v155, v137 offset:12336
	s_waitcnt vmcnt(19)
	v_cvt_pk_bf16_f32 v136, v48, v49
	v_cvt_pk_bf16_f32 v137, v50, v51
	ds_write_b16 v156, v136
	ds_write_b16_d16_hi v156, v136 offset:4112
	ds_write_b16 v156, v137 offset:8224
	ds_write_b16_d16_hi v156, v137 offset:12336
	s_waitcnt vmcnt(18)
	v_cvt_pk_bf16_f32 v136, v52, v53
	v_cvt_pk_bf16_f32 v137, v54, v55
	ds_write_b16 v157, v136
	ds_write_b16_d16_hi v157, v136 offset:4112
	ds_write_b16 v157, v137 offset:8224
	ds_write_b16_d16_hi v157, v137 offset:12336
	s_waitcnt vmcnt(17)
	v_cvt_pk_bf16_f32 v136, v56, v57
	v_cvt_pk_bf16_f32 v137, v58, v59
	ds_write_b16 v158, v136
	ds_write_b16_d16_hi v158, v136 offset:4112
	ds_write_b16 v158, v137 offset:8224
	ds_write_b16_d16_hi v158, v137 offset:12336
	s_waitcnt vmcnt(16)
	v_cvt_pk_bf16_f32 v136, v60, v61
	v_cvt_pk_bf16_f32 v137, v62, v63
	ds_write_b16 v159, v136
	ds_write_b16_d16_hi v159, v136 offset:4112
	ds_write_b16 v159, v137 offset:8224
	ds_write_b16_d16_hi v159, v137 offset:12336
	s_waitcnt vmcnt(15)
	v_cvt_pk_bf16_f32 v136, v64, v65
	v_cvt_pk_bf16_f32 v137, v66, v67
	v_max3_f32 v130, |v2|, 0, |v6|
	ds_write_b16 v160, v136
	ds_write_b16_d16_hi v160, v136 offset:4112
	ds_write_b16 v160, v137 offset:8224
	ds_write_b16_d16_hi v160, v137 offset:12336
	s_waitcnt vmcnt(14)
	v_cvt_pk_bf16_f32 v136, v68, v69
	v_cvt_pk_bf16_f32 v137, v70, v71
	v_max3_f32 v130, v130, |v10|, |v14|
	ds_write_b16 v161, v136
	ds_write_b16_d16_hi v161, v136 offset:4112
	ds_write_b16 v161, v137 offset:8224
	ds_write_b16_d16_hi v161, v137 offset:12336
	s_waitcnt vmcnt(13)
	v_cvt_pk_bf16_f32 v136, v72, v73
	v_cvt_pk_bf16_f32 v137, v74, v75
	v_max3_f32 v130, v130, |v18|, |v22|
	ds_write_b16 v162, v136
	ds_write_b16_d16_hi v162, v136 offset:4112
	ds_write_b16 v162, v137 offset:8224
	ds_write_b16_d16_hi v162, v137 offset:12336
	s_waitcnt vmcnt(12)
	v_cvt_pk_bf16_f32 v136, v76, v77
	v_cvt_pk_bf16_f32 v137, v78, v79
	v_max3_f32 v128, |v0|, 0, |v4|
	v_max3_f32 v130, v130, |v26|, |v30|
	ds_write_b16 v163, v136
	ds_write_b16_d16_hi v163, v136 offset:4112
	ds_write_b16 v163, v137 offset:8224
	ds_write_b16_d16_hi v163, v137 offset:12336
	s_waitcnt vmcnt(11)
	v_cvt_pk_bf16_f32 v136, v80, v81
	v_cvt_pk_bf16_f32 v137, v82, v83
	v_max3_f32 v128, v128, |v8|, |v12|
	v_max3_f32 v130, v130, |v34|, |v38|
	ds_write_b16 v164, v136
	ds_write_b16_d16_hi v164, v136 offset:4112
	ds_write_b16 v164, v137 offset:8224
	ds_write_b16_d16_hi v164, v137 offset:12336
	s_waitcnt vmcnt(10)
	v_cvt_pk_bf16_f32 v136, v84, v85
	v_cvt_pk_bf16_f32 v137, v86, v87
	v_max3_f32 v128, v128, |v16|, |v20|
	v_max3_f32 v130, v130, |v42|, |v46|
	ds_write_b16 v165, v136
	ds_write_b16_d16_hi v165, v136 offset:4112
	ds_write_b16 v165, v137 offset:8224
	ds_write_b16_d16_hi v165, v137 offset:12336
	s_waitcnt vmcnt(9)
; #define LAS __attribute__((address_space(3)))
; __device__ __forceinline__ unsigned cvt_pk_bf16(float lo, float hi) { unsigned r; asm volatile("v_cvt_pk_bf16_f32 %0, %1, %2" : "=v"(r) : "v"(lo), "v"(hi)); return r; }
; __device__ __forceinline__ void do_slabs_impl(LAS unsigned char* lds, unsigned char* ws, const float* w_up, const float* w_dn, const float* w_in, int vcu, int G, int wave, int j0, int j1) {
;     ...
;             for (int i = 0; i < 32; ++i) { const int k = wave * 256 + i * 8 + kq; const f32x4 x = v[i];
;                 mx[0] = fmaxf(mx[0], fabsf(x[0])); mx[1] = fmaxf(mx[1], fabsf(x[1])); mx[2] = fmaxf(mx[2], fabsf(x[2])); mx[3] = fmaxf(mx[3], fabsf(x[3]));
;                 const unsigned p01 = cvt_pk_bf16(x[0], x[1]), p23 = cvt_pk_bf16(x[2], x[3]);
;                 const int ks = k ^ (((c4 >> 3) & 3) << 3);
;                 slab[(c4 + 0) * PITCH + ks] = (bf16)(p01 & 0xffffu); slab[(c4 + 1) * PITCH + ks] = (bf16)(p01 >> 16); slab[(c4 + 2) * PITCH + ks] = (bf16)(p23 & 0xffffu); slab[(c4 + 3) * PITCH + ks] = (bf16)(p23 >> 16); }
; #pragma unroll
;             for (int q = 0; q < 4; ++q) { float m = mx[q]; m = fmaxf(m, __shfl_xor(m, 8)); m = fmaxf(m, __shfl_xor(m, 16)); m = fmaxf(m, __shfl_xor(m, 32)); mx[q] = m; }
;             if (lane < 8) { LAS float* d = red + wave * 32 + c4; d[0] = mx[0]; d[1] = mx[1]; d[2] = mx[2]; d[3] = mx[3]; }
	v_cvt_pk_bf16_f32 v136, v88, v89
	v_cvt_pk_bf16_f32 v137, v90, v91
	v_max3_f32 v128, v128, |v24|, |v28|
	v_max3_f32 v130, v130, |v50|, |v54|
	ds_write_b16 v166, v136
	ds_write_b16_d16_hi v166, v136 offset:4112
	ds_write_b16 v166, v137 offset:8224
	ds_write_b16_d16_hi v166, v137 offset:12336
	s_waitcnt vmcnt(8)
	v_cvt_pk_bf16_f32 v136, v92, v93
	v_cvt_pk_bf16_f32 v137, v94, v95
	v_max3_f32 v129, |v1|, 0, |v5|
	v_max3_f32 v128, v128, |v32|, |v36|
	v_max3_f32 v130, v130, |v58|, |v62|
	ds_write_b16 v167, v136
	ds_write_b16_d16_hi v167, v136 offset:4112
	ds_write_b16 v167, v137 offset:8224
	ds_write_b16_d16_hi v167, v137 offset:12336
	s_waitcnt vmcnt(7)
	v_cvt_pk_bf16_f32 v136, v96, v97
	v_cvt_pk_bf16_f32 v137, v98, v99
	v_max3_f32 v129, v129, |v9|, |v13|
	v_max3_f32 v128, v128, |v40|, |v44|
	v_max3_f32 v130, v130, |v66|, |v70|
	ds_write_b16 v168, v136
	ds_write_b16_d16_hi v168, v136 offset:4112
	ds_write_b16 v168, v137 offset:8224
	ds_write_b16_d16_hi v168, v137 offset:12336
	s_waitcnt vmcnt(6)
	v_cvt_pk_bf16_f32 v136, v100, v101
	v_cvt_pk_bf16_f32 v137, v102, v103
	v_max3_f32 v129, v129, |v17|, |v21|
	v_max3_f32 v128, v128, |v48|, |v52|
	v_max3_f32 v130, v130, |v74|, |v78|
	ds_write_b16 v169, v136
	ds_write_b16_d16_hi v169, v136 offset:4112
	ds_write_b16 v169, v137 offset:8224
	ds_write_b16_d16_hi v169, v137 offset:12336
	s_waitcnt vmcnt(5)
	v_cvt_pk_bf16_f32 v136, v104, v105
	v_cvt_pk_bf16_f32 v137, v106, v107
	v_max3_f32 v129, v129, |v25|, |v29|
	v_max3_f32 v128, v128, |v56|, |v60|
	v_max3_f32 v130, v130, |v82|, |v86|
	ds_write_b16 v170, v136
	ds_write_b16_d16_hi v170, v136 offset:4112
	ds_write_b16 v170, v137 offset:8224
	ds_write_b16_d16_hi v170, v137 offset:12336
	s_waitcnt vmcnt(4)
	v_cvt_pk_bf16_f32 v136, v108, v109
	v_cvt_pk_bf16_f32 v137, v110, v111
	v_max3_f32 v129, v129, |v33|, |v37|
	v_max3_f32 v128, v128, |v64|, |v68|
	v_max3_f32 v130, v130, |v90|, |v94|
	ds_write_b16 v171, v136
	ds_write_b16_d16_hi v171, v136 offset:4112
	ds_write_b16 v171, v137 offset:8224
	ds_write_b16_d16_hi v171, v137 offset:12336
	s_waitcnt vmcnt(3)
	v_cvt_pk_bf16_f32 v136, v112, v113
	v_cvt_pk_bf16_f32 v137, v114, v115
	v_max3_f32 v129, v129, |v41|, |v45|
	v_max3_f32 v128, v128, |v72|, |v76|
	v_max3_f32 v130, v130, |v98|, |v102|
	ds_write_b16 v172, v136
	ds_write_b16_d16_hi v172, v136 offset:4112
	ds_write_b16 v172, v137 offset:8224
	ds_write_b16_d16_hi v172, v137 offset:12336
	s_waitcnt vmcnt(2)
	v_cvt_pk_bf16_f32 v136, v116, v117
	v_cvt_pk_bf16_f32 v137, v118, v119
	v_max3_f32 v129, v129, |v49|, |v53|
	v_max3_f32 v128, v128, |v80|, |v84|
	v_max3_f32 v130, v130, |v106|, |v110|
	ds_write_b16 v173, v136
	ds_write_b16_d16_hi v173, v136 offset:4112
	ds_write_b16 v173, v137 offset:8224
	ds_write_b16_d16_hi v173, v137 offset:12336
	s_waitcnt vmcnt(1)
	v_cvt_pk_bf16_f32 v136, v120, v121
	v_cvt_pk_bf16_f32 v137, v122, v123
	v_max3_f32 v129, v129, |v57|, |v61|
	v_max3_f32 v128, v128, |v88|, |v92|
	v_max3_f32 v130, v130, |v114|, |v118|
	ds_write_b16 v174, v136
	ds_write_b16_d16_hi v174, v136 offset:4112
	ds_write_b16 v174, v137 offset:8224
	ds_write_b16_d16_hi v174, v137 offset:12336
	v_and_b32_e32 v137, 64, v177
	v_max3_f32 v131, |v3|, 0, |v7|
	v_max3_f32 v129, v129, |v65|, |v69|
	v_max3_f32 v128, v128, |v96|, |v100|
	s_waitcnt vmcnt(0)
	v_max3_f32 v136, v130, |v122|, |v126|
	v_xor_b32_e32 v130, 8, v177
	v_add_u32_e32 v137, 64, v137
	v_max3_f32 v131, v131, |v11|, |v15|
	v_max3_f32 v129, v129, |v73|, |v77|
	v_max3_f32 v128, v128, |v104|, |v108|
	v_cmp_lt_i32_e32 vcc, v130, v137
	v_max3_f32 v131, v131, |v19|, |v23|
	v_max3_f32 v129, v129, |v81|, |v85|
	v_max3_f32 v128, v128, |v112|, |v116|
	v_cndmask_b32_e32 v130, v177, v130, vcc
	v_max3_f32 v131, v131, |v27|, |v31|
	v_max3_f32 v129, v129, |v89|, |v93|
	v_max3_f32 v128, v128, |v120|, |v124|
	v_lshlrev_b32_e32 v130, 2, v130
	v_max3_f32 v131, v131, |v35|, |v39|
	v_max3_f32 v129, v129, |v97|, |v101|
	ds_bpermute_b32 v139, v130, v128
	v_max3_f32 v131, v131, |v43|, |v47|
	v_max3_f32 v129, v129, |v105|, |v109|
	v_xor_b32_e32 v138, 16, v177
	v_max3_f32 v131, v131, |v51|, |v55|
	v_max3_f32 v129, v129, |v113|, |v117|
	v_cmp_lt_i32_e32 vcc, v138, v137
	v_xor_b32_e32 v182, 32, v177
	v_max3_f32 v131, v131, |v59|, |v63|
	v_max3_f32 v129, v129, |v121|, |v125|
	v_cndmask_b32_e32 v138, v177, v138, vcc
	v_cmp_lt_i32_e32 vcc, v182, v137
	v_max3_f32 v131, v131, |v67|, |v71|
	v_max3_f32 v131, v131, |v75|, |v79|
	v_cndmask_b32_e32 v137, v177, v182, vcc
	ds_bpermute_b32 v182, v130, v129
	s_waitcnt lgkmcnt(1)
	v_max_f32_e32 v139, v139, v139
	v_max3_f32 v131, v131, |v83|, |v87|
	v_lshlrev_b32_e32 v138, 2, v138
	v_max_f32_e32 v128, v128, v139
	v_max3_f32 v131, v131, |v91|, |v95|
	ds_bpermute_b32 v139, v138, v128
	v_max3_f32 v131, v131, |v99|, |v103|
	v_max3_f32 v131, v131, |v107|, |v111|
	v_lshlrev_b32_e32 v183, 2, v137
	s_waitcnt lgkmcnt(1)
	v_max_f32_e32 v137, v182, v182
	v_max3_f32 v131, v131, |v115|, |v119|
	v_max_f32_e32 v137, v129, v137
	v_max3_f32 v131, v131, |v123|, |v127|
	ds_bpermute_b32 v182, v138, v137
	s_waitcnt lgkmcnt(1)
	v_max_f32_e32 v129, v139, v139
	ds_bpermute_b32 v139, v130, v136
	ds_bpermute_b32 v184, v130, v131
	v_max_f32_e32 v128, v128, v129
	s_waitcnt lgkmcnt(2)
	v_max_f32_e32 v182, v182, v182
	v_max_f32_e32 v130, v137, v182
	s_waitcnt lgkmcnt(1)
	v_max_f32_e32 v137, v139, v139
	s_waitcnt lgkmcnt(0)
	v_max_f32_e32 v139, v184, v184
	v_max_f32_e32 v136, v136, v137
	v_max_f32_e32 v139, v131, v139
	ds_bpermute_b32 v137, v138, v136
	ds_bpermute_b32 v138, v138, v139
	ds_bpermute_b32 v129, v183, v128
	ds_bpermute_b32 v131, v183, v130
	v_cvt_pk_bf16_f32 v180, v124, v125
	s_waitcnt lgkmcnt(3)
	v_max_f32_e32 v137, v137, v137
	s_waitcnt lgkmcnt(2)
	v_max_f32_e32 v138, v138, v138
	v_max_f32_e32 v136, v136, v137
	v_max_f32_e32 v138, v139, v138
	ds_bpermute_b32 v137, v183, v136
	ds_bpermute_b32 v139, v183, v138
	v_cvt_pk_bf16_f32 v181, v126, v127
	ds_write_b16 v175, v180
	ds_write_b16_d16_hi v175, v180 offset:4112
	ds_write_b16 v175, v181 offset:8224
	ds_write_b16_d16_hi v175, v181 offset:12336
	s_and_saveexec_b64 s[38:39], s[4:5]
	s_cbranch_execz .LBB0_686
	s_waitcnt lgkmcnt(4)
	v_max_f32_e32 v139, v139, v139
	v_max_f32_e32 v138, v138, v138
	v_max_f32_e32 v137, v137, v137
	v_max_f32_e32 v136, v136, v136
	v_max_f32_e32 v131, v131, v131
	v_max_f32_e32 v130, v130, v130
	v_max_f32_e32 v129, v129, v129
	v_max_f32_e32 v128, v128, v128
	v_max_f32_e32 v139, v138, v139
	v_max_f32_e32 v138, v136, v137
	v_max_f32_e32 v137, v130, v131
	v_max_f32_e32 v136, v128, v129
	ds_write_b128 v176, v[136:139]

; __device__ __forceinline__ unsigned cvt_pk_bf16(float lo, float hi) { unsigned r; asm volatile("v_cvt_pk_bf16_f32 %0, %1, %2" : "=v"(r) : "v"(lo), "v"(hi)); return r; }
; __device__ __forceinline__ void do_slabs_impl(LAS unsigned char* lds, unsigned char* ws, const float* w_up, const float* w_dn, const float* w_in, int vcu, int G, int wave, int j0, int j1) {
;     ...
;         if (cur.valid) {
;             f32x4 mx = (f32x4){0.f, 0.f, 0.f, 0.f};
; #pragma unroll
;             for (int i = 0; i < 32; ++i) { const int k = wave * 256 + i * 8 + kq; const f32x4 x = v[i];
;                 mx[0] = fmaxf(mx[0], fabsf(x[0])); mx[1] = fmaxf(mx[1], fabsf(x[1])); mx[2] = fmaxf(mx[2], fabsf(x[2])); mx[3] = fmaxf(mx[3], fabsf(x[3]));
;                 const unsigned p01 = cvt_pk_bf16(x[0], x[1]), p23 = cvt_pk_bf16(x[2], x[3]);
;                 const int ks = k ^ (((c4 >> 3) & 3) << 3);
;                 slab[(c4 + 0) * PITCH + ks] = (bf16)(p01 & 0xffffu); slab[(c4 + 1) * PITCH + ks] = (bf16)(p01 >> 16); slab[(c4 + 2) * PITCH + ks] = (bf16)(p23 & 0xffffu); slab[(c4 + 3) * PITCH + ks] = (bf16)(p23 >> 16); }
.LBB0_1105:
	s_cmp_lg_u32 s33, 0
	s_cselect_b64 s[40:41], -1, 0
	s_cmp_eq_u32 s33, 0
	s_cbranch_scc1 .LBB0_1109
	s_waitcnt vmcnt(31)
	v_cvt_pk_bf16_f32 v128, v0, v1
	v_cvt_pk_bf16_f32 v129, v2, v3
	ds_write_b16 v144, v128
	ds_write_b16_d16_hi v144, v128 offset:4112
	ds_write_b16 v144, v129 offset:8224
	ds_write_b16_d16_hi v144, v129 offset:12336
	s_waitcnt vmcnt(30)
	v_cvt_pk_bf16_f32 v136, v4, v5
	v_cvt_pk_bf16_f32 v137, v6, v7
	ds_write_b16 v145, v136
	ds_write_b16_d16_hi v145, v136 offset:4112
	ds_write_b16 v145, v137 offset:8224
	ds_write_b16_d16_hi v145, v137 offset:12336
	s_waitcnt vmcnt(29)
	v_cvt_pk_bf16_f32 v136, v8, v9
	v_cvt_pk_bf16_f32 v137, v10, v11
	ds_write_b16 v146, v136
	ds_write_b16_d16_hi v146, v136 offset:4112
	ds_write_b16 v146, v137 offset:8224
	ds_write_b16_d16_hi v146, v137 offset:12336
	s_waitcnt vmcnt(28)
	v_cvt_pk_bf16_f32 v136, v12, v13
	v_cvt_pk_bf16_f32 v137, v14, v15
	ds_write_b16 v147, v136
	ds_write_b16_d16_hi v147, v136 offset:4112
	ds_write_b16 v147, v137 offset:8224
	ds_write_b16_d16_hi v147, v137 offset:12336
	s_waitcnt vmcnt(27)
	v_cvt_pk_bf16_f32 v136, v16, v17
	v_cvt_pk_bf16_f32 v137, v18, v19
	ds_write_b16 v148, v136
	ds_write_b16_d16_hi v148, v136 offset:4112
	ds_write_b16 v148, v137 offset:8224
	ds_write_b16_d16_hi v148, v137 offset:12336
	s_waitcnt vmcnt(26)
	v_cvt_pk_bf16_f32 v136, v20, v21
	v_cvt_pk_bf16_f32 v137, v22, v23
	ds_write_b16 v149, v136
	ds_write_b16_d16_hi v149, v136 offset:4112
	ds_write_b16 v149, v137 offset:8224
	ds_write_b16_d16_hi v149, v137 offset:12336
	s_waitcnt vmcnt(25)
	v_cvt_pk_bf16_f32 v136, v24, v25
	v_cvt_pk_bf16_f32 v137, v26, v27
	ds_write_b16 v150, v136
	ds_write_b16_d16_hi v150, v136 offset:4112
	ds_write_b16 v150, v137 offset:8224
	ds_write_b16_d16_hi v150, v137 offset:12336
	s_waitcnt vmcnt(24)
	v_cvt_pk_bf16_f32 v136, v28, v29
	v_cvt_pk_bf16_f32 v137, v30, v31
	ds_write_b16 v151, v136
	ds_write_b16_d16_hi v151, v136 offset:4112
	ds_write_b16 v151, v137 offset:8224
	ds_write_b16_d16_hi v151, v137 offset:12336
	s_waitcnt vmcnt(23)
	v_cvt_pk_bf16_f32 v136, v32, v33
	v_cvt_pk_bf16_f32 v137, v34, v35
	ds_write_b16 v152, v136
	ds_write_b16_d16_hi v152, v136 offset:4112
	ds_write_b16 v152, v137 offset:8224
	ds_write_b16_d16_hi v152, v137 offset:12336
	s_waitcnt vmcnt(22)
	v_cvt_pk_bf16_f32 v136, v36, v37
	v_cvt_pk_bf16_f32 v137, v38, v39
	ds_write_b16 v153, v136
	ds_write_b16_d16_hi v153, v136 offset:4112
	ds_write_b16 v153, v137 offset:8224
	ds_write_b16_d16_hi v153, v137 offset:12336
	s_waitcnt vmcnt(21)
	v_cvt_pk_bf16_f32 v136, v40, v41
	v_cvt_pk_bf16_f32 v137, v42, v43
	ds_write_b16 v154, v136
	ds_write_b16_d16_hi v154, v136 offset:4112
	ds_write_b16 v154, v137 offset:8224
	ds_write_b16_d16_hi v154, v137 offset:12336
	s_waitcnt vmcnt(20)
	v_cvt_pk_bf16_f32 v136, v44, v45
	v_cvt_pk_bf16_f32 v137, v46, v47
	ds_write_b16 v155, v136
	ds_write_b16_d16_hi v155, v136 offset:4112
	ds_write_b16 v155, v137 offset:8224
	ds_write_b16_d16_hi v155, v137 offset:12336
	s_waitcnt vmcnt(19)
	v_cvt_pk_bf16_f32 v136, v48, v49
	v_cvt_pk_bf16_f32 v137, v50, v51
	ds_write_b16 v156, v136
	ds_write_b16_d16_hi v156, v136 offset:4112
	ds_write_b16 v156, v137 offset:8224
	ds_write_b16_d16_hi v156, v137 offset:12336
	s_waitcnt vmcnt(18)
	v_cvt_pk_bf16_f32 v136, v52, v53
	v_cvt_pk_bf16_f32 v137, v54, v55
	ds_write_b16 v157, v136
	ds_write_b16_d16_hi v157, v136 offset:4112
	ds_write_b16 v157, v137 offset:8224
	ds_write_b16_d16_hi v157, v137 offset:12336
	s_waitcnt vmcnt(17)
	v_cvt_pk_bf16_f32 v136, v56, v57
	v_cvt_pk_bf16_f32 v137, v58, v59
	ds_write_b16 v158, v136
	ds_write_b16_d16_hi v158, v136 offset:4112
	ds_write_b16 v158, v137 offset:8224
	ds_write_b16_d16_hi v158, v137 offset:12336
	s_waitcnt vmcnt(16)
	v_cvt_pk_bf16_f32 v136, v60, v61
	v_cvt_pk_bf16_f32 v137, v62, v63
	ds_write_b16 v159, v136
	ds_write_b16_d16_hi v159, v136 offset:4112
	ds_write_b16 v159, v137 offset:8224
	ds_write_b16_d16_hi v159, v137 offset:12336
	s_waitcnt vmcnt(15)
	v_cvt_pk_bf16_f32 v136, v64, v65
	v_cvt_pk_bf16_f32 v137, v66, v67
	v_max3_f32 v130, |v2|, 0, |v6|
	ds_write_b16 v160, v136
	ds_write_b16_d16_hi v160, v136 offset:4112
	ds_write_b16 v160, v137 offset:8224
	ds_write_b16_d16_hi v160, v137 offset:12336
	s_waitcnt vmcnt(14)
	v_cvt_pk_bf16_f32 v136, v68, v69
	v_cvt_pk_bf16_f32 v137, v70, v71
	v_max3_f32 v130, v130, |v10|, |v14|
	ds_write_b16 v161, v136
	ds_write_b16_d16_hi v161, v136 offset:4112
	ds_write_b16 v161, v137 offset:8224
	ds_write_b16_d16_hi v161, v137 offset:12336
	s_waitcnt vmcnt(13)
	v_cvt_pk_bf16_f32 v136, v72, v73
	v_cvt_pk_bf16_f32 v137, v74, v75
	v_max3_f32 v130, v130, |v18|, |v22|
	ds_write_b16 v162, v136
	ds_write_b16_d16_hi v162, v136 offset:4112
	ds_write_b16 v162, v137 offset:8224
	ds_write_b16_d16_hi v162, v137 offset:12336
	s_waitcnt vmcnt(12)
	v_cvt_pk_bf16_f32 v136, v76, v77
	v_cvt_pk_bf16_f32 v137, v78, v79
	v_max3_f32 v128, |v0|, 0, |v4|
	v_max3_f32 v130, v130, |v26|, |v30|
	ds_write_b16 v163, v136
	ds_write_b16_d16_hi v163, v136 offset:4112
	ds_write_b16 v163, v137 offset:8224
	ds_write_b16_d16_hi v163, v137 offset:12336
	s_waitcnt vmcnt(11)
	v_cvt_pk_bf16_f32 v136, v80, v81
	v_cvt_pk_bf16_f32 v137, v82, v83
	v_max3_f32 v128, v128, |v8|, |v12|
	v_max3_f32 v130, v130, |v34|, |v38|
	ds_write_b16 v164, v136
	ds_write_b16_d16_hi v164, v136 offset:4112
	ds_write_b16 v164, v137 offset:8224
	ds_write_b16_d16_hi v164, v137 offset:12336
	s_waitcnt vmcnt(10)
	v_cvt_pk_bf16_f32 v136, v84, v85
	v_cvt_pk_bf16_f32 v137, v86, v87
	v_max3_f32 v128, v128, |v16|, |v20|
	v_max3_f32 v130, v130, |v42|, |v46|
	ds_write_b16 v165, v136
	ds_write_b16_d16_hi v165, v136 offset:4112
	ds_write_b16 v165, v137 offset:8224
	ds_write_b16_d16_hi v165, v137 offset:12336
	s_waitcnt vmcnt(9)
; #define LAS __attribute__((address_space(3)))
; __device__ __forceinline__ unsigned cvt_pk_bf16(float lo, float hi) { unsigned r; asm volatile("v_cvt_pk_bf16_f32 %0, %1, %2" : "=v"(r) : "v"(lo), "v"(hi)); return r; }
; __device__ __forceinline__ void do_slabs_impl(LAS unsigned char* lds, unsigned char* ws, const float* w_up, const float* w_dn, const float* w_in, int vcu, int G, int wave, int j0, int j1) {
;     ...
;             for (int i = 0; i < 32; ++i) { const int k = wave * 256 + i * 8 + kq; const f32x4 x = v[i];
;                 mx[0] = fmaxf(mx[0], fabsf(x[0])); mx[1] = fmaxf(mx[1], fabsf(x[1])); mx[2] = fmaxf(mx[2], fabsf(x[2])); mx[3] = fmaxf(mx[3], fabsf(x[3]));
;                 const unsigned p01 = cvt_pk_bf16(x[0], x[1]), p23 = cvt_pk_bf16(x[2], x[3]);
;                 const int ks = k ^ (((c4 >> 3) & 3) << 3);
;                 slab[(c4 + 0) * PITCH + ks] = (bf16)(p01 & 0xffffu); slab[(c4 + 1) * PITCH + ks] = (bf16)(p01 >> 16); slab[(c4 + 2) * PITCH + ks] = (bf16)(p23 & 0xffffu); slab[(c4 + 3) * PITCH + ks] = (bf16)(p23 >> 16); }
; #pragma unroll
;             for (int q = 0; q < 4; ++q) { float m = mx[q]; m = fmaxf(m, __shfl_xor(m, 8)); m = fmaxf(m, __shfl_xor(m, 16)); m = fmaxf(m, __shfl_xor(m, 32)); mx[q] = m; }
;             if (lane < 8) { LAS float* d = red + wave * 32 + c4; d[0] = mx[0]; d[1] = mx[1]; d[2] = mx[2]; d[3] = mx[3]; }
	v_cvt_pk_bf16_f32 v136, v88, v89
	v_cvt_pk_bf16_f32 v137, v90, v91
	v_max3_f32 v128, v128, |v24|, |v28|
	v_max3_f32 v130, v130, |v50|, |v54|
	ds_write_b16 v166, v136
	ds_write_b16_d16_hi v166, v136 offset:4112
	ds_write_b16 v166, v137 offset:8224
	ds_write_b16_d16_hi v166, v137 offset:12336
	s_waitcnt vmcnt(8)
	v_cvt_pk_bf16_f32 v136, v92, v93
	v_cvt_pk_bf16_f32 v137, v94, v95
	v_max3_f32 v129, |v1|, 0, |v5|
	v_max3_f32 v128, v128, |v32|, |v36|
	v_max3_f32 v130, v130, |v58|, |v62|
	ds_write_b16 v167, v136
	ds_write_b16_d16_hi v167, v136 offset:4112
	ds_write_b16 v167, v137 offset:8224
	ds_write_b16_d16_hi v167, v137 offset:12336
	s_waitcnt vmcnt(7)
	v_cvt_pk_bf16_f32 v136, v96, v97
	v_cvt_pk_bf16_f32 v137, v98, v99
	v_max3_f32 v129, v129, |v9|, |v13|
	v_max3_f32 v128, v128, |v40|, |v44|
	v_max3_f32 v130, v130, |v66|, |v70|
	ds_write_b16 v168, v136
	ds_write_b16_d16_hi v168, v136 offset:4112
	ds_write_b16 v168, v137 offset:8224
	ds_write_b16_d16_hi v168, v137 offset:12336
	s_waitcnt vmcnt(6)
	v_cvt_pk_bf16_f32 v136, v100, v101
	v_cvt_pk_bf16_f32 v137, v102, v103
	v_max3_f32 v129, v129, |v17|, |v21|
	v_max3_f32 v128, v128, |v48|, |v52|
	v_max3_f32 v130, v130, |v74|, |v78|
	ds_write_b16 v169, v136
	ds_write_b16_d16_hi v169, v136 offset:4112
	ds_write_b16 v169, v137 offset:8224
	ds_write_b16_d16_hi v169, v137 offset:12336
	s_waitcnt vmcnt(5)
	v_cvt_pk_bf16_f32 v136, v104, v105
	v_cvt_pk_bf16_f32 v137, v106, v107
	v_max3_f32 v129, v129, |v25|, |v29|
	v_max3_f32 v128, v128, |v56|, |v60|
	v_max3_f32 v130, v130, |v82|, |v86|
	ds_write_b16 v170, v136
	ds_write_b16_d16_hi v170, v136 offset:4112
	ds_write_b16 v170, v137 offset:8224
	ds_write_b16_d16_hi v170, v137 offset:12336
	s_waitcnt vmcnt(4)
	v_cvt_pk_bf16_f32 v136, v108, v109
	v_cvt_pk_bf16_f32 v137, v110, v111
	v_max3_f32 v129, v129, |v33|, |v37|
	v_max3_f32 v128, v128, |v64|, |v68|
	v_max3_f32 v130, v130, |v90|, |v94|
	ds_write_b16 v171, v136
	ds_write_b16_d16_hi v171, v136 offset:4112
	ds_write_b16 v171, v137 offset:8224
	ds_write_b16_d16_hi v171, v137 offset:12336
	s_waitcnt vmcnt(3)
	v_cvt_pk_bf16_f32 v136, v112, v113
	v_cvt_pk_bf16_f32 v137, v114, v115
	v_max3_f32 v129, v129, |v41|, |v45|
	v_max3_f32 v128, v128, |v72|, |v76|
	v_max3_f32 v130, v130, |v98|, |v102|
	ds_write_b16 v172, v136
	ds_write_b16_d16_hi v172, v136 offset:4112
	ds_write_b16 v172, v137 offset:8224
	ds_write_b16_d16_hi v172, v137 offset:12336
	s_waitcnt vmcnt(2)
	v_cvt_pk_bf16_f32 v136, v116, v117
	v_cvt_pk_bf16_f32 v137, v118, v119
	v_max3_f32 v129, v129, |v49|, |v53|
	v_max3_f32 v128, v128, |v80|, |v84|
	v_max3_f32 v130, v130, |v106|, |v110|
	ds_write_b16 v173, v136
	ds_write_b16_d16_hi v173, v136 offset:4112
	ds_write_b16 v173, v137 offset:8224
	ds_write_b16_d16_hi v173, v137 offset:12336
	s_waitcnt vmcnt(1)
	v_cvt_pk_bf16_f32 v136, v120, v121
	v_cvt_pk_bf16_f32 v137, v122, v123
	v_max3_f32 v129, v129, |v57|, |v61|
	v_max3_f32 v128, v128, |v88|, |v92|
	v_max3_f32 v130, v130, |v114|, |v118|
	ds_write_b16 v174, v136
	ds_write_b16_d16_hi v174, v136 offset:4112
	ds_write_b16 v174, v137 offset:8224
	ds_write_b16_d16_hi v174, v137 offset:12336
	v_and_b32_e32 v137, 64, v177
	v_max3_f32 v131, |v3|, 0, |v7|
	v_max3_f32 v129, v129, |v65|, |v69|
	v_max3_f32 v128, v128, |v96|, |v100|
	s_waitcnt vmcnt(0)
	v_max3_f32 v136, v130, |v122|, |v126|
	v_xor_b32_e32 v130, 8, v177
	v_add_u32_e32 v137, 64, v137
	v_max3_f32 v131, v131, |v11|, |v15|
	v_max3_f32 v129, v129, |v73|, |v77|
	v_max3_f32 v128, v128, |v104|, |v108|
	v_cmp_lt_i32_e32 vcc, v130, v137
	v_max3_f32 v131, v131, |v19|, |v23|
	v_max3_f32 v129, v129, |v81|, |v85|
	v_max3_f32 v128, v128, |v112|, |v116|
	v_cndmask_b32_e32 v130, v177, v130, vcc
	v_max3_f32 v131, v131, |v27|, |v31|
	v_max3_f32 v129, v129, |v89|, |v93|
	v_max3_f32 v128, v128, |v120|, |v124|
	v_lshlrev_b32_e32 v130, 2, v130
	v_max3_f32 v131, v131, |v35|, |v39|
	v_max3_f32 v129, v129, |v97|, |v101|
	ds_bpermute_b32 v139, v130, v128
	v_max3_f32 v131, v131, |v43|, |v47|
	v_max3_f32 v129, v129, |v105|, |v109|
	v_xor_b32_e32 v138, 16, v177
	v_max3_f32 v131, v131, |v51|, |v55|
	v_max3_f32 v129, v129, |v113|, |v117|
	v_cmp_lt_i32_e32 vcc, v138, v137
	v_xor_b32_e32 v182, 32, v177
	v_max3_f32 v131, v131, |v59|, |v63|
	v_max3_f32 v129, v129, |v121|, |v125|
	v_cndmask_b32_e32 v138, v177, v138, vcc
	v_cmp_lt_i32_e32 vcc, v182, v137
	v_max3_f32 v131, v131, |v67|, |v71|
	v_max3_f32 v131, v131, |v75|, |v79|
	v_cndmask_b32_e32 v137, v177, v182, vcc
	ds_bpermute_b32 v182, v130, v129
	s_waitcnt lgkmcnt(0)
	v_max_f32_e32 v139, v139, v139
	v_max3_f32 v131, v131, |v83|, |v87|
	v_lshlrev_b32_e32 v138, 2, v138
	v_max_f32_e32 v128, v128, v139
	v_max3_f32 v131, v131, |v91|, |v95|
	ds_bpermute_b32 v139, v138, v128
	v_max3_f32 v131, v131, |v99|, |v103|
	v_max3_f32 v131, v131, |v107|, |v111|
	v_lshlrev_b32_e32 v183, 2, v137
	v_max_f32_e32 v137, v182, v182
	v_max3_f32 v131, v131, |v115|, |v119|
	v_max_f32_e32 v137, v129, v137
	v_max3_f32 v131, v131, |v123|, |v127|
	ds_bpermute_b32 v182, v138, v137
	s_waitcnt lgkmcnt(1)
	v_max_f32_e32 v129, v139, v139
	ds_bpermute_b32 v139, v130, v136
	ds_bpermute_b32 v184, v130, v131
	v_max_f32_e32 v128, v128, v129
	s_waitcnt lgkmcnt(2)
	v_max_f32_e32 v182, v182, v182
	v_max_f32_e32 v130, v137, v182
	s_waitcnt lgkmcnt(1)
	v_max_f32_e32 v137, v139, v139
	s_waitcnt lgkmcnt(0)
	v_max_f32_e32 v139, v184, v184
	v_max_f32_e32 v136, v136, v137
	v_max_f32_e32 v139, v131, v139
	ds_bpermute_b32 v137, v138, v136
	ds_bpermute_b32 v138, v138, v139
	ds_bpermute_b32 v129, v183, v128
	ds_bpermute_b32 v131, v183, v130
	v_cvt_pk_bf16_f32 v180, v124, v125
	s_waitcnt lgkmcnt(3)
	v_max_f32_e32 v137, v137, v137
	s_waitcnt lgkmcnt(2)
	v_max_f32_e32 v138, v138, v138
	v_max_f32_e32 v136, v136, v137
	v_max_f32_e32 v138, v139, v138
	ds_bpermute_b32 v137, v183, v136
	ds_bpermute_b32 v139, v183, v138
	v_cvt_pk_bf16_f32 v181, v126, v127
	ds_write_b16 v175, v180
	ds_write_b16_d16_hi v175, v180 offset:4112
	ds_write_b16 v175, v181 offset:8224
	ds_write_b16_d16_hi v175, v181 offset:12336
	s_and_saveexec_b64 s[42:43], s[4:5]
	s_cbranch_execz .LBB0_1108
	s_waitcnt lgkmcnt(4)
	v_max_f32_e32 v139, v139, v139
	v_max_f32_e32 v138, v138, v138
	v_max_f32_e32 v137, v137, v137
	v_max_f32_e32 v136, v136, v136
	v_max_f32_e32 v131, v131, v131
	v_max_f32_e32 v130, v130, v130
	v_max_f32_e32 v129, v129, v129
	v_max_f32_e32 v128, v128, v128
	v_max_f32_e32 v139, v138, v139
	v_max_f32_e32 v138, v136, v137
	v_max_f32_e32 v137, v130, v131
	v_max_f32_e32 v136, v128, v129
	ds_write_b128 v176, v[136:139]

; __device__ __forceinline__ unsigned cvt_pk_bf16(float lo, float hi) { unsigned r; asm volatile("v_cvt_pk_bf16_f32 %0, %1, %2" : "=v"(r) : "v"(lo), "v"(hi)); return r; }
; __device__ __forceinline__ void do_slabs_impl(LAS unsigned char* lds, unsigned char* ws, const float* w_up, const float* w_dn, const float* w_in, int vcu, int G, int wave, int j0, int j1) {
;     ...
;         if (cur.valid) {
;             f32x4 mx = (f32x4){0.f, 0.f, 0.f, 0.f};
; #pragma unroll
;             for (int i = 0; i < 32; ++i) { const int k = wave * 256 + i * 8 + kq; const f32x4 x = v[i];
;                 mx[0] = fmaxf(mx[0], fabsf(x[0])); mx[1] = fmaxf(mx[1], fabsf(x[1])); mx[2] = fmaxf(mx[2], fabsf(x[2])); mx[3] = fmaxf(mx[3], fabsf(x[3]));
;                 const unsigned p01 = cvt_pk_bf16(x[0], x[1]), p23 = cvt_pk_bf16(x[2], x[3]);
;                 const int ks = k ^ (((c4 >> 3) & 3) << 3);
;                 slab[(c4 + 0) * PITCH + ks] = (bf16)(p01 & 0xffffu); slab[(c4 + 1) * PITCH + ks] = (bf16)(p01 >> 16); slab[(c4 + 2) * PITCH + ks] = (bf16)(p23 & 0xffffu); slab[(c4 + 3) * PITCH + ks] = (bf16)(p23 >> 16); }
.LBB0_1140:
	s_cmp_lg_u32 s24, 0
	s_cselect_b64 s[36:37], -1, 0
	s_cmp_eq_u32 s24, 0
	s_cbranch_scc1 .LBB0_1144
	s_waitcnt vmcnt(31)
	v_cvt_pk_bf16_f32 v128, v0, v1
	v_cvt_pk_bf16_f32 v129, v2, v3
	ds_write_b16 v144, v128
	ds_write_b16_d16_hi v144, v128 offset:4112
	ds_write_b16 v144, v129 offset:8224
	ds_write_b16_d16_hi v144, v129 offset:12336
	s_waitcnt vmcnt(30)
	v_cvt_pk_bf16_f32 v136, v4, v5
	v_cvt_pk_bf16_f32 v137, v6, v7
	ds_write_b16 v145, v136
	ds_write_b16_d16_hi v145, v136 offset:4112
	ds_write_b16 v145, v137 offset:8224
	ds_write_b16_d16_hi v145, v137 offset:12336
	s_waitcnt vmcnt(29)
	v_cvt_pk_bf16_f32 v136, v8, v9
	v_cvt_pk_bf16_f32 v137, v10, v11
	ds_write_b16 v146, v136
	ds_write_b16_d16_hi v146, v136 offset:4112
	ds_write_b16 v146, v137 offset:8224
	ds_write_b16_d16_hi v146, v137 offset:12336
	s_waitcnt vmcnt(28)
	v_cvt_pk_bf16_f32 v136, v12, v13
	v_cvt_pk_bf16_f32 v137, v14, v15
	ds_write_b16 v147, v136
	ds_write_b16_d16_hi v147, v136 offset:4112
	ds_write_b16 v147, v137 offset:8224
	ds_write_b16_d16_hi v147, v137 offset:12336
	s_waitcnt vmcnt(27)
	v_cvt_pk_bf16_f32 v136, v16, v17
	v_cvt_pk_bf16_f32 v137, v18, v19
	ds_write_b16 v148, v136
	ds_write_b16_d16_hi v148, v136 offset:4112
	ds_write_b16 v148, v137 offset:8224
	ds_write_b16_d16_hi v148, v137 offset:12336
	s_waitcnt vmcnt(26)
	v_cvt_pk_bf16_f32 v136, v20, v21
	v_cvt_pk_bf16_f32 v137, v22, v23
	ds_write_b16 v149, v136
	ds_write_b16_d16_hi v149, v136 offset:4112
	ds_write_b16 v149, v137 offset:8224
	ds_write_b16_d16_hi v149, v137 offset:12336
	s_waitcnt vmcnt(25)
	v_cvt_pk_bf16_f32 v136, v24, v25
	v_cvt_pk_bf16_f32 v137, v26, v27
	ds_write_b16 v150, v136
	ds_write_b16_d16_hi v150, v136 offset:4112
	ds_write_b16 v150, v137 offset:8224
	ds_write_b16_d16_hi v150, v137 offset:12336
	s_waitcnt vmcnt(24)
	v_cvt_pk_bf16_f32 v136, v28, v29
	v_cvt_pk_bf16_f32 v137, v30, v31
	ds_write_b16 v151, v136
	ds_write_b16_d16_hi v151, v136 offset:4112
	ds_write_b16 v151, v137 offset:8224
	ds_write_b16_d16_hi v151, v137 offset:12336
	s_waitcnt vmcnt(23)
	v_cvt_pk_bf16_f32 v136, v32, v33
	v_cvt_pk_bf16_f32 v137, v34, v35
	ds_write_b16 v152, v136
	ds_write_b16_d16_hi v152, v136 offset:4112
	ds_write_b16 v152, v137 offset:8224
	ds_write_b16_d16_hi v152, v137 offset:12336
	s_waitcnt vmcnt(22)
	v_cvt_pk_bf16_f32 v136, v36, v37
	v_cvt_pk_bf16_f32 v137, v38, v39
	ds_write_b16 v153, v136
	ds_write_b16_d16_hi v153, v136 offset:4112
	ds_write_b16 v153, v137 offset:8224
	ds_write_b16_d16_hi v153, v137 offset:12336
	s_waitcnt vmcnt(21)
	v_cvt_pk_bf16_f32 v136, v40, v41
	v_cvt_pk_bf16_f32 v137, v42, v43
	ds_write_b16 v154, v136
	ds_write_b16_d16_hi v154, v136 offset:4112
	ds_write_b16 v154, v137 offset:8224
	ds_write_b16_d16_hi v154, v137 offset:12336
	s_waitcnt vmcnt(20)
	v_cvt_pk_bf16_f32 v136, v44, v45
	v_cvt_pk_bf16_f32 v137, v46, v47
	ds_write_b16 v155, v136
	ds_write_b16_d16_hi v155, v136 offset:4112
	ds_write_b16 v155, v137 offset:8224
	ds_write_b16_d16_hi v155, v137 offset:12336
	s_waitcnt vmcnt(19)
	v_cvt_pk_bf16_f32 v136, v48, v49
	v_cvt_pk_bf16_f32 v137, v50, v51
	ds_write_b16 v156, v136
	ds_write_b16_d16_hi v156, v136 offset:4112
	ds_write_b16 v156, v137 offset:8224
	ds_write_b16_d16_hi v156, v137 offset:12336
	s_waitcnt vmcnt(18)
	v_cvt_pk_bf16_f32 v136, v52, v53
	v_cvt_pk_bf16_f32 v137, v54, v55
	ds_write_b16 v157, v136
	ds_write_b16_d16_hi v157, v136 offset:4112
	ds_write_b16 v157, v137 offset:8224
	ds_write_b16_d16_hi v157, v137 offset:12336
	s_waitcnt vmcnt(17)
	v_cvt_pk_bf16_f32 v136, v56, v57
	v_cvt_pk_bf16_f32 v137, v58, v59
	ds_write_b16 v158, v136
	ds_write_b16_d16_hi v158, v136 offset:4112
	ds_write_b16 v158, v137 offset:8224
	ds_write_b16_d16_hi v158, v137 offset:12336
	s_waitcnt vmcnt(16)
	v_cvt_pk_bf16_f32 v136, v60, v61
	v_cvt_pk_bf16_f32 v137, v62, v63
	ds_write_b16 v159, v136
	ds_write_b16_d16_hi v159, v136 offset:4112
	ds_write_b16 v159, v137 offset:8224
	ds_write_b16_d16_hi v159, v137 offset:12336
	s_waitcnt vmcnt(15)
	v_cvt_pk_bf16_f32 v136, v64, v65
	v_cvt_pk_bf16_f32 v137, v66, v67
	v_max3_f32 v130, |v2|, 0, |v6|
	ds_write_b16 v160, v136
	ds_write_b16_d16_hi v160, v136 offset:4112
	ds_write_b16 v160, v137 offset:8224
	ds_write_b16_d16_hi v160, v137 offset:12336
	s_waitcnt vmcnt(14)
	v_cvt_pk_bf16_f32 v136, v68, v69
	v_cvt_pk_bf16_f32 v137, v70, v71
	v_max3_f32 v130, v130, |v10|, |v14|
	ds_write_b16 v161, v136
	ds_write_b16_d16_hi v161, v136 offset:4112
	ds_write_b16 v161, v137 offset:8224
	ds_write_b16_d16_hi v161, v137 offset:12336
	s_waitcnt vmcnt(13)
	v_cvt_pk_bf16_f32 v136, v72, v73
	v_cvt_pk_bf16_f32 v137, v74, v75
	v_max3_f32 v130, v130, |v18|, |v22|
	ds_write_b16 v162, v136
	ds_write_b16_d16_hi v162, v136 offset:4112
	ds_write_b16 v162, v137 offset:8224
	ds_write_b16_d16_hi v162, v137 offset:12336
	s_waitcnt vmcnt(12)
	v_cvt_pk_bf16_f32 v136, v76, v77
	v_cvt_pk_bf16_f32 v137, v78, v79
	v_max3_f32 v128, |v0|, 0, |v4|
	v_max3_f32 v130, v130, |v26|, |v30|
	ds_write_b16 v163, v136
	ds_write_b16_d16_hi v163, v136 offset:4112
	ds_write_b16 v163, v137 offset:8224
	ds_write_b16_d16_hi v163, v137 offset:12336
	s_waitcnt vmcnt(11)
	v_cvt_pk_bf16_f32 v136, v80, v81
	v_cvt_pk_bf16_f32 v137, v82, v83
	v_max3_f32 v128, v128, |v8|, |v12|
	v_max3_f32 v130, v130, |v34|, |v38|
	ds_write_b16 v164, v136
	ds_write_b16_d16_hi v164, v136 offset:4112
	ds_write_b16 v164, v137 offset:8224
	ds_write_b16_d16_hi v164, v137 offset:12336
	s_waitcnt vmcnt(10)
	v_cvt_pk_bf16_f32 v136, v84, v85
	v_cvt_pk_bf16_f32 v137, v86, v87
	v_max3_f32 v128, v128, |v16|, |v20|
	v_max3_f32 v130, v130, |v42|, |v46|
	ds_write_b16 v165, v136
	ds_write_b16_d16_hi v165, v136 offset:4112
	ds_write_b16 v165, v137 offset:8224
	ds_write_b16_d16_hi v165, v137 offset:12336
	s_waitcnt vmcnt(9)
; #define LAS __attribute__((address_space(3)))
; __device__ __forceinline__ unsigned cvt_pk_bf16(float lo, float hi) { unsigned r; asm volatile("v_cvt_pk_bf16_f32 %0, %1, %2" : "=v"(r) : "v"(lo), "v"(hi)); return r; }
; __device__ __forceinline__ void do_slabs_impl(LAS unsigned char* lds, unsigned char* ws, const float* w_up, const float* w_dn, const float* w_in, int vcu, int G, int wave, int j0, int j1) {
;     ...
;             for (int i = 0; i < 32; ++i) { const int k = wave * 256 + i * 8 + kq; const f32x4 x = v[i];
;                 mx[0] = fmaxf(mx[0], fabsf(x[0])); mx[1] = fmaxf(mx[1], fabsf(x[1])); mx[2] = fmaxf(mx[2], fabsf(x[2])); mx[3] = fmaxf(mx[3], fabsf(x[3]));
;                 const unsigned p01 = cvt_pk_bf16(x[0], x[1]), p23 = cvt_pk_bf16(x[2], x[3]);
;                 const int ks = k ^ (((c4 >> 3) & 3) << 3);
;                 slab[(c4 + 0) * PITCH + ks] = (bf16)(p01 & 0xffffu); slab[(c4 + 1) * PITCH + ks] = (bf16)(p01 >> 16); slab[(c4 + 2) * PITCH + ks] = (bf16)(p23 & 0xffffu); slab[(c4 + 3) * PITCH + ks] = (bf16)(p23 >> 16); }
; #pragma unroll
;             for (int q = 0; q < 4; ++q) { float m = mx[q]; m = fmaxf(m, __shfl_xor(m, 8)); m = fmaxf(m, __shfl_xor(m, 16)); m = fmaxf(m, __shfl_xor(m, 32)); mx[q] = m; }
;             if (lane < 8) { LAS float* d = red + wave * 32 + c4; d[0] = mx[0]; d[1] = mx[1]; d[2] = mx[2]; d[3] = mx[3]; }
	v_cvt_pk_bf16_f32 v136, v88, v89
	v_cvt_pk_bf16_f32 v137, v90, v91
	v_max3_f32 v128, v128, |v24|, |v28|
	v_max3_f32 v130, v130, |v50|, |v54|
	ds_write_b16 v166, v136
	ds_write_b16_d16_hi v166, v136 offset:4112
	ds_write_b16 v166, v137 offset:8224
	ds_write_b16_d16_hi v166, v137 offset:12336
	s_waitcnt vmcnt(8)
	v_cvt_pk_bf16_f32 v136, v92, v93
	v_cvt_pk_bf16_f32 v137, v94, v95
	v_max3_f32 v129, |v1|, 0, |v5|
	v_max3_f32 v128, v128, |v32|, |v36|
	v_max3_f32 v130, v130, |v58|, |v62|
	ds_write_b16 v167, v136
	ds_write_b16_d16_hi v167, v136 offset:4112
	ds_write_b16 v167, v137 offset:8224
	ds_write_b16_d16_hi v167, v137 offset:12336
	s_waitcnt vmcnt(7)
	v_cvt_pk_bf16_f32 v136, v96, v97
	v_cvt_pk_bf16_f32 v137, v98, v99
	v_max3_f32 v129, v129, |v9|, |v13|
	v_max3_f32 v128, v128, |v40|, |v44|
	v_max3_f32 v130, v130, |v66|, |v70|
	ds_write_b16 v168, v136
	ds_write_b16_d16_hi v168, v136 offset:4112
	ds_write_b16 v168, v137 offset:8224
	ds_write_b16_d16_hi v168, v137 offset:12336
	s_waitcnt vmcnt(6)
	v_cvt_pk_bf16_f32 v136, v100, v101
	v_cvt_pk_bf16_f32 v137, v102, v103
	v_max3_f32 v129, v129, |v17|, |v21|
	v_max3_f32 v128, v128, |v48|, |v52|
	v_max3_f32 v130, v130, |v74|, |v78|
	ds_write_b16 v169, v136
	ds_write_b16_d16_hi v169, v136 offset:4112
	ds_write_b16 v169, v137 offset:8224
	ds_write_b16_d16_hi v169, v137 offset:12336
	s_waitcnt vmcnt(5)
	v_cvt_pk_bf16_f32 v136, v104, v105
	v_cvt_pk_bf16_f32 v137, v106, v107
	v_max3_f32 v129, v129, |v25|, |v29|
	v_max3_f32 v128, v128, |v56|, |v60|
	v_max3_f32 v130, v130, |v82|, |v86|
	ds_write_b16 v170, v136
	ds_write_b16_d16_hi v170, v136 offset:4112
	ds_write_b16 v170, v137 offset:8224
	ds_write_b16_d16_hi v170, v137 offset:12336
	s_waitcnt vmcnt(4)
	v_cvt_pk_bf16_f32 v136, v108, v109
	v_cvt_pk_bf16_f32 v137, v110, v111
	v_max3_f32 v129, v129, |v33|, |v37|
	v_max3_f32 v128, v128, |v64|, |v68|
	v_max3_f32 v130, v130, |v90|, |v94|
	ds_write_b16 v171, v136
	ds_write_b16_d16_hi v171, v136 offset:4112
	ds_write_b16 v171, v137 offset:8224
	ds_write_b16_d16_hi v171, v137 offset:12336
	s_waitcnt vmcnt(3)
	v_cvt_pk_bf16_f32 v136, v112, v113
	v_cvt_pk_bf16_f32 v137, v114, v115
	v_max3_f32 v129, v129, |v41|, |v45|
	v_max3_f32 v128, v128, |v72|, |v76|
	v_max3_f32 v130, v130, |v98|, |v102|
	ds_write_b16 v172, v136
	ds_write_b16_d16_hi v172, v136 offset:4112
	ds_write_b16 v172, v137 offset:8224
	ds_write_b16_d16_hi v172, v137 offset:12336
	s_waitcnt vmcnt(2)
	v_cvt_pk_bf16_f32 v136, v116, v117
	v_cvt_pk_bf16_f32 v137, v118, v119
	v_max3_f32 v129, v129, |v49|, |v53|
	v_max3_f32 v128, v128, |v80|, |v84|
	v_max3_f32 v130, v130, |v106|, |v110|
	ds_write_b16 v173, v136
	ds_write_b16_d16_hi v173, v136 offset:4112
	ds_write_b16 v173, v137 offset:8224
	ds_write_b16_d16_hi v173, v137 offset:12336
	s_waitcnt vmcnt(1)
	v_cvt_pk_bf16_f32 v136, v120, v121
	v_cvt_pk_bf16_f32 v137, v122, v123
	v_max3_f32 v129, v129, |v57|, |v61|
	v_max3_f32 v128, v128, |v88|, |v92|
	v_max3_f32 v130, v130, |v114|, |v118|
	ds_write_b16 v174, v136
	ds_write_b16_d16_hi v174, v136 offset:4112
	ds_write_b16 v174, v137 offset:8224
	ds_write_b16_d16_hi v174, v137 offset:12336
	v_and_b32_e32 v137, 64, v177
	v_max3_f32 v131, |v3|, 0, |v7|
	v_max3_f32 v129, v129, |v65|, |v69|
	v_max3_f32 v128, v128, |v96|, |v100|
	s_waitcnt vmcnt(0)
	v_max3_f32 v136, v130, |v122|, |v126|
	v_xor_b32_e32 v130, 8, v177
	v_add_u32_e32 v137, 64, v137
	v_max3_f32 v131, v131, |v11|, |v15|
	v_max3_f32 v129, v129, |v73|, |v77|
	v_max3_f32 v128, v128, |v104|, |v108|
	v_cmp_lt_i32_e32 vcc, v130, v137
	v_max3_f32 v131, v131, |v19|, |v23|
	v_max3_f32 v129, v129, |v81|, |v85|
	v_max3_f32 v128, v128, |v112|, |v116|
	v_cndmask_b32_e32 v130, v177, v130, vcc
	v_max3_f32 v131, v131, |v27|, |v31|
	v_max3_f32 v129, v129, |v89|, |v93|
	v_max3_f32 v128, v128, |v120|, |v124|
	v_lshlrev_b32_e32 v130, 2, v130
	v_max3_f32 v131, v131, |v35|, |v39|
	v_max3_f32 v129, v129, |v97|, |v101|
	ds_bpermute_b32 v139, v130, v128
	v_max3_f32 v131, v131, |v43|, |v47|
	v_max3_f32 v129, v129, |v105|, |v109|
	v_xor_b32_e32 v138, 16, v177
	v_max3_f32 v131, v131, |v51|, |v55|
	v_max3_f32 v129, v129, |v113|, |v117|
	v_cmp_lt_i32_e32 vcc, v138, v137
	v_xor_b32_e32 v182, 32, v177
	v_max3_f32 v131, v131, |v59|, |v63|
	v_max3_f32 v129, v129, |v121|, |v125|
	v_cndmask_b32_e32 v138, v177, v138, vcc
	v_cmp_lt_i32_e32 vcc, v182, v137
	v_max3_f32 v131, v131, |v67|, |v71|
	v_max3_f32 v131, v131, |v75|, |v79|
	v_cndmask_b32_e32 v137, v177, v182, vcc
	ds_bpermute_b32 v182, v130, v129
	s_waitcnt lgkmcnt(0)
	v_max_f32_e32 v139, v139, v139
	v_max3_f32 v131, v131, |v83|, |v87|
	v_lshlrev_b32_e32 v138, 2, v138
	v_max_f32_e32 v128, v128, v139
	v_max3_f32 v131, v131, |v91|, |v95|
	ds_bpermute_b32 v139, v138, v128
	v_max3_f32 v131, v131, |v99|, |v103|
	v_max3_f32 v131, v131, |v107|, |v111|
	v_lshlrev_b32_e32 v183, 2, v137
	v_max_f32_e32 v137, v182, v182
	v_max3_f32 v131, v131, |v115|, |v119|
	v_max_f32_e32 v137, v129, v137
	v_max3_f32 v131, v131, |v123|, |v127|
	ds_bpermute_b32 v182, v138, v137
	s_waitcnt lgkmcnt(1)
	v_max_f32_e32 v129, v139, v139
	ds_bpermute_b32 v139, v130, v136
	ds_bpermute_b32 v184, v130, v131
	v_max_f32_e32 v128, v128, v129
	s_waitcnt lgkmcnt(2)
	v_max_f32_e32 v182, v182, v182
	v_max_f32_e32 v130, v137, v182
	s_waitcnt lgkmcnt(1)
	v_max_f32_e32 v137, v139, v139
	s_waitcnt lgkmcnt(0)
	v_max_f32_e32 v139, v184, v184
	v_max_f32_e32 v136, v136, v137
	v_max_f32_e32 v139, v131, v139
	ds_bpermute_b32 v137, v138, v136
	ds_bpermute_b32 v138, v138, v139
	ds_bpermute_b32 v129, v183, v128
	ds_bpermute_b32 v131, v183, v130
	v_cvt_pk_bf16_f32 v180, v124, v125
	s_waitcnt lgkmcnt(3)
	v_max_f32_e32 v137, v137, v137
	s_waitcnt lgkmcnt(2)
	v_max_f32_e32 v138, v138, v138
	v_max_f32_e32 v136, v136, v137
	v_max_f32_e32 v138, v139, v138
	ds_bpermute_b32 v137, v183, v136
	ds_bpermute_b32 v139, v183, v138
	v_cvt_pk_bf16_f32 v181, v126, v127
	ds_write_b16 v175, v180
	ds_write_b16_d16_hi v175, v180 offset:4112
	ds_write_b16 v175, v181 offset:8224
	ds_write_b16_d16_hi v175, v181 offset:12336
	s_and_saveexec_b64 s[38:39], s[4:5]
	s_cbranch_execz .LBB0_1143
	s_waitcnt lgkmcnt(4)
	v_max_f32_e32 v139, v139, v139
	v_max_f32_e32 v138, v138, v138
	v_max_f32_e32 v137, v137, v137
	v_max_f32_e32 v136, v136, v136
	v_max_f32_e32 v131, v131, v131
	v_max_f32_e32 v130, v130, v130
	v_max_f32_e32 v129, v129, v129
	v_max_f32_e32 v128, v128, v128
	v_max_f32_e32 v139, v138, v139
	v_max_f32_e32 v138, v136, v137
	v_max_f32_e32 v137, v130, v131
	v_max_f32_e32 v136, v128, v129
	ds_write_b128 v176, v[136:139]

; __device__ __forceinline__ unsigned cvt_pk_bf16(float lo, float hi) { unsigned r; asm volatile("v_cvt_pk_bf16_f32 %0, %1, %2" : "=v"(r) : "v"(lo), "v"(hi)); return r; }
; __device__ __forceinline__ void do_slabs_impl(LAS unsigned char* lds, unsigned char* ws, const float* w_up, const float* w_dn, const float* w_in, int vcu, int G, int wave, int j0, int j1) {
;     ...
;         if (cur.valid) {
;             f32x4 mx = (f32x4){0.f, 0.f, 0.f, 0.f};
; #pragma unroll
;             for (int i = 0; i < 32; ++i) { const int k = wave * 256 + i * 8 + kq; const f32x4 x = v[i];
;                 mx[0] = fmaxf(mx[0], fabsf(x[0])); mx[1] = fmaxf(mx[1], fabsf(x[1])); mx[2] = fmaxf(mx[2], fabsf(x[2])); mx[3] = fmaxf(mx[3], fabsf(x[3]));
;                 const unsigned p01 = cvt_pk_bf16(x[0], x[1]), p23 = cvt_pk_bf16(x[2], x[3]);
;                 const int ks = k ^ (((c4 >> 3) & 3) << 3);
;                 slab[(c4 + 0) * PITCH + ks] = (bf16)(p01 & 0xffffu); slab[(c4 + 1) * PITCH + ks] = (bf16)(p01 >> 16); slab[(c4 + 2) * PITCH + ks] = (bf16)(p23 & 0xffffu); slab[(c4 + 3) * PITCH + ks] = (bf16)(p23 >> 16); }
.LBB0_1272:
	s_cmp_lg_u32 s65, 0
	s_cselect_b64 s[60:61], -1, 0
	s_cmp_eq_u32 s65, 0
	s_cbranch_scc1 .LBB0_1276
	s_waitcnt vmcnt(31)
	v_cvt_pk_bf16_f32 v128, v0, v1
	v_cvt_pk_bf16_f32 v129, v2, v3
	ds_write_b16 v143, v128
	ds_write_b16_d16_hi v143, v128 offset:4112
	ds_write_b16 v143, v129 offset:8224
	ds_write_b16_d16_hi v143, v129 offset:12336
	s_waitcnt vmcnt(30)
	s_waitcnt vmcnt(30)
	v_cvt_pk_bf16_f32 v134, v4, v5
	v_cvt_pk_bf16_f32 v135, v6, v7
	ds_write_b16 v146, v134
	ds_write_b16_d16_hi v146, v134 offset:4112
	ds_write_b16 v146, v135 offset:8224
	ds_write_b16_d16_hi v146, v135 offset:12336
	s_waitcnt vmcnt(29)
	s_waitcnt vmcnt(29)
	v_cvt_pk_bf16_f32 v134, v8, v9
	v_cvt_pk_bf16_f32 v135, v10, v11
	ds_write_b16 v147, v134
	ds_write_b16_d16_hi v147, v134 offset:4112
	ds_write_b16 v147, v135 offset:8224
	ds_write_b16_d16_hi v147, v135 offset:12336
	s_waitcnt vmcnt(28)
	s_waitcnt vmcnt(28)
	v_cvt_pk_bf16_f32 v134, v12, v13
	v_cvt_pk_bf16_f32 v135, v14, v15
	ds_write_b16 v148, v134
	ds_write_b16_d16_hi v148, v134 offset:4112
	ds_write_b16 v148, v135 offset:8224
	ds_write_b16_d16_hi v148, v135 offset:12336
	s_waitcnt vmcnt(27)
	s_waitcnt vmcnt(27)
	v_cvt_pk_bf16_f32 v134, v16, v17
	v_cvt_pk_bf16_f32 v135, v18, v19
	ds_write_b16 v149, v134
	ds_write_b16_d16_hi v149, v134 offset:4112
	ds_write_b16 v149, v135 offset:8224
	ds_write_b16_d16_hi v149, v135 offset:12336
	s_waitcnt vmcnt(26)
	s_waitcnt vmcnt(26)
	v_cvt_pk_bf16_f32 v134, v20, v21
	v_cvt_pk_bf16_f32 v135, v22, v23
	ds_write_b16 v150, v134
	ds_write_b16_d16_hi v150, v134 offset:4112
	ds_write_b16 v150, v135 offset:8224
	ds_write_b16_d16_hi v150, v135 offset:12336
	s_waitcnt vmcnt(25)
	s_waitcnt vmcnt(25)
	v_cvt_pk_bf16_f32 v134, v24, v25
	v_cvt_pk_bf16_f32 v135, v26, v27
	ds_write_b16 v151, v134
	ds_write_b16_d16_hi v151, v134 offset:4112
	ds_write_b16 v151, v135 offset:8224
	ds_write_b16_d16_hi v151, v135 offset:12336
	s_waitcnt vmcnt(24)
	s_waitcnt vmcnt(24)
	v_cvt_pk_bf16_f32 v134, v28, v29
	v_cvt_pk_bf16_f32 v135, v30, v31
	ds_write_b16 v152, v134
	ds_write_b16_d16_hi v152, v134 offset:4112
	ds_write_b16 v152, v135 offset:8224
	ds_write_b16_d16_hi v152, v135 offset:12336
	s_waitcnt vmcnt(23)
	s_waitcnt vmcnt(23)
	v_cvt_pk_bf16_f32 v134, v32, v33
	v_cvt_pk_bf16_f32 v135, v34, v35
	ds_write_b16 v153, v134
	ds_write_b16_d16_hi v153, v134 offset:4112
	ds_write_b16 v153, v135 offset:8224
	ds_write_b16_d16_hi v153, v135 offset:12336
	s_waitcnt vmcnt(22)
	s_waitcnt vmcnt(22)
	v_cvt_pk_bf16_f32 v134, v36, v37
	v_cvt_pk_bf16_f32 v135, v38, v39
	ds_write_b16 v154, v134
	ds_write_b16_d16_hi v154, v134 offset:4112
	ds_write_b16 v154, v135 offset:8224
	ds_write_b16_d16_hi v154, v135 offset:12336
	s_waitcnt vmcnt(21)
	s_waitcnt vmcnt(21)
	v_cvt_pk_bf16_f32 v134, v40, v41
	v_cvt_pk_bf16_f32 v135, v42, v43
	ds_write_b16 v155, v134
	ds_write_b16_d16_hi v155, v134 offset:4112
	ds_write_b16 v155, v135 offset:8224
	ds_write_b16_d16_hi v155, v135 offset:12336
	s_waitcnt vmcnt(20)
	s_waitcnt vmcnt(20)
	v_cvt_pk_bf16_f32 v134, v44, v45
	v_cvt_pk_bf16_f32 v135, v46, v47
	ds_write_b16 v156, v134
	ds_write_b16_d16_hi v156, v134 offset:4112
	ds_write_b16 v156, v135 offset:8224
	ds_write_b16_d16_hi v156, v135 offset:12336
	s_waitcnt vmcnt(19)
	s_waitcnt vmcnt(19)
	v_cvt_pk_bf16_f32 v134, v48, v49
	v_cvt_pk_bf16_f32 v135, v50, v51
	ds_write_b16 v157, v134
	ds_write_b16_d16_hi v157, v134 offset:4112
	ds_write_b16 v157, v135 offset:8224
	ds_write_b16_d16_hi v157, v135 offset:12336
	s_waitcnt vmcnt(18)
	s_waitcnt vmcnt(18)
	v_cvt_pk_bf16_f32 v134, v52, v53
	v_cvt_pk_bf16_f32 v135, v54, v55
	ds_write_b16 v158, v134
	ds_write_b16_d16_hi v158, v134 offset:4112
	ds_write_b16 v158, v135 offset:8224
	ds_write_b16_d16_hi v158, v135 offset:12336
	s_waitcnt vmcnt(17)
	s_waitcnt vmcnt(17)
	v_cvt_pk_bf16_f32 v134, v56, v57
	v_cvt_pk_bf16_f32 v135, v58, v59
	ds_write_b16 v159, v134
	ds_write_b16_d16_hi v159, v134 offset:4112
	ds_write_b16 v159, v135 offset:8224
	ds_write_b16_d16_hi v159, v135 offset:12336
	s_waitcnt vmcnt(16)
	s_waitcnt vmcnt(16)
	v_cvt_pk_bf16_f32 v134, v60, v61
	v_cvt_pk_bf16_f32 v135, v62, v63
	ds_write_b16 v160, v134
	ds_write_b16_d16_hi v160, v134 offset:4112
	ds_write_b16 v160, v135 offset:8224
	ds_write_b16_d16_hi v160, v135 offset:12336
	s_waitcnt vmcnt(15)
	s_waitcnt vmcnt(15)
	v_cvt_pk_bf16_f32 v134, v64, v65
	v_cvt_pk_bf16_f32 v135, v66, v67
	v_max3_f32 v130, |v2|, 0, |v6|
	ds_write_b16 v161, v134
	ds_write_b16_d16_hi v161, v134 offset:4112
	ds_write_b16 v161, v135 offset:8224
	ds_write_b16_d16_hi v161, v135 offset:12336
	s_waitcnt vmcnt(14)
	s_waitcnt vmcnt(14)
	v_cvt_pk_bf16_f32 v134, v68, v69
	v_cvt_pk_bf16_f32 v135, v70, v71
	v_max3_f32 v130, v130, |v10|, |v14|
	ds_write_b16 v162, v134
	ds_write_b16_d16_hi v162, v134 offset:4112
	ds_write_b16 v162, v135 offset:8224
	ds_write_b16_d16_hi v162, v135 offset:12336
	s_waitcnt vmcnt(13)
	s_waitcnt vmcnt(13)
	v_cvt_pk_bf16_f32 v134, v72, v73
	v_cvt_pk_bf16_f32 v135, v74, v75
	v_max3_f32 v130, v130, |v18|, |v22|
	ds_write_b16 v163, v134
	ds_write_b16_d16_hi v163, v134 offset:4112
	ds_write_b16 v163, v135 offset:8224
	ds_write_b16_d16_hi v163, v135 offset:12336
	s_waitcnt vmcnt(12)
	s_waitcnt vmcnt(12)
	v_cvt_pk_bf16_f32 v134, v76, v77
	v_cvt_pk_bf16_f32 v135, v78, v79
	v_max3_f32 v128, |v0|, 0, |v4|
	v_max3_f32 v130, v130, |v26|, |v30|
	ds_write_b16 v164, v134
	ds_write_b16_d16_hi v164, v134 offset:4112
	ds_write_b16 v164, v135 offset:8224
	ds_write_b16_d16_hi v164, v135 offset:12336
	s_waitcnt vmcnt(11)
	s_waitcnt vmcnt(11)
; #define LAS __attribute__((address_space(3)))
; __device__ __forceinline__ unsigned cvt_pk_bf16(float lo, float hi) { unsigned r; asm volatile("v_cvt_pk_bf16_f32 %0, %1, %2" : "=v"(r) : "v"(lo), "v"(hi)); return r; }
; __device__ __forceinline__ void do_slabs_impl(LAS unsigned char* lds, unsigned char* ws, const float* w_up, const float* w_dn, const float* w_in, int vcu, int G, int wave, int j0, int j1) {
;     ...
;         if (cur.valid) {
;             f32x4 mx = (f32x4){0.f, 0.f, 0.f, 0.f};
; #pragma unroll
;             for (int i = 0; i < 32; ++i) { const int k = wave * 256 + i * 8 + kq; const f32x4 x = v[i];
;                 mx[0] = fmaxf(mx[0], fabsf(x[0])); mx[1] = fmaxf(mx[1], fabsf(x[1])); mx[2] = fmaxf(mx[2], fabsf(x[2])); mx[3] = fmaxf(mx[3], fabsf(x[3]));
;                 const unsigned p01 = cvt_pk_bf16(x[0], x[1]), p23 = cvt_pk_bf16(x[2], x[3]);
;                 const int ks = k ^ (((c4 >> 3) & 3) << 3);
;                 slab[(c4 + 0) * PITCH + ks] = (bf16)(p01 & 0xffffu); slab[(c4 + 1) * PITCH + ks] = (bf16)(p01 >> 16); slab[(c4 + 2) * PITCH + ks] = (bf16)(p23 & 0xffffu); slab[(c4 + 3) * PITCH + ks] = (bf16)(p23 >> 16); }
; #pragma unroll
;             for (int q = 0; q < 4; ++q) { float m = mx[q]; m = fmaxf(m, __shfl_xor(m, 8)); m = fmaxf(m, __shfl_xor(m, 16)); m = fmaxf(m, __shfl_xor(m, 32)); mx[q] = m; }
;             if (lane < 8) { LAS float* d = red + wave * 32 + c4; d[0] = mx[0]; d[1] = mx[1]; d[2] = mx[2]; d[3] = mx[3]; }
	v_cvt_pk_bf16_f32 v134, v80, v81
	v_cvt_pk_bf16_f32 v135, v82, v83
	v_max3_f32 v128, v128, |v8|, |v12|
	v_max3_f32 v130, v130, |v34|, |v38|
	ds_write_b16 v165, v134
	ds_write_b16_d16_hi v165, v134 offset:4112
	ds_write_b16 v165, v135 offset:8224
	ds_write_b16_d16_hi v165, v135 offset:12336
	s_waitcnt vmcnt(10)
	s_waitcnt vmcnt(10)
	v_cvt_pk_bf16_f32 v134, v84, v85
	v_cvt_pk_bf16_f32 v135, v86, v87
	v_max3_f32 v128, v128, |v16|, |v20|
	v_max3_f32 v130, v130, |v42|, |v46|
	ds_write_b16 v170, v134
	ds_write_b16_d16_hi v170, v134 offset:4112
	ds_write_b16 v170, v135 offset:8224
	ds_write_b16_d16_hi v170, v135 offset:12336
	s_waitcnt vmcnt(9)
	s_waitcnt vmcnt(9)
	v_cvt_pk_bf16_f32 v134, v88, v89
	v_cvt_pk_bf16_f32 v135, v90, v91
	v_max3_f32 v128, v128, |v24|, |v28|
	v_max3_f32 v130, v130, |v50|, |v54|
	ds_write_b16 v171, v134
	ds_write_b16_d16_hi v171, v134 offset:4112
	ds_write_b16 v171, v135 offset:8224
	ds_write_b16_d16_hi v171, v135 offset:12336
	s_waitcnt vmcnt(8)
	s_waitcnt vmcnt(8)
	v_cvt_pk_bf16_f32 v134, v92, v93
	v_cvt_pk_bf16_f32 v135, v94, v95
	v_max3_f32 v129, |v1|, 0, |v5|
	v_max3_f32 v128, v128, |v32|, |v36|
	v_max3_f32 v130, v130, |v58|, |v62|
	ds_write_b16 v172, v134
	ds_write_b16_d16_hi v172, v134 offset:4112
	ds_write_b16 v172, v135 offset:8224
	ds_write_b16_d16_hi v172, v135 offset:12336
	s_waitcnt vmcnt(7)
	s_waitcnt vmcnt(7)
	v_cvt_pk_bf16_f32 v134, v96, v97
	v_cvt_pk_bf16_f32 v135, v98, v99
	v_max3_f32 v129, v129, |v9|, |v13|
	v_max3_f32 v128, v128, |v40|, |v44|
	v_max3_f32 v130, v130, |v66|, |v70|
	ds_write_b16 v173, v134
	ds_write_b16_d16_hi v173, v134 offset:4112
	ds_write_b16 v173, v135 offset:8224
	ds_write_b16_d16_hi v173, v135 offset:12336
	s_waitcnt vmcnt(6)
	s_waitcnt vmcnt(6)
	v_cvt_pk_bf16_f32 v134, v100, v101
	v_cvt_pk_bf16_f32 v135, v102, v103
	v_max3_f32 v129, v129, |v17|, |v21|
	v_max3_f32 v128, v128, |v48|, |v52|
	v_max3_f32 v130, v130, |v74|, |v78|
	ds_write_b16 v174, v134
	ds_write_b16_d16_hi v174, v134 offset:4112
	ds_write_b16 v174, v135 offset:8224
	ds_write_b16_d16_hi v174, v135 offset:12336
	s_waitcnt vmcnt(5)
	s_waitcnt vmcnt(5)
	v_cvt_pk_bf16_f32 v134, v104, v105
	v_cvt_pk_bf16_f32 v135, v106, v107
	v_max3_f32 v129, v129, |v25|, |v29|
	v_max3_f32 v128, v128, |v56|, |v60|
	v_max3_f32 v130, v130, |v82|, |v86|
	ds_write_b16 v175, v134
	ds_write_b16_d16_hi v175, v134 offset:4112
	ds_write_b16 v175, v135 offset:8224
	ds_write_b16_d16_hi v175, v135 offset:12336
	s_waitcnt vmcnt(4)
	s_waitcnt vmcnt(4)
	v_cvt_pk_bf16_f32 v134, v108, v109
	v_cvt_pk_bf16_f32 v135, v110, v111
	v_max3_f32 v129, v129, |v33|, |v37|
	v_max3_f32 v128, v128, |v64|, |v68|
	v_max3_f32 v130, v130, |v90|, |v94|
	ds_write_b16 v176, v134
	ds_write_b16_d16_hi v176, v134 offset:4112
	ds_write_b16 v176, v135 offset:8224
	ds_write_b16_d16_hi v176, v135 offset:12336
	s_waitcnt vmcnt(3)
	s_waitcnt vmcnt(3)
	v_cvt_pk_bf16_f32 v134, v112, v113
	v_cvt_pk_bf16_f32 v135, v114, v115
	v_max3_f32 v129, v129, |v41|, |v45|
	v_max3_f32 v128, v128, |v72|, |v76|
	v_max3_f32 v130, v130, |v98|, |v102|
	ds_write_b16 v177, v134
	ds_write_b16_d16_hi v177, v134 offset:4112
	ds_write_b16 v177, v135 offset:8224
	ds_write_b16_d16_hi v177, v135 offset:12336
	s_waitcnt vmcnt(2)
	s_waitcnt vmcnt(2)
	v_cvt_pk_bf16_f32 v134, v116, v117
	v_cvt_pk_bf16_f32 v135, v118, v119
	v_max3_f32 v129, v129, |v49|, |v53|
	v_max3_f32 v128, v128, |v80|, |v84|
	v_max3_f32 v130, v130, |v106|, |v110|
	ds_write_b16 v178, v134
	ds_write_b16_d16_hi v178, v134 offset:4112
	ds_write_b16 v178, v135 offset:8224
	ds_write_b16_d16_hi v178, v135 offset:12336
	s_waitcnt vmcnt(1)
	s_waitcnt vmcnt(1)
	v_cvt_pk_bf16_f32 v134, v120, v121
	v_cvt_pk_bf16_f32 v135, v122, v123
	v_max3_f32 v129, v129, |v57|, |v61|
	v_max3_f32 v128, v128, |v88|, |v92|
	v_max3_f32 v130, v130, |v114|, |v118|
	ds_write_b16 v179, v134
	ds_write_b16_d16_hi v179, v134 offset:4112
	ds_write_b16 v179, v135 offset:8224
	ds_write_b16_d16_hi v179, v135 offset:12336
	v_and_b32_e32 v135, 64, v166
	v_max3_f32 v131, |v3|, 0, |v7|
	v_max3_f32 v129, v129, |v65|, |v69|
	v_max3_f32 v128, v128, |v96|, |v100|
	s_waitcnt vmcnt(0)
	v_max3_f32 v134, v130, |v122|, |v126|
	v_xor_b32_e32 v130, 8, v166
	v_add_u32_e32 v135, 64, v135
	v_max3_f32 v131, v131, |v11|, |v15|
	v_max3_f32 v129, v129, |v73|, |v77|
	v_max3_f32 v128, v128, |v104|, |v108|
	v_cmp_lt_i32_e32 vcc, v130, v135
	v_max3_f32 v131, v131, |v19|, |v23|
	v_max3_f32 v129, v129, |v81|, |v85|
	v_max3_f32 v128, v128, |v112|, |v116|
	v_cndmask_b32_e32 v130, v166, v130, vcc
	v_max3_f32 v131, v131, |v27|, |v31|
	v_max3_f32 v129, v129, |v89|, |v93|
	v_max3_f32 v128, v128, |v120|, |v124|
	v_lshlrev_b32_e32 v130, 2, v130
	v_max3_f32 v131, v131, |v35|, |v39|
	v_max3_f32 v129, v129, |v97|, |v101|
	ds_bpermute_b32 v137, v130, v128
	v_max3_f32 v131, v131, |v43|, |v47|
	v_max3_f32 v129, v129, |v105|, |v109|
	v_xor_b32_e32 v136, 16, v166
	v_max3_f32 v131, v131, |v51|, |v55|
	v_max3_f32 v129, v129, |v113|, |v117|
	v_cmp_lt_i32_e32 vcc, v136, v135
	v_xor_b32_e32 v183, 32, v166
	v_max3_f32 v131, v131, |v59|, |v63|
	v_max3_f32 v129, v129, |v121|, |v125|
	v_cndmask_b32_e32 v136, v166, v136, vcc
	v_cmp_lt_i32_e32 vcc, v183, v135
	v_max3_f32 v131, v131, |v67|, |v71|
	v_max3_f32 v131, v131, |v75|, |v79|
	v_cndmask_b32_e32 v135, v166, v183, vcc
	ds_bpermute_b32 v183, v130, v129
	s_waitcnt lgkmcnt(0)
	v_max_f32_e32 v137, v137, v137
	v_max3_f32 v131, v131, |v83|, |v87|
	v_lshlrev_b32_e32 v136, 2, v136
	v_max_f32_e32 v128, v128, v137
	v_max3_f32 v131, v131, |v91|, |v95|
	ds_bpermute_b32 v137, v136, v128
	v_max3_f32 v131, v131, |v99|, |v103|
	v_max3_f32 v131, v131, |v107|, |v111|
	v_lshlrev_b32_e32 v184, 2, v135
	s_waitcnt lgkmcnt(1)
	v_max_f32_e32 v135, v183, v183
	v_max3_f32 v131, v131, |v115|, |v119|
	v_max_f32_e32 v135, v129, v135
	v_max3_f32 v131, v131, |v123|, |v127|
	ds_bpermute_b32 v183, v136, v135
	s_waitcnt lgkmcnt(1)
	v_max_f32_e32 v129, v137, v137
	ds_bpermute_b32 v137, v130, v134
	ds_bpermute_b32 v185, v130, v131
	v_max_f32_e32 v128, v128, v129
	s_waitcnt lgkmcnt(2)
	v_max_f32_e32 v183, v183, v183
	v_max_f32_e32 v130, v135, v183
	s_waitcnt lgkmcnt(1)
	v_max_f32_e32 v135, v137, v137
	s_waitcnt lgkmcnt(0)
	v_max_f32_e32 v137, v185, v185
	v_max_f32_e32 v134, v134, v135
	v_max_f32_e32 v137, v131, v137
	ds_bpermute_b32 v135, v136, v134
	ds_bpermute_b32 v136, v136, v137
	ds_bpermute_b32 v129, v184, v128
	ds_bpermute_b32 v131, v184, v130
	v_cvt_pk_bf16_f32 v181, v124, v125
	s_waitcnt lgkmcnt(3)
	v_max_f32_e32 v135, v135, v135
	s_waitcnt lgkmcnt(2)
	v_max_f32_e32 v136, v136, v136
	v_max_f32_e32 v134, v134, v135
	v_max_f32_e32 v136, v137, v136
	ds_bpermute_b32 v135, v184, v134
	ds_bpermute_b32 v137, v184, v136
	v_cvt_pk_bf16_f32 v182, v126, v127
	ds_write_b16 v180, v181
	ds_write_b16_d16_hi v180, v181 offset:4112
	ds_write_b16 v180, v182 offset:8224
	ds_write_b16_d16_hi v180, v182 offset:12336
	s_and_saveexec_b64 s[8:9], s[4:5]
	s_cbranch_execz .LBB0_1275
; #define LAS __attribute__((address_space(3)))
; __device__ __forceinline__ void do_slabs_impl(LAS unsigned char* lds, unsigned char* ws, const float* w_up, const float* w_dn, const float* w_in, int vcu, int G, int wave, int j0, int j1) {
;     ...
;             if (lane < 8) { LAS float* d = red + wave * 32 + c4; d[0] = mx[0]; d[1] = mx[1]; d[2] = mx[2]; d[3] = mx[3]; }
	s_waitcnt lgkmcnt(4)
	v_max_f32_e32 v137, v137, v137
	v_max_f32_e32 v136, v136, v136
	v_max_f32_e32 v135, v135, v135
	v_max_f32_e32 v134, v134, v134
	v_max_f32_e32 v131, v131, v131
	v_max_f32_e32 v130, v130, v130
	v_max_f32_e32 v129, v129, v129
	v_max_f32_e32 v128, v128, v128
	v_max_f32_e32 v137, v136, v137
	v_max_f32_e32 v136, v134, v135
	v_max_f32_e32 v135, v130, v131
	v_max_f32_e32 v134, v128, v129
	ds_write_b128 v140, v[134:137]

; __device__ __forceinline__ unsigned cvt_pk_bf16(float lo, float hi) { unsigned r; asm volatile("v_cvt_pk_bf16_f32 %0, %1, %2" : "=v"(r) : "v"(lo), "v"(hi)); return r; }
; __device__ __forceinline__ void do_slabs_impl(LAS unsigned char* lds, unsigned char* ws, const float* w_up, const float* w_dn, const float* w_in, int vcu, int G, int wave, int j0, int j1) {
;     ...
;         if (cur.valid) {
;             f32x4 mx = (f32x4){0.f, 0.f, 0.f, 0.f};
; #pragma unroll
;             for (int i = 0; i < 32; ++i) { const int k = wave * 256 + i * 8 + kq; const f32x4 x = v[i];
;                 mx[0] = fmaxf(mx[0], fabsf(x[0])); mx[1] = fmaxf(mx[1], fabsf(x[1])); mx[2] = fmaxf(mx[2], fabsf(x[2])); mx[3] = fmaxf(mx[3], fabsf(x[3]));
;                 const unsigned p01 = cvt_pk_bf16(x[0], x[1]), p23 = cvt_pk_bf16(x[2], x[3]);
;                 const int ks = k ^ (((c4 >> 3) & 3) << 3);
;                 slab[(c4 + 0) * PITCH + ks] = (bf16)(p01 & 0xffffu); slab[(c4 + 1) * PITCH + ks] = (bf16)(p01 >> 16); slab[(c4 + 2) * PITCH + ks] = (bf16)(p23 & 0xffffu); slab[(c4 + 3) * PITCH + ks] = (bf16)(p23 >> 16); }
.LBB0_1354:
	s_cmp_lg_u32 s23, 0
	s_cselect_b64 s[36:37], -1, 0
	s_cmp_eq_u32 s23, 0
	s_cbranch_scc1 .LBB0_1358
	s_waitcnt vmcnt(31)
	v_cvt_pk_bf16_f32 v128, v0, v1
	v_cvt_pk_bf16_f32 v129, v2, v3
	ds_write_b16 v144, v128
	ds_write_b16_d16_hi v144, v128 offset:4112
	ds_write_b16 v144, v129 offset:8224
	ds_write_b16_d16_hi v144, v129 offset:12336
	s_waitcnt vmcnt(30)
	v_cvt_pk_bf16_f32 v136, v4, v5
	v_cvt_pk_bf16_f32 v137, v6, v7
	ds_write_b16 v145, v136
	ds_write_b16_d16_hi v145, v136 offset:4112
	ds_write_b16 v145, v137 offset:8224
	ds_write_b16_d16_hi v145, v137 offset:12336
	s_waitcnt vmcnt(29)
	v_cvt_pk_bf16_f32 v136, v8, v9
	v_cvt_pk_bf16_f32 v137, v10, v11
	ds_write_b16 v146, v136
	ds_write_b16_d16_hi v146, v136 offset:4112
	ds_write_b16 v146, v137 offset:8224
	ds_write_b16_d16_hi v146, v137 offset:12336
	s_waitcnt vmcnt(28)
	v_cvt_pk_bf16_f32 v136, v12, v13
	v_cvt_pk_bf16_f32 v137, v14, v15
	ds_write_b16 v147, v136
	ds_write_b16_d16_hi v147, v136 offset:4112
	ds_write_b16 v147, v137 offset:8224
	ds_write_b16_d16_hi v147, v137 offset:12336
	s_waitcnt vmcnt(27)
	v_cvt_pk_bf16_f32 v136, v16, v17
	v_cvt_pk_bf16_f32 v137, v18, v19
	ds_write_b16 v148, v136
	ds_write_b16_d16_hi v148, v136 offset:4112
	ds_write_b16 v148, v137 offset:8224
	ds_write_b16_d16_hi v148, v137 offset:12336
	s_waitcnt vmcnt(26)
	v_cvt_pk_bf16_f32 v136, v20, v21
	v_cvt_pk_bf16_f32 v137, v22, v23
	ds_write_b16 v149, v136
	ds_write_b16_d16_hi v149, v136 offset:4112
	ds_write_b16 v149, v137 offset:8224
	ds_write_b16_d16_hi v149, v137 offset:12336
	s_waitcnt vmcnt(25)
	v_cvt_pk_bf16_f32 v136, v24, v25
	v_cvt_pk_bf16_f32 v137, v26, v27
	ds_write_b16 v150, v136
	ds_write_b16_d16_hi v150, v136 offset:4112
	ds_write_b16 v150, v137 offset:8224
	ds_write_b16_d16_hi v150, v137 offset:12336
	s_waitcnt vmcnt(24)
	v_cvt_pk_bf16_f32 v136, v28, v29
	v_cvt_pk_bf16_f32 v137, v30, v31
	ds_write_b16 v151, v136
	ds_write_b16_d16_hi v151, v136 offset:4112
	ds_write_b16 v151, v137 offset:8224
	ds_write_b16_d16_hi v151, v137 offset:12336
	s_waitcnt vmcnt(23)
	v_cvt_pk_bf16_f32 v136, v32, v33
	v_cvt_pk_bf16_f32 v137, v34, v35
	ds_write_b16 v152, v136
	ds_write_b16_d16_hi v152, v136 offset:4112
	ds_write_b16 v152, v137 offset:8224
	ds_write_b16_d16_hi v152, v137 offset:12336
	s_waitcnt vmcnt(22)
	v_cvt_pk_bf16_f32 v136, v36, v37
	v_cvt_pk_bf16_f32 v137, v38, v39
	ds_write_b16 v153, v136
	ds_write_b16_d16_hi v153, v136 offset:4112
	ds_write_b16 v153, v137 offset:8224
	ds_write_b16_d16_hi v153, v137 offset:12336
	s_waitcnt vmcnt(21)
	v_cvt_pk_bf16_f32 v136, v40, v41
	v_cvt_pk_bf16_f32 v137, v42, v43
	ds_write_b16 v154, v136
	ds_write_b16_d16_hi v154, v136 offset:4112
	ds_write_b16 v154, v137 offset:8224
	ds_write_b16_d16_hi v154, v137 offset:12336
	s_waitcnt vmcnt(20)
	v_cvt_pk_bf16_f32 v136, v44, v45
	v_cvt_pk_bf16_f32 v137, v46, v47
	ds_write_b16 v155, v136
	ds_write_b16_d16_hi v155, v136 offset:4112
	ds_write_b16 v155, v137 offset:8224
	ds_write_b16_d16_hi v155, v137 offset:12336
	s_waitcnt vmcnt(19)
	v_cvt_pk_bf16_f32 v136, v48, v49
	v_cvt_pk_bf16_f32 v137, v50, v51
	ds_write_b16 v156, v136
	ds_write_b16_d16_hi v156, v136 offset:4112
	ds_write_b16 v156, v137 offset:8224
	ds_write_b16_d16_hi v156, v137 offset:12336
	s_waitcnt vmcnt(18)
	v_cvt_pk_bf16_f32 v136, v52, v53
	v_cvt_pk_bf16_f32 v137, v54, v55
	ds_write_b16 v157, v136
	ds_write_b16_d16_hi v157, v136 offset:4112
	ds_write_b16 v157, v137 offset:8224
	ds_write_b16_d16_hi v157, v137 offset:12336
	s_waitcnt vmcnt(17)
	v_cvt_pk_bf16_f32 v136, v56, v57
	v_cvt_pk_bf16_f32 v137, v58, v59
	ds_write_b16 v158, v136
	ds_write_b16_d16_hi v158, v136 offset:4112
	ds_write_b16 v158, v137 offset:8224
	ds_write_b16_d16_hi v158, v137 offset:12336
	s_waitcnt vmcnt(16)
	v_cvt_pk_bf16_f32 v136, v60, v61
	v_cvt_pk_bf16_f32 v137, v62, v63
	ds_write_b16 v159, v136
	ds_write_b16_d16_hi v159, v136 offset:4112
	ds_write_b16 v159, v137 offset:8224
	ds_write_b16_d16_hi v159, v137 offset:12336
	s_waitcnt vmcnt(15)
	v_cvt_pk_bf16_f32 v136, v64, v65
	v_cvt_pk_bf16_f32 v137, v66, v67
	v_max3_f32 v130, |v2|, 0, |v6|
	ds_write_b16 v160, v136
	ds_write_b16_d16_hi v160, v136 offset:4112
	ds_write_b16 v160, v137 offset:8224
	ds_write_b16_d16_hi v160, v137 offset:12336
	s_waitcnt vmcnt(14)
	v_cvt_pk_bf16_f32 v136, v68, v69
	v_cvt_pk_bf16_f32 v137, v70, v71
	v_max3_f32 v130, v130, |v10|, |v14|
	ds_write_b16 v161, v136
	ds_write_b16_d16_hi v161, v136 offset:4112
	ds_write_b16 v161, v137 offset:8224
	ds_write_b16_d16_hi v161, v137 offset:12336
	s_waitcnt vmcnt(13)
	v_cvt_pk_bf16_f32 v136, v72, v73
	v_cvt_pk_bf16_f32 v137, v74, v75
	v_max3_f32 v130, v130, |v18|, |v22|
	ds_write_b16 v162, v136
	ds_write_b16_d16_hi v162, v136 offset:4112
	ds_write_b16 v162, v137 offset:8224
	ds_write_b16_d16_hi v162, v137 offset:12336
	s_waitcnt vmcnt(12)
	v_cvt_pk_bf16_f32 v136, v76, v77
	v_cvt_pk_bf16_f32 v137, v78, v79
	v_max3_f32 v128, |v0|, 0, |v4|
	v_max3_f32 v130, v130, |v26|, |v30|
	ds_write_b16 v163, v136
	ds_write_b16_d16_hi v163, v136 offset:4112
	ds_write_b16 v163, v137 offset:8224
	ds_write_b16_d16_hi v163, v137 offset:12336
	s_waitcnt vmcnt(11)
	v_cvt_pk_bf16_f32 v136, v80, v81
	v_cvt_pk_bf16_f32 v137, v82, v83
	v_max3_f32 v128, v128, |v8|, |v12|
	v_max3_f32 v130, v130, |v34|, |v38|
	ds_write_b16 v164, v136
	ds_write_b16_d16_hi v164, v136 offset:4112
	ds_write_b16 v164, v137 offset:8224
	ds_write_b16_d16_hi v164, v137 offset:12336
	s_waitcnt vmcnt(10)
	v_cvt_pk_bf16_f32 v136, v84, v85
	v_cvt_pk_bf16_f32 v137, v86, v87
	v_max3_f32 v128, v128, |v16|, |v20|
	v_max3_f32 v130, v130, |v42|, |v46|
	ds_write_b16 v165, v136
	ds_write_b16_d16_hi v165, v136 offset:4112
	ds_write_b16 v165, v137 offset:8224
	ds_write_b16_d16_hi v165, v137 offset:12336
	s_waitcnt vmcnt(9)
; #define LAS __attribute__((address_space(3)))
; __device__ __forceinline__ unsigned cvt_pk_bf16(float lo, float hi) { unsigned r; asm volatile("v_cvt_pk_bf16_f32 %0, %1, %2" : "=v"(r) : "v"(lo), "v"(hi)); return r; }
; __device__ __forceinline__ void do_slabs_impl(LAS unsigned char* lds, unsigned char* ws, const float* w_up, const float* w_dn, const float* w_in, int vcu, int G, int wave, int j0, int j1) {
;     ...
;         if (cur.valid) {
;             f32x4 mx = (f32x4){0.f, 0.f, 0.f, 0.f};
; #pragma unroll
;             for (int i = 0; i < 32; ++i) { const int k = wave * 256 + i * 8 + kq; const f32x4 x = v[i];
;                 mx[0] = fmaxf(mx[0], fabsf(x[0])); mx[1] = fmaxf(mx[1], fabsf(x[1])); mx[2] = fmaxf(mx[2], fabsf(x[2])); mx[3] = fmaxf(mx[3], fabsf(x[3]));
;                 const unsigned p01 = cvt_pk_bf16(x[0], x[1]), p23 = cvt_pk_bf16(x[2], x[3]);
;                 const int ks = k ^ (((c4 >> 3) & 3) << 3);
;                 slab[(c4 + 0) * PITCH + ks] = (bf16)(p01 & 0xffffu); slab[(c4 + 1) * PITCH + ks] = (bf16)(p01 >> 16); slab[(c4 + 2) * PITCH + ks] = (bf16)(p23 & 0xffffu); slab[(c4 + 3) * PITCH + ks] = (bf16)(p23 >> 16); }
; #pragma unroll
;             for (int q = 0; q < 4; ++q) { float m = mx[q]; m = fmaxf(m, __shfl_xor(m, 8)); m = fmaxf(m, __shfl_xor(m, 16)); m = fmaxf(m, __shfl_xor(m, 32)); mx[q] = m; }
;             if (lane < 8) { LAS float* d = red + wave * 32 + c4; d[0] = mx[0]; d[1] = mx[1]; d[2] = mx[2]; d[3] = mx[3]; }
	v_cvt_pk_bf16_f32 v136, v88, v89
	v_cvt_pk_bf16_f32 v137, v90, v91
	v_max3_f32 v128, v128, |v24|, |v28|
	v_max3_f32 v130, v130, |v50|, |v54|
	ds_write_b16 v167, v136
	ds_write_b16_d16_hi v167, v136 offset:4112
	ds_write_b16 v167, v137 offset:8224
	ds_write_b16_d16_hi v167, v137 offset:12336
	s_waitcnt vmcnt(8)
	v_cvt_pk_bf16_f32 v136, v92, v93
	v_cvt_pk_bf16_f32 v137, v94, v95
	v_max3_f32 v129, |v1|, 0, |v5|
	v_max3_f32 v128, v128, |v32|, |v36|
	v_max3_f32 v130, v130, |v58|, |v62|
	ds_write_b16 v168, v136
	ds_write_b16_d16_hi v168, v136 offset:4112
	ds_write_b16 v168, v137 offset:8224
	ds_write_b16_d16_hi v168, v137 offset:12336
	s_waitcnt vmcnt(7)
	v_cvt_pk_bf16_f32 v136, v96, v97
	v_cvt_pk_bf16_f32 v137, v98, v99
	v_max3_f32 v129, v129, |v9|, |v13|
	v_max3_f32 v128, v128, |v40|, |v44|
	v_max3_f32 v130, v130, |v66|, |v70|
	ds_write_b16 v169, v136
	ds_write_b16_d16_hi v169, v136 offset:4112
	ds_write_b16 v169, v137 offset:8224
	ds_write_b16_d16_hi v169, v137 offset:12336
	s_waitcnt vmcnt(6)
	v_cvt_pk_bf16_f32 v136, v100, v101
	v_cvt_pk_bf16_f32 v137, v102, v103
	v_max3_f32 v129, v129, |v17|, |v21|
	v_max3_f32 v128, v128, |v48|, |v52|
	v_max3_f32 v130, v130, |v74|, |v78|
	ds_write_b16 v170, v136
	ds_write_b16_d16_hi v170, v136 offset:4112
	ds_write_b16 v170, v137 offset:8224
	ds_write_b16_d16_hi v170, v137 offset:12336
	s_waitcnt vmcnt(5)
	v_cvt_pk_bf16_f32 v136, v104, v105
	v_cvt_pk_bf16_f32 v137, v106, v107
	v_max3_f32 v129, v129, |v25|, |v29|
	v_max3_f32 v128, v128, |v56|, |v60|
	v_max3_f32 v130, v130, |v82|, |v86|
	ds_write_b16 v171, v136
	ds_write_b16_d16_hi v171, v136 offset:4112
	ds_write_b16 v171, v137 offset:8224
	ds_write_b16_d16_hi v171, v137 offset:12336
	s_waitcnt vmcnt(4)
	v_cvt_pk_bf16_f32 v136, v108, v109
	v_cvt_pk_bf16_f32 v137, v110, v111
	v_max3_f32 v129, v129, |v33|, |v37|
	v_max3_f32 v128, v128, |v64|, |v68|
	v_max3_f32 v130, v130, |v90|, |v94|
	ds_write_b16 v172, v136
	ds_write_b16_d16_hi v172, v136 offset:4112
	ds_write_b16 v172, v137 offset:8224
	ds_write_b16_d16_hi v172, v137 offset:12336
	s_waitcnt vmcnt(3)
	v_cvt_pk_bf16_f32 v136, v112, v113
	v_cvt_pk_bf16_f32 v137, v114, v115
	v_max3_f32 v129, v129, |v41|, |v45|
	v_max3_f32 v128, v128, |v72|, |v76|
	v_max3_f32 v130, v130, |v98|, |v102|
	ds_write_b16 v173, v136
	ds_write_b16_d16_hi v173, v136 offset:4112
	ds_write_b16 v173, v137 offset:8224
	ds_write_b16_d16_hi v173, v137 offset:12336
	s_waitcnt vmcnt(2)
	v_cvt_pk_bf16_f32 v136, v116, v117
	v_cvt_pk_bf16_f32 v137, v118, v119
	v_max3_f32 v129, v129, |v49|, |v53|
	v_max3_f32 v128, v128, |v80|, |v84|
	v_max3_f32 v130, v130, |v106|, |v110|
	ds_write_b16 v174, v136
	ds_write_b16_d16_hi v174, v136 offset:4112
	ds_write_b16 v174, v137 offset:8224
	ds_write_b16_d16_hi v174, v137 offset:12336
	s_waitcnt vmcnt(1)
	v_cvt_pk_bf16_f32 v136, v120, v121
	v_cvt_pk_bf16_f32 v137, v122, v123
	v_max3_f32 v129, v129, |v57|, |v61|
	v_max3_f32 v128, v128, |v88|, |v92|
	v_max3_f32 v130, v130, |v114|, |v118|
	ds_write_b16 v175, v136
	ds_write_b16_d16_hi v175, v136 offset:4112
	ds_write_b16 v175, v137 offset:8224
	ds_write_b16_d16_hi v175, v137 offset:12336
	v_and_b32_e32 v137, 64, v166
	v_max3_f32 v131, |v3|, 0, |v7|
	v_max3_f32 v129, v129, |v65|, |v69|
	v_max3_f32 v128, v128, |v96|, |v100|
	s_waitcnt vmcnt(0)
	v_max3_f32 v136, v130, |v122|, |v126|
	v_xor_b32_e32 v130, 8, v166
	v_add_u32_e32 v137, 64, v137
	v_max3_f32 v131, v131, |v11|, |v15|
	v_max3_f32 v129, v129, |v73|, |v77|
	v_max3_f32 v128, v128, |v104|, |v108|
	v_cmp_lt_i32_e32 vcc, v130, v137
	v_max3_f32 v131, v131, |v19|, |v23|
	v_max3_f32 v129, v129, |v81|, |v85|
	v_max3_f32 v128, v128, |v112|, |v116|
	v_cndmask_b32_e32 v130, v166, v130, vcc
	v_max3_f32 v131, v131, |v27|, |v31|
	v_max3_f32 v129, v129, |v89|, |v93|
	v_max3_f32 v128, v128, |v120|, |v124|
	v_lshlrev_b32_e32 v130, 2, v130
	v_max3_f32 v131, v131, |v35|, |v39|
	v_max3_f32 v129, v129, |v97|, |v101|
	ds_bpermute_b32 v139, v130, v128
	v_max3_f32 v131, v131, |v43|, |v47|
	v_max3_f32 v129, v129, |v105|, |v109|
	v_xor_b32_e32 v138, 16, v166
	v_max3_f32 v131, v131, |v51|, |v55|
	v_max3_f32 v129, v129, |v113|, |v117|
	v_cmp_lt_i32_e32 vcc, v138, v137
	v_xor_b32_e32 v182, 32, v166
	v_max3_f32 v131, v131, |v59|, |v63|
	v_max3_f32 v129, v129, |v121|, |v125|
	v_cndmask_b32_e32 v138, v166, v138, vcc
	v_cmp_lt_i32_e32 vcc, v182, v137
	v_max3_f32 v131, v131, |v67|, |v71|
	v_max3_f32 v131, v131, |v75|, |v79|
	v_cndmask_b32_e32 v137, v166, v182, vcc
	ds_bpermute_b32 v182, v130, v129
	s_waitcnt lgkmcnt(0)
	v_max_f32_e32 v139, v139, v139
	v_max3_f32 v131, v131, |v83|, |v87|
	v_lshlrev_b32_e32 v138, 2, v138
	v_max_f32_e32 v128, v128, v139
	v_max3_f32 v131, v131, |v91|, |v95|
	ds_bpermute_b32 v139, v138, v128
	v_max3_f32 v131, v131, |v99|, |v103|
	v_max3_f32 v131, v131, |v107|, |v111|
	v_lshlrev_b32_e32 v183, 2, v137
	v_max_f32_e32 v137, v182, v182
	v_max3_f32 v131, v131, |v115|, |v119|
	v_max_f32_e32 v137, v129, v137
	v_max3_f32 v131, v131, |v123|, |v127|
	ds_bpermute_b32 v182, v138, v137
	s_waitcnt lgkmcnt(1)
	v_max_f32_e32 v129, v139, v139
	ds_bpermute_b32 v139, v130, v136
	ds_bpermute_b32 v184, v130, v131
	v_max_f32_e32 v128, v128, v129
	s_waitcnt lgkmcnt(2)
	v_max_f32_e32 v182, v182, v182
	v_max_f32_e32 v130, v137, v182
	s_waitcnt lgkmcnt(1)
	v_max_f32_e32 v137, v139, v139
	s_waitcnt lgkmcnt(0)
	v_max_f32_e32 v139, v184, v184
	v_max_f32_e32 v136, v136, v137
	v_max_f32_e32 v139, v131, v139
	ds_bpermute_b32 v137, v138, v136
	ds_bpermute_b32 v138, v138, v139
	ds_bpermute_b32 v129, v183, v128
	ds_bpermute_b32 v131, v183, v130
	v_cvt_pk_bf16_f32 v180, v124, v125
	s_waitcnt lgkmcnt(3)
	v_max_f32_e32 v137, v137, v137
	s_waitcnt lgkmcnt(2)
	v_max_f32_e32 v138, v138, v138
	v_max_f32_e32 v136, v136, v137
	v_max_f32_e32 v138, v139, v138
	ds_bpermute_b32 v137, v183, v136
	ds_bpermute_b32 v139, v183, v138
	v_cvt_pk_bf16_f32 v181, v126, v127
	ds_write_b16 v176, v180
	ds_write_b16_d16_hi v176, v180 offset:4112
	ds_write_b16 v176, v181 offset:8224
	ds_write_b16_d16_hi v176, v181 offset:12336
	s_and_saveexec_b64 s[38:39], s[4:5]
	s_cbranch_execz .LBB0_1357
	s_waitcnt lgkmcnt(4)
	v_max_f32_e32 v139, v139, v139
	v_max_f32_e32 v138, v138, v138
	v_max_f32_e32 v137, v137, v137
	v_max_f32_e32 v136, v136, v136
	v_max_f32_e32 v131, v131, v131
	v_max_f32_e32 v130, v130, v130
	v_max_f32_e32 v129, v129, v129
	v_max_f32_e32 v128, v128, v128
	v_max_f32_e32 v139, v138, v139
	v_max_f32_e32 v138, v136, v137
	v_max_f32_e32 v137, v130, v131
	v_max_f32_e32 v136, v128, v129
	ds_write_b128 v177, v[136:139]

; __device__ __forceinline__ unsigned cvt_pk_bf16(float lo, float hi) { unsigned r; asm volatile("v_cvt_pk_bf16_f32 %0, %1, %2" : "=v"(r) : "v"(lo), "v"(hi)); return r; }
; __device__ __forceinline__ void do_slabs_impl(LAS unsigned char* lds, unsigned char* ws, const float* w_up, const float* w_dn, const float* w_in, int vcu, int G, int wave, int j0, int j1) {
;     ...
;         if (cur.valid) {
;             f32x4 mx = (f32x4){0.f, 0.f, 0.f, 0.f};
; #pragma unroll
;             for (int i = 0; i < 32; ++i) { const int k = wave * 256 + i * 8 + kq; const f32x4 x = v[i];
;                 mx[0] = fmaxf(mx[0], fabsf(x[0])); mx[1] = fmaxf(mx[1], fabsf(x[1])); mx[2] = fmaxf(mx[2], fabsf(x[2])); mx[3] = fmaxf(mx[3], fabsf(x[3]));
;                 const unsigned p01 = cvt_pk_bf16(x[0], x[1]), p23 = cvt_pk_bf16(x[2], x[3]);
;                 const int ks = k ^ (((c4 >> 3) & 3) << 3);
;                 slab[(c4 + 0) * PITCH + ks] = (bf16)(p01 & 0xffffu); slab[(c4 + 1) * PITCH + ks] = (bf16)(p01 >> 16); slab[(c4 + 2) * PITCH + ks] = (bf16)(p23 & 0xffffu); slab[(c4 + 3) * PITCH + ks] = (bf16)(p23 >> 16); }
.LBB0_1403:
	s_cmp_lg_u32 s27, 0
	s_cselect_b64 s[36:37], -1, 0
	s_cmp_eq_u32 s27, 0
	s_cbranch_scc1 .LBB0_1407
	s_waitcnt vmcnt(31)
	v_cvt_pk_bf16_f32 v128, v0, v1
	v_cvt_pk_bf16_f32 v129, v2, v3
	ds_write_b16 v144, v128
	ds_write_b16_d16_hi v144, v128 offset:4112
	ds_write_b16 v144, v129 offset:8224
	ds_write_b16_d16_hi v144, v129 offset:12336
	s_waitcnt vmcnt(30)
	v_cvt_pk_bf16_f32 v136, v4, v5
	v_cvt_pk_bf16_f32 v137, v6, v7
	ds_write_b16 v145, v136
	ds_write_b16_d16_hi v145, v136 offset:4112
	ds_write_b16 v145, v137 offset:8224
	ds_write_b16_d16_hi v145, v137 offset:12336
	s_waitcnt vmcnt(29)
	v_cvt_pk_bf16_f32 v136, v8, v9
	v_cvt_pk_bf16_f32 v137, v10, v11
	ds_write_b16 v146, v136
	ds_write_b16_d16_hi v146, v136 offset:4112
	ds_write_b16 v146, v137 offset:8224
	ds_write_b16_d16_hi v146, v137 offset:12336
	s_waitcnt vmcnt(28)
	v_cvt_pk_bf16_f32 v136, v12, v13
	v_cvt_pk_bf16_f32 v137, v14, v15
	ds_write_b16 v147, v136
	ds_write_b16_d16_hi v147, v136 offset:4112
	ds_write_b16 v147, v137 offset:8224
	ds_write_b16_d16_hi v147, v137 offset:12336
	s_waitcnt vmcnt(27)
	v_cvt_pk_bf16_f32 v136, v16, v17
	v_cvt_pk_bf16_f32 v137, v18, v19
	ds_write_b16 v148, v136
	ds_write_b16_d16_hi v148, v136 offset:4112
	ds_write_b16 v148, v137 offset:8224
	ds_write_b16_d16_hi v148, v137 offset:12336
	s_waitcnt vmcnt(26)
	v_cvt_pk_bf16_f32 v136, v20, v21
	v_cvt_pk_bf16_f32 v137, v22, v23
	ds_write_b16 v149, v136
	ds_write_b16_d16_hi v149, v136 offset:4112
	ds_write_b16 v149, v137 offset:8224
	ds_write_b16_d16_hi v149, v137 offset:12336
	s_waitcnt vmcnt(25)
	v_cvt_pk_bf16_f32 v136, v24, v25
	v_cvt_pk_bf16_f32 v137, v26, v27
	ds_write_b16 v150, v136
	ds_write_b16_d16_hi v150, v136 offset:4112
	ds_write_b16 v150, v137 offset:8224
	ds_write_b16_d16_hi v150, v137 offset:12336
	s_waitcnt vmcnt(24)
	v_cvt_pk_bf16_f32 v136, v28, v29
	v_cvt_pk_bf16_f32 v137, v30, v31
	ds_write_b16 v151, v136
	ds_write_b16_d16_hi v151, v136 offset:4112
	ds_write_b16 v151, v137 offset:8224
	ds_write_b16_d16_hi v151, v137 offset:12336
	s_waitcnt vmcnt(23)
	v_cvt_pk_bf16_f32 v136, v32, v33
	v_cvt_pk_bf16_f32 v137, v34, v35
	ds_write_b16 v152, v136
	ds_write_b16_d16_hi v152, v136 offset:4112
	ds_write_b16 v152, v137 offset:8224
	ds_write_b16_d16_hi v152, v137 offset:12336
	s_waitcnt vmcnt(22)
	v_cvt_pk_bf16_f32 v136, v36, v37
	v_cvt_pk_bf16_f32 v137, v38, v39
	ds_write_b16 v153, v136
	ds_write_b16_d16_hi v153, v136 offset:4112
	ds_write_b16 v153, v137 offset:8224
	ds_write_b16_d16_hi v153, v137 offset:12336
	s_waitcnt vmcnt(21)
	v_cvt_pk_bf16_f32 v136, v40, v41
	v_cvt_pk_bf16_f32 v137, v42, v43
	ds_write_b16 v154, v136
	ds_write_b16_d16_hi v154, v136 offset:4112
	ds_write_b16 v154, v137 offset:8224
	ds_write_b16_d16_hi v154, v137 offset:12336
	s_waitcnt vmcnt(20)
	v_cvt_pk_bf16_f32 v136, v44, v45
	v_cvt_pk_bf16_f32 v137, v46, v47
	ds_write_b16 v155, v136
	ds_write_b16_d16_hi v155, v136 offset:4112
	ds_write_b16 v155, v137 offset:8224
	ds_write_b16_d16_hi v155, v137 offset:12336
	s_waitcnt vmcnt(19)
	v_cvt_pk_bf16_f32 v136, v48, v49
	v_cvt_pk_bf16_f32 v137, v50, v51
	ds_write_b16 v156, v136
	ds_write_b16_d16_hi v156, v136 offset:4112
	ds_write_b16 v156, v137 offset:8224
	ds_write_b16_d16_hi v156, v137 offset:12336
	s_waitcnt vmcnt(18)
	v_cvt_pk_bf16_f32 v136, v52, v53
	v_cvt_pk_bf16_f32 v137, v54, v55
	ds_write_b16 v157, v136
	ds_write_b16_d16_hi v157, v136 offset:4112
	ds_write_b16 v157, v137 offset:8224
	ds_write_b16_d16_hi v157, v137 offset:12336
	s_waitcnt vmcnt(17)
	v_cvt_pk_bf16_f32 v136, v56, v57
	v_cvt_pk_bf16_f32 v137, v58, v59
	ds_write_b16 v158, v136
	ds_write_b16_d16_hi v158, v136 offset:4112
	ds_write_b16 v158, v137 offset:8224
	ds_write_b16_d16_hi v158, v137 offset:12336
	s_waitcnt vmcnt(16)
	v_cvt_pk_bf16_f32 v136, v60, v61
	v_cvt_pk_bf16_f32 v137, v62, v63
	ds_write_b16 v159, v136
	ds_write_b16_d16_hi v159, v136 offset:4112
	ds_write_b16 v159, v137 offset:8224
	ds_write_b16_d16_hi v159, v137 offset:12336
	s_waitcnt vmcnt(15)
	v_cvt_pk_bf16_f32 v136, v64, v65
	v_cvt_pk_bf16_f32 v137, v66, v67
	v_max3_f32 v130, |v2|, 0, |v6|
	ds_write_b16 v160, v136
	ds_write_b16_d16_hi v160, v136 offset:4112
	ds_write_b16 v160, v137 offset:8224
	ds_write_b16_d16_hi v160, v137 offset:12336
	s_waitcnt vmcnt(14)
	v_cvt_pk_bf16_f32 v136, v68, v69
	v_cvt_pk_bf16_f32 v137, v70, v71
	v_max3_f32 v130, v130, |v10|, |v14|
	ds_write_b16 v161, v136
	ds_write_b16_d16_hi v161, v136 offset:4112
	ds_write_b16 v161, v137 offset:8224
	ds_write_b16_d16_hi v161, v137 offset:12336
	s_waitcnt vmcnt(13)
	v_cvt_pk_bf16_f32 v136, v72, v73
	v_cvt_pk_bf16_f32 v137, v74, v75
	v_max3_f32 v130, v130, |v18|, |v22|
	ds_write_b16 v162, v136
	ds_write_b16_d16_hi v162, v136 offset:4112
	ds_write_b16 v162, v137 offset:8224
	ds_write_b16_d16_hi v162, v137 offset:12336
	s_waitcnt vmcnt(12)
	v_cvt_pk_bf16_f32 v136, v76, v77
	v_cvt_pk_bf16_f32 v137, v78, v79
	v_max3_f32 v128, |v0|, 0, |v4|
	v_max3_f32 v130, v130, |v26|, |v30|
	ds_write_b16 v163, v136
	ds_write_b16_d16_hi v163, v136 offset:4112
	ds_write_b16 v163, v137 offset:8224
	ds_write_b16_d16_hi v163, v137 offset:12336
	s_waitcnt vmcnt(11)
	v_cvt_pk_bf16_f32 v136, v80, v81
	v_cvt_pk_bf16_f32 v137, v82, v83
	v_max3_f32 v128, v128, |v8|, |v12|
	v_max3_f32 v130, v130, |v34|, |v38|
	ds_write_b16 v164, v136
	ds_write_b16_d16_hi v164, v136 offset:4112
	ds_write_b16 v164, v137 offset:8224
	ds_write_b16_d16_hi v164, v137 offset:12336
	s_waitcnt vmcnt(10)
	v_cvt_pk_bf16_f32 v136, v84, v85
	v_cvt_pk_bf16_f32 v137, v86, v87
	v_max3_f32 v128, v128, |v16|, |v20|
	v_max3_f32 v130, v130, |v42|, |v46|
	ds_write_b16 v165, v136
	ds_write_b16_d16_hi v165, v136 offset:4112
	ds_write_b16 v165, v137 offset:8224
	ds_write_b16_d16_hi v165, v137 offset:12336
	s_waitcnt vmcnt(9)
; #define LAS __attribute__((address_space(3)))
; __device__ __forceinline__ unsigned cvt_pk_bf16(float lo, float hi) { unsigned r; asm volatile("v_cvt_pk_bf16_f32 %0, %1, %2" : "=v"(r) : "v"(lo), "v"(hi)); return r; }
; __device__ __forceinline__ void do_slabs_impl(LAS unsigned char* lds, unsigned char* ws, const float* w_up, const float* w_dn, const float* w_in, int vcu, int G, int wave, int j0, int j1) {
;     ...
;         if (cur.valid) {
;             f32x4 mx = (f32x4){0.f, 0.f, 0.f, 0.f};
; #pragma unroll
;             for (int i = 0; i < 32; ++i) { const int k = wave * 256 + i * 8 + kq; const f32x4 x = v[i];
;                 mx[0] = fmaxf(mx[0], fabsf(x[0])); mx[1] = fmaxf(mx[1], fabsf(x[1])); mx[2] = fmaxf(mx[2], fabsf(x[2])); mx[3] = fmaxf(mx[3], fabsf(x[3]));
;                 const unsigned p01 = cvt_pk_bf16(x[0], x[1]), p23 = cvt_pk_bf16(x[2], x[3]);
;                 const int ks = k ^ (((c4 >> 3) & 3) << 3);
;                 slab[(c4 + 0) * PITCH + ks] = (bf16)(p01 & 0xffffu); slab[(c4 + 1) * PITCH + ks] = (bf16)(p01 >> 16); slab[(c4 + 2) * PITCH + ks] = (bf16)(p23 & 0xffffu); slab[(c4 + 3) * PITCH + ks] = (bf16)(p23 >> 16); }
; #pragma unroll
;             for (int q = 0; q < 4; ++q) { float m = mx[q]; m = fmaxf(m, __shfl_xor(m, 8)); m = fmaxf(m, __shfl_xor(m, 16)); m = fmaxf(m, __shfl_xor(m, 32)); mx[q] = m; }
;             if (lane < 8) { LAS float* d = red + wave * 32 + c4; d[0] = mx[0]; d[1] = mx[1]; d[2] = mx[2]; d[3] = mx[3]; }
	v_cvt_pk_bf16_f32 v136, v88, v89
	v_cvt_pk_bf16_f32 v137, v90, v91
	v_max3_f32 v128, v128, |v24|, |v28|
	v_max3_f32 v130, v130, |v50|, |v54|
	ds_write_b16 v167, v136
	ds_write_b16_d16_hi v167, v136 offset:4112
	ds_write_b16 v167, v137 offset:8224
	ds_write_b16_d16_hi v167, v137 offset:12336
	s_waitcnt vmcnt(8)
	v_cvt_pk_bf16_f32 v136, v92, v93
	v_cvt_pk_bf16_f32 v137, v94, v95
	v_max3_f32 v129, |v1|, 0, |v5|
	v_max3_f32 v128, v128, |v32|, |v36|
	v_max3_f32 v130, v130, |v58|, |v62|
	ds_write_b16 v168, v136
	ds_write_b16_d16_hi v168, v136 offset:4112
	ds_write_b16 v168, v137 offset:8224
	ds_write_b16_d16_hi v168, v137 offset:12336
	s_waitcnt vmcnt(7)
	v_cvt_pk_bf16_f32 v136, v96, v97
	v_cvt_pk_bf16_f32 v137, v98, v99
	v_max3_f32 v129, v129, |v9|, |v13|
	v_max3_f32 v128, v128, |v40|, |v44|
	v_max3_f32 v130, v130, |v66|, |v70|
	ds_write_b16 v169, v136
	ds_write_b16_d16_hi v169, v136 offset:4112
	ds_write_b16 v169, v137 offset:8224
	ds_write_b16_d16_hi v169, v137 offset:12336
	s_waitcnt vmcnt(6)
	v_cvt_pk_bf16_f32 v136, v100, v101
	v_cvt_pk_bf16_f32 v137, v102, v103
	v_max3_f32 v129, v129, |v17|, |v21|
	v_max3_f32 v128, v128, |v48|, |v52|
	v_max3_f32 v130, v130, |v74|, |v78|
	ds_write_b16 v170, v136
	ds_write_b16_d16_hi v170, v136 offset:4112
	ds_write_b16 v170, v137 offset:8224
	ds_write_b16_d16_hi v170, v137 offset:12336
	s_waitcnt vmcnt(5)
	v_cvt_pk_bf16_f32 v136, v104, v105
	v_cvt_pk_bf16_f32 v137, v106, v107
	v_max3_f32 v129, v129, |v25|, |v29|
	v_max3_f32 v128, v128, |v56|, |v60|
	v_max3_f32 v130, v130, |v82|, |v86|
	ds_write_b16 v171, v136
	ds_write_b16_d16_hi v171, v136 offset:4112
	ds_write_b16 v171, v137 offset:8224
	ds_write_b16_d16_hi v171, v137 offset:12336
	s_waitcnt vmcnt(4)
	v_cvt_pk_bf16_f32 v136, v108, v109
	v_cvt_pk_bf16_f32 v137, v110, v111
	v_max3_f32 v129, v129, |v33|, |v37|
	v_max3_f32 v128, v128, |v64|, |v68|
	v_max3_f32 v130, v130, |v90|, |v94|
	ds_write_b16 v172, v136
	ds_write_b16_d16_hi v172, v136 offset:4112
	ds_write_b16 v172, v137 offset:8224
	ds_write_b16_d16_hi v172, v137 offset:12336
	s_waitcnt vmcnt(3)
	v_cvt_pk_bf16_f32 v136, v112, v113
	v_cvt_pk_bf16_f32 v137, v114, v115
	v_max3_f32 v129, v129, |v41|, |v45|
	v_max3_f32 v128, v128, |v72|, |v76|
	v_max3_f32 v130, v130, |v98|, |v102|
	ds_write_b16 v173, v136
	ds_write_b16_d16_hi v173, v136 offset:4112
	ds_write_b16 v173, v137 offset:8224
	ds_write_b16_d16_hi v173, v137 offset:12336
	s_waitcnt vmcnt(2)
	v_cvt_pk_bf16_f32 v136, v116, v117
	v_cvt_pk_bf16_f32 v137, v118, v119
	v_max3_f32 v129, v129, |v49|, |v53|
	v_max3_f32 v128, v128, |v80|, |v84|
	v_max3_f32 v130, v130, |v106|, |v110|
	ds_write_b16 v174, v136
	ds_write_b16_d16_hi v174, v136 offset:4112
	ds_write_b16 v174, v137 offset:8224
	ds_write_b16_d16_hi v174, v137 offset:12336
	s_waitcnt vmcnt(1)
	v_cvt_pk_bf16_f32 v136, v120, v121
	v_cvt_pk_bf16_f32 v137, v122, v123
	v_max3_f32 v129, v129, |v57|, |v61|
	v_max3_f32 v128, v128, |v88|, |v92|
	v_max3_f32 v130, v130, |v114|, |v118|
	ds_write_b16 v175, v136
	ds_write_b16_d16_hi v175, v136 offset:4112
	ds_write_b16 v175, v137 offset:8224
	ds_write_b16_d16_hi v175, v137 offset:12336
	v_and_b32_e32 v137, 64, v166
	v_max3_f32 v131, |v3|, 0, |v7|
	v_max3_f32 v129, v129, |v65|, |v69|
	v_max3_f32 v128, v128, |v96|, |v100|
	s_waitcnt vmcnt(0)
	v_max3_f32 v136, v130, |v122|, |v126|
	v_xor_b32_e32 v130, 8, v166
	v_add_u32_e32 v137, 64, v137
	v_max3_f32 v131, v131, |v11|, |v15|
	v_max3_f32 v129, v129, |v73|, |v77|
	v_max3_f32 v128, v128, |v104|, |v108|
	v_cmp_lt_i32_e32 vcc, v130, v137
	v_max3_f32 v131, v131, |v19|, |v23|
	v_max3_f32 v129, v129, |v81|, |v85|
	v_max3_f32 v128, v128, |v112|, |v116|
	v_cndmask_b32_e32 v130, v166, v130, vcc
	v_max3_f32 v131, v131, |v27|, |v31|
	v_max3_f32 v129, v129, |v89|, |v93|
	v_max3_f32 v128, v128, |v120|, |v124|
	v_lshlrev_b32_e32 v130, 2, v130
	v_max3_f32 v131, v131, |v35|, |v39|
	v_max3_f32 v129, v129, |v97|, |v101|
	ds_bpermute_b32 v139, v130, v128
	v_max3_f32 v131, v131, |v43|, |v47|
	v_max3_f32 v129, v129, |v105|, |v109|
	v_xor_b32_e32 v138, 16, v166
	v_max3_f32 v131, v131, |v51|, |v55|
	v_max3_f32 v129, v129, |v113|, |v117|
	v_cmp_lt_i32_e32 vcc, v138, v137
	v_xor_b32_e32 v182, 32, v166
	v_max3_f32 v131, v131, |v59|, |v63|
	v_max3_f32 v129, v129, |v121|, |v125|
	v_cndmask_b32_e32 v138, v166, v138, vcc
	v_cmp_lt_i32_e32 vcc, v182, v137
	v_max3_f32 v131, v131, |v67|, |v71|
	v_max3_f32 v131, v131, |v75|, |v79|
	v_cndmask_b32_e32 v137, v166, v182, vcc
	ds_bpermute_b32 v182, v130, v129
	s_waitcnt lgkmcnt(0)
	v_max_f32_e32 v139, v139, v139
	v_max3_f32 v131, v131, |v83|, |v87|
	v_lshlrev_b32_e32 v138, 2, v138
	v_max_f32_e32 v128, v128, v139
	v_max3_f32 v131, v131, |v91|, |v95|
	ds_bpermute_b32 v139, v138, v128
	v_max3_f32 v131, v131, |v99|, |v103|
	v_max3_f32 v131, v131, |v107|, |v111|
	v_lshlrev_b32_e32 v183, 2, v137
	v_max_f32_e32 v137, v182, v182
	v_max3_f32 v131, v131, |v115|, |v119|
	v_max_f32_e32 v137, v129, v137
	v_max3_f32 v131, v131, |v123|, |v127|
	ds_bpermute_b32 v182, v138, v137
	s_waitcnt lgkmcnt(1)
	v_max_f32_e32 v129, v139, v139
	ds_bpermute_b32 v139, v130, v136
	ds_bpermute_b32 v184, v130, v131
	v_max_f32_e32 v128, v128, v129
	s_waitcnt lgkmcnt(2)
	v_max_f32_e32 v182, v182, v182
	v_max_f32_e32 v130, v137, v182
	s_waitcnt lgkmcnt(1)
	v_max_f32_e32 v137, v139, v139
	s_waitcnt lgkmcnt(0)
	v_max_f32_e32 v139, v184, v184
	v_max_f32_e32 v136, v136, v137
	v_max_f32_e32 v139, v131, v139
	ds_bpermute_b32 v137, v138, v136
	ds_bpermute_b32 v138, v138, v139
	ds_bpermute_b32 v129, v183, v128
	ds_bpermute_b32 v131, v183, v130
	v_cvt_pk_bf16_f32 v180, v124, v125
	s_waitcnt lgkmcnt(3)
	v_max_f32_e32 v137, v137, v137
	s_waitcnt lgkmcnt(2)
	v_max_f32_e32 v138, v138, v138
	v_max_f32_e32 v136, v136, v137
	v_max_f32_e32 v138, v139, v138
	ds_bpermute_b32 v137, v183, v136
	ds_bpermute_b32 v139, v183, v138
	v_cvt_pk_bf16_f32 v181, v126, v127
	ds_write_b16 v176, v180
	ds_write_b16_d16_hi v176, v180 offset:4112
	ds_write_b16 v176, v181 offset:8224
	ds_write_b16_d16_hi v176, v181 offset:12336
	s_and_saveexec_b64 s[38:39], s[4:5]
	s_cbranch_execz .LBB0_1406
	s_waitcnt lgkmcnt(4)
	v_max_f32_e32 v139, v139, v139
	v_max_f32_e32 v138, v138, v138
	v_max_f32_e32 v137, v137, v137
	v_max_f32_e32 v136, v136, v136
	v_max_f32_e32 v131, v131, v131
	v_max_f32_e32 v130, v130, v130
	v_max_f32_e32 v129, v129, v129
	v_max_f32_e32 v128, v128, v128
	v_max_f32_e32 v139, v138, v139
	v_max_f32_e32 v138, v136, v137
	v_max_f32_e32 v137, v130, v131
	v_max_f32_e32 v136, v128, v129
	ds_write_b128 v177, v[136:139]

; #define SLAB_LOAD(dsc, v) do { if ((dsc).valid) { const GAS char* b_ = (const GAS char*)(dsc).W; unsigned o_ = (unsigned)((wave * 256 + kq) * (dsc).NS + c4) * 4u; const unsigned st_ = (unsigned)(dsc).NS * 32u; \
;     _Pragma("unroll") for (int i_ = 0; i_ < 32; ++i_) { v[i_] = __builtin_nontemporal_load((const GAS f32x4*)(b_ + o_)); o_ += st_; } } } while (0)
; __device__ __forceinline__ void do_slabs_impl(LAS unsigned char* lds, unsigned char* ws, const float* w_up, const float* w_dn, const float* w_in, int vcu, int G, int wave, int j0, int j1) {
;     ...
;         if (j + 1 < j1) { cur = slab_desc(F, j + 1); SLAB_LOAD(cur, v); }
.LBB0_1583:
	s_andn2_b64 vcc, exec, s[6:7]
	s_cbranch_vccnz .LBB0_1585
	v_readlane_b32 s0, v255, 49
	v_readlane_b32 s1, v255, 50
	v_add_u32_e32 v132, 0x10000, v192
	v_add_u32_e32 v136, 0x30000, v192
	s_waitcnt vmcnt(0)
	v_lshl_add_u64 v[92:93], s[0:1], 0, v[192:193]
	v_add_u32_e32 v140, 0x50000, v192
	v_add_u32_e32 v144, 0x70000, v192
	v_add_u32_e32 v148, 0x90000, v192
	v_add_u32_e32 v152, 0xb0000, v192
	v_add_u32_e32 v156, 0xd0000, v192
	v_add_u32_e32 v160, 0xf0000, v192
	v_add_u32_e32 v164, 0x110000, v192
	v_add_u32_e32 v168, 0x130000, v192
	v_add_u32_e32 v172, 0x150000, v192
	v_add_u32_e32 v176, 0x170000, v192
	v_add_u32_e32 v180, 0x190000, v192
	v_add_u32_e32 v184, 0x1b0000, v192
	v_add_u32_e32 v188, 0x1d0000, v192
	v_add_u32_e32 v134, 0x20000, v192
	global_load_dwordx4 v[92:95], v[92:93], off nt
	s_nop 0
	global_load_dwordx4 v[0:3], v132, s[0:1] nt
	global_load_dwordx4 v[4:7], v134, s[0:1] nt
	v_add_u32_e32 v138, 0x40000, v192
	global_load_dwordx4 v[8:11], v136, s[0:1] nt
	global_load_dwordx4 v[12:15], v138, s[0:1] nt
	v_add_u32_e32 v142, 0x60000, v192
	global_load_dwordx4 v[16:19], v140, s[0:1] nt
	global_load_dwordx4 v[20:23], v142, s[0:1] nt
	v_add_u32_e32 v146, 0x80000, v192
	global_load_dwordx4 v[24:27], v144, s[0:1] nt
	global_load_dwordx4 v[28:31], v146, s[0:1] nt
	v_add_u32_e32 v150, 0xa0000, v192
	global_load_dwordx4 v[32:35], v148, s[0:1] nt
	global_load_dwordx4 v[36:39], v150, s[0:1] nt
	v_add_u32_e32 v154, 0xc0000, v192
	global_load_dwordx4 v[40:43], v152, s[0:1] nt
	global_load_dwordx4 v[44:47], v154, s[0:1] nt
	v_add_u32_e32 v158, 0xe0000, v192
	global_load_dwordx4 v[48:51], v156, s[0:1] nt
	global_load_dwordx4 v[52:55], v158, s[0:1] nt
	v_add_u32_e32 v162, 0x100000, v192
	global_load_dwordx4 v[56:59], v160, s[0:1] nt
	global_load_dwordx4 v[60:63], v162, s[0:1] nt
	v_add_u32_e32 v166, 0x120000, v192
	global_load_dwordx4 v[64:67], v164, s[0:1] nt
	global_load_dwordx4 v[68:71], v166, s[0:1] nt
	v_add_u32_e32 v170, 0x140000, v192
	global_load_dwordx4 v[72:75], v168, s[0:1] nt
	global_load_dwordx4 v[76:79], v170, s[0:1] nt
	v_add_u32_e32 v174, 0x160000, v192
	global_load_dwordx4 v[80:83], v172, s[0:1] nt
	global_load_dwordx4 v[84:87], v174, s[0:1] nt
	v_add_u32_e32 v178, 0x180000, v192
	global_load_dwordx4 v[88:91], v176, s[0:1] nt
	global_load_dwordx4 v[96:99], v178, s[0:1] nt
	v_add_u32_e32 v182, 0x1a0000, v192
	global_load_dwordx4 v[100:103], v180, s[0:1] nt
	global_load_dwordx4 v[104:107], v182, s[0:1] nt
	v_add_u32_e32 v186, 0x1c0000, v192
	global_load_dwordx4 v[108:111], v184, s[0:1] nt
	global_load_dwordx4 v[112:115], v186, s[0:1] nt
	v_add_u32_e32 v190, 0x1e0000, v192
	global_load_dwordx4 v[116:119], v188, s[0:1] nt
	global_load_dwordx4 v[120:123], v190, s[0:1] nt
	v_add_u32_e32 v194, 0x1f0000, v192
	s_nop 0
	global_load_dwordx4 v[124:127], v194, s[0:1] nt
	v_mov_b32_e32 v133, v193
	v_mov_b32_e32 v135, v193
	v_mov_b32_e32 v137, v193
	v_mov_b32_e32 v139, v193
	v_mov_b32_e32 v141, v193
	v_mov_b32_e32 v143, v193
	v_mov_b32_e32 v145, v193
	v_mov_b32_e32 v147, v193
	v_mov_b32_e32 v149, v193
	v_mov_b32_e32 v151, v193
	v_mov_b32_e32 v153, v193
	v_mov_b32_e32 v155, v193
	v_mov_b32_e32 v157, v193
	v_mov_b32_e32 v159, v193
	v_mov_b32_e32 v161, v193
	v_mov_b32_e32 v163, v193
	v_mov_b32_e32 v165, v193
	v_mov_b32_e32 v167, v193
	v_mov_b32_e32 v169, v193
	v_mov_b32_e32 v171, v193
	v_mov_b32_e32 v173, v193
	v_mov_b32_e32 v175, v193
	v_mov_b32_e32 v177, v193
	v_mov_b32_e32 v179, v193
	v_mov_b32_e32 v181, v193
	v_mov_b32_e32 v183, v193
	v_mov_b32_e32 v185, v193
	v_mov_b32_e32 v187, v193
	v_mov_b32_e32 v189, v193
	v_mov_b32_e32 v191, v193
	v_mov_b32_e32 v195, v193

; __device__ __forceinline__ unsigned cvt_pk_bf16(float lo, float hi) { unsigned r; asm volatile("v_cvt_pk_bf16_f32 %0, %1, %2" : "=v"(r) : "v"(lo), "v"(hi)); return r; }
; __device__ __forceinline__ void do_slabs_impl(LAS unsigned char* lds, unsigned char* ws, const float* w_up, const float* w_dn, const float* w_in, int vcu, int G, int wave, int j0, int j1) {
;     ...
;         if (cur.valid) {
;             f32x4 mx = (f32x4){0.f, 0.f, 0.f, 0.f};
; #pragma unroll
;             for (int i = 0; i < 32; ++i) { const int k = wave * 256 + i * 8 + kq; const f32x4 x = v[i];
;                 mx[0] = fmaxf(mx[0], fabsf(x[0])); mx[1] = fmaxf(mx[1], fabsf(x[1])); mx[2] = fmaxf(mx[2], fabsf(x[2])); mx[3] = fmaxf(mx[3], fabsf(x[3]));
;                 const unsigned p01 = cvt_pk_bf16(x[0], x[1]), p23 = cvt_pk_bf16(x[2], x[3]);
;                 const int ks = k ^ (((c4 >> 3) & 3) << 3);
;                 slab[(c4 + 0) * PITCH + ks] = (bf16)(p01 & 0xffffu); slab[(c4 + 1) * PITCH + ks] = (bf16)(p01 >> 16); slab[(c4 + 2) * PITCH + ks] = (bf16)(p23 & 0xffffu); slab[(c4 + 3) * PITCH + ks] = (bf16)(p23 >> 16); }
.LBB0_1587:
	s_cmp_lg_u32 s2, 0
	s_cselect_b64 s[52:53], -1, 0
	s_cmp_eq_u32 s2, 0
	s_cbranch_scc1 .LBB0_1591
	s_waitcnt vmcnt(31)
	v_cvt_pk_bf16_f32 v128, v92, v93
	v_cvt_pk_bf16_f32 v129, v94, v95
	ds_write_b16 v211, v128
	ds_write_b16_d16_hi v211, v128 offset:4112
	ds_write_b16 v211, v129 offset:8224
	ds_write_b16_d16_hi v211, v129 offset:12336
	s_waitcnt vmcnt(30)
	v_cvt_pk_bf16_f32 v199, v0, v1
	v_cvt_pk_bf16_f32 v202, v2, v3
	ds_write_b16 v212, v199
	ds_write_b16_d16_hi v212, v199 offset:4112
	ds_write_b16 v212, v202 offset:8224
	ds_write_b16_d16_hi v212, v202 offset:12336
	s_waitcnt vmcnt(29)
	v_cvt_pk_bf16_f32 v199, v4, v5
	v_cvt_pk_bf16_f32 v202, v6, v7
	ds_write_b16 v213, v199
	ds_write_b16_d16_hi v213, v199 offset:4112
	ds_write_b16 v213, v202 offset:8224
	ds_write_b16_d16_hi v213, v202 offset:12336
	s_waitcnt vmcnt(28)
	v_cvt_pk_bf16_f32 v199, v8, v9
	v_cvt_pk_bf16_f32 v202, v10, v11
	ds_write_b16 v214, v199
	ds_write_b16_d16_hi v214, v199 offset:4112
	ds_write_b16 v214, v202 offset:8224
	ds_write_b16_d16_hi v214, v202 offset:12336
	s_waitcnt vmcnt(27)
	v_cvt_pk_bf16_f32 v199, v12, v13
	v_cvt_pk_bf16_f32 v202, v14, v15
	ds_write_b16 v215, v199
	ds_write_b16_d16_hi v215, v199 offset:4112
	ds_write_b16 v215, v202 offset:8224
	ds_write_b16_d16_hi v215, v202 offset:12336
	s_waitcnt vmcnt(26)
	v_cvt_pk_bf16_f32 v199, v16, v17
	v_cvt_pk_bf16_f32 v202, v18, v19
	ds_write_b16 v216, v199
	ds_write_b16_d16_hi v216, v199 offset:4112
	ds_write_b16 v216, v202 offset:8224
	ds_write_b16_d16_hi v216, v202 offset:12336
	s_waitcnt vmcnt(25)
	v_cvt_pk_bf16_f32 v199, v20, v21
	v_cvt_pk_bf16_f32 v202, v22, v23
	ds_write_b16 v217, v199
	ds_write_b16_d16_hi v217, v199 offset:4112
	ds_write_b16 v217, v202 offset:8224
	ds_write_b16_d16_hi v217, v202 offset:12336
	s_waitcnt vmcnt(24)
	v_cvt_pk_bf16_f32 v199, v24, v25
	v_cvt_pk_bf16_f32 v202, v26, v27
	ds_write_b16 v218, v199
	ds_write_b16_d16_hi v218, v199 offset:4112
	ds_write_b16 v218, v202 offset:8224
	ds_write_b16_d16_hi v218, v202 offset:12336
	s_waitcnt vmcnt(23)
	v_cvt_pk_bf16_f32 v199, v28, v29
	v_cvt_pk_bf16_f32 v202, v30, v31
	ds_write_b16 v219, v199
	ds_write_b16_d16_hi v219, v199 offset:4112
	ds_write_b16 v219, v202 offset:8224
	ds_write_b16_d16_hi v219, v202 offset:12336
	s_waitcnt vmcnt(22)
	v_cvt_pk_bf16_f32 v199, v32, v33
	v_cvt_pk_bf16_f32 v202, v34, v35
	ds_write_b16 v220, v199
	ds_write_b16_d16_hi v220, v199 offset:4112
	ds_write_b16 v220, v202 offset:8224
	ds_write_b16_d16_hi v220, v202 offset:12336
	s_waitcnt vmcnt(21)
	v_cvt_pk_bf16_f32 v199, v36, v37
	v_cvt_pk_bf16_f32 v202, v38, v39
	ds_write_b16 v221, v199
	ds_write_b16_d16_hi v221, v199 offset:4112
	ds_write_b16 v221, v202 offset:8224
	ds_write_b16_d16_hi v221, v202 offset:12336
	s_waitcnt vmcnt(20)
	v_cvt_pk_bf16_f32 v199, v40, v41
	v_cvt_pk_bf16_f32 v202, v42, v43
	ds_write_b16 v222, v199
	ds_write_b16_d16_hi v222, v199 offset:4112
	ds_write_b16 v222, v202 offset:8224
	ds_write_b16_d16_hi v222, v202 offset:12336
	s_waitcnt vmcnt(19)
	v_cvt_pk_bf16_f32 v199, v44, v45
	v_cvt_pk_bf16_f32 v202, v46, v47
	ds_write_b16 v223, v199
	ds_write_b16_d16_hi v223, v199 offset:4112
	ds_write_b16 v223, v202 offset:8224
	ds_write_b16_d16_hi v223, v202 offset:12336
	s_waitcnt vmcnt(18)
	v_cvt_pk_bf16_f32 v199, v48, v49
	v_cvt_pk_bf16_f32 v202, v50, v51
	ds_write_b16 v224, v199
	ds_write_b16_d16_hi v224, v199 offset:4112
	ds_write_b16 v224, v202 offset:8224
	ds_write_b16_d16_hi v224, v202 offset:12336
	s_waitcnt vmcnt(17)
	v_cvt_pk_bf16_f32 v199, v52, v53
	v_cvt_pk_bf16_f32 v202, v54, v55
	ds_write_b16 v225, v199
	ds_write_b16_d16_hi v225, v199 offset:4112
	ds_write_b16 v225, v202 offset:8224
	ds_write_b16_d16_hi v225, v202 offset:12336
	s_waitcnt vmcnt(16)
	v_cvt_pk_bf16_f32 v199, v56, v57
	v_cvt_pk_bf16_f32 v202, v58, v59
	ds_write_b16 v226, v199
	ds_write_b16_d16_hi v226, v199 offset:4112
	ds_write_b16 v226, v202 offset:8224
	ds_write_b16_d16_hi v226, v202 offset:12336
	s_waitcnt vmcnt(15)
	v_cvt_pk_bf16_f32 v199, v60, v61
	v_cvt_pk_bf16_f32 v202, v62, v63
	v_max3_f32 v130, |v94|, 0, |v2|
	ds_write_b16 v227, v199
	ds_write_b16_d16_hi v227, v199 offset:4112
	ds_write_b16 v227, v202 offset:8224
	ds_write_b16_d16_hi v227, v202 offset:12336
	s_waitcnt vmcnt(14)
	v_cvt_pk_bf16_f32 v199, v64, v65
	v_cvt_pk_bf16_f32 v202, v66, v67
	v_max3_f32 v130, v130, |v6|, |v10|
	ds_write_b16 v228, v199
	ds_write_b16_d16_hi v228, v199 offset:4112
	ds_write_b16 v228, v202 offset:8224
	ds_write_b16_d16_hi v228, v202 offset:12336
	s_waitcnt vmcnt(13)
	v_cvt_pk_bf16_f32 v199, v68, v69
	v_cvt_pk_bf16_f32 v202, v70, v71
	v_max3_f32 v130, v130, |v14|, |v18|
	ds_write_b16 v229, v199
	ds_write_b16_d16_hi v229, v199 offset:4112
	ds_write_b16 v229, v202 offset:8224
	ds_write_b16_d16_hi v229, v202 offset:12336
	s_waitcnt vmcnt(12)
	v_cvt_pk_bf16_f32 v199, v72, v73
	v_cvt_pk_bf16_f32 v202, v74, v75
	v_max3_f32 v128, |v92|, 0, |v0|
	v_max3_f32 v130, v130, |v22|, |v26|
	ds_write_b16 v230, v199
	ds_write_b16_d16_hi v230, v199 offset:4112
	ds_write_b16 v230, v202 offset:8224
	ds_write_b16_d16_hi v230, v202 offset:12336
	s_waitcnt vmcnt(11)
	v_cvt_pk_bf16_f32 v199, v76, v77
	v_cvt_pk_bf16_f32 v202, v78, v79
	v_max3_f32 v128, v128, |v4|, |v8|
	v_max3_f32 v130, v130, |v30|, |v34|
	ds_write_b16 v231, v199
	ds_write_b16_d16_hi v231, v199 offset:4112
	ds_write_b16 v231, v202 offset:8224
	ds_write_b16_d16_hi v231, v202 offset:12336
	s_waitcnt vmcnt(10)
	v_cvt_pk_bf16_f32 v199, v80, v81
	v_cvt_pk_bf16_f32 v202, v82, v83
	v_max3_f32 v128, v128, |v12|, |v16|
	v_max3_f32 v130, v130, |v38|, |v42|
	ds_write_b16 v232, v199
	ds_write_b16_d16_hi v232, v199 offset:4112
	ds_write_b16 v232, v202 offset:8224
	ds_write_b16_d16_hi v232, v202 offset:12336
	s_waitcnt vmcnt(9)
; #define LAS __attribute__((address_space(3)))
; __device__ __forceinline__ unsigned cvt_pk_bf16(float lo, float hi) { unsigned r; asm volatile("v_cvt_pk_bf16_f32 %0, %1, %2" : "=v"(r) : "v"(lo), "v"(hi)); return r; }
; __device__ __forceinline__ void do_slabs_impl(LAS unsigned char* lds, unsigned char* ws, const float* w_up, const float* w_dn, const float* w_in, int vcu, int G, int wave, int j0, int j1) {
;     ...
;         if (cur.valid) {
;             f32x4 mx = (f32x4){0.f, 0.f, 0.f, 0.f};
; #pragma unroll
;             for (int i = 0; i < 32; ++i) { const int k = wave * 256 + i * 8 + kq; const f32x4 x = v[i];
;                 mx[0] = fmaxf(mx[0], fabsf(x[0])); mx[1] = fmaxf(mx[1], fabsf(x[1])); mx[2] = fmaxf(mx[2], fabsf(x[2])); mx[3] = fmaxf(mx[3], fabsf(x[3]));
;                 const unsigned p01 = cvt_pk_bf16(x[0], x[1]), p23 = cvt_pk_bf16(x[2], x[3]);
;                 const int ks = k ^ (((c4 >> 3) & 3) << 3);
;                 slab[(c4 + 0) * PITCH + ks] = (bf16)(p01 & 0xffffu); slab[(c4 + 1) * PITCH + ks] = (bf16)(p01 >> 16); slab[(c4 + 2) * PITCH + ks] = (bf16)(p23 & 0xffffu); slab[(c4 + 3) * PITCH + ks] = (bf16)(p23 >> 16); }
; #pragma unroll
;             for (int q = 0; q < 4; ++q) { float m = mx[q]; m = fmaxf(m, __shfl_xor(m, 8)); m = fmaxf(m, __shfl_xor(m, 16)); m = fmaxf(m, __shfl_xor(m, 32)); mx[q] = m; }
;             if (lane < 8) { LAS float* d = red + wave * 32 + c4; d[0] = mx[0]; d[1] = mx[1]; d[2] = mx[2]; d[3] = mx[3]; }
	v_cvt_pk_bf16_f32 v199, v84, v85
	v_cvt_pk_bf16_f32 v202, v86, v87
	v_max3_f32 v128, v128, |v20|, |v24|
	v_max3_f32 v130, v130, |v46|, |v50|
	ds_write_b16 v233, v199
	ds_write_b16_d16_hi v233, v199 offset:4112
	ds_write_b16 v233, v202 offset:8224
	ds_write_b16_d16_hi v233, v202 offset:12336
	s_waitcnt vmcnt(8)
	v_cvt_pk_bf16_f32 v199, v88, v89
	v_cvt_pk_bf16_f32 v202, v90, v91
	v_max3_f32 v129, |v93|, 0, |v1|
	v_max3_f32 v128, v128, |v28|, |v32|
	v_max3_f32 v130, v130, |v54|, |v58|
	ds_write_b16 v234, v199
	ds_write_b16_d16_hi v234, v199 offset:4112
	ds_write_b16 v234, v202 offset:8224
	ds_write_b16_d16_hi v234, v202 offset:12336
	s_waitcnt vmcnt(7)
	v_cvt_pk_bf16_f32 v199, v96, v97
	v_cvt_pk_bf16_f32 v202, v98, v99
	v_max3_f32 v129, v129, |v5|, |v9|
	v_max3_f32 v128, v128, |v36|, |v40|
	v_max3_f32 v130, v130, |v62|, |v66|
	ds_write_b16 v235, v199
	ds_write_b16_d16_hi v235, v199 offset:4112
	ds_write_b16 v235, v202 offset:8224
	ds_write_b16_d16_hi v235, v202 offset:12336
	s_waitcnt vmcnt(6)
	v_cvt_pk_bf16_f32 v199, v100, v101
	v_cvt_pk_bf16_f32 v202, v102, v103
	v_max3_f32 v129, v129, |v13|, |v17|
	v_max3_f32 v128, v128, |v44|, |v48|
	v_max3_f32 v130, v130, |v70|, |v74|
	ds_write_b16 v236, v199
	ds_write_b16_d16_hi v236, v199 offset:4112
	ds_write_b16 v236, v202 offset:8224
	ds_write_b16_d16_hi v236, v202 offset:12336
	s_waitcnt vmcnt(5)
	v_cvt_pk_bf16_f32 v199, v104, v105
	v_cvt_pk_bf16_f32 v202, v106, v107
	v_max3_f32 v129, v129, |v21|, |v25|
	v_max3_f32 v128, v128, |v52|, |v56|
	v_max3_f32 v130, v130, |v78|, |v82|
	ds_write_b16 v237, v199
	ds_write_b16_d16_hi v237, v199 offset:4112
	ds_write_b16 v237, v202 offset:8224
	ds_write_b16_d16_hi v237, v202 offset:12336
	s_waitcnt vmcnt(4)
	v_cvt_pk_bf16_f32 v199, v108, v109
	v_cvt_pk_bf16_f32 v202, v110, v111
	v_max3_f32 v129, v129, |v29|, |v33|
	v_max3_f32 v128, v128, |v60|, |v64|
	v_max3_f32 v130, v130, |v86|, |v90|
	ds_write_b16 v238, v199
	ds_write_b16_d16_hi v238, v199 offset:4112
	ds_write_b16 v238, v202 offset:8224
	ds_write_b16_d16_hi v238, v202 offset:12336
	s_waitcnt vmcnt(3)
	v_cvt_pk_bf16_f32 v199, v112, v113
	v_cvt_pk_bf16_f32 v202, v114, v115
	v_max3_f32 v129, v129, |v37|, |v41|
	v_max3_f32 v128, v128, |v68|, |v72|
	v_max3_f32 v130, v130, |v98|, |v102|
	ds_write_b16 v239, v199
	ds_write_b16_d16_hi v239, v199 offset:4112
	ds_write_b16 v239, v202 offset:8224
	ds_write_b16_d16_hi v239, v202 offset:12336
	s_waitcnt vmcnt(2)
	v_cvt_pk_bf16_f32 v199, v116, v117
	v_cvt_pk_bf16_f32 v202, v118, v119
	v_max3_f32 v129, v129, |v45|, |v49|
	v_max3_f32 v128, v128, |v76|, |v80|
	v_max3_f32 v130, v130, |v106|, |v110|
	ds_write_b16 v240, v199
	ds_write_b16_d16_hi v240, v199 offset:4112
	ds_write_b16 v240, v202 offset:8224
	ds_write_b16_d16_hi v240, v202 offset:12336
	s_waitcnt vmcnt(1)
	v_cvt_pk_bf16_f32 v199, v120, v121
	v_cvt_pk_bf16_f32 v202, v122, v123
	v_max3_f32 v129, v129, |v53|, |v57|
	v_max3_f32 v128, v128, |v84|, |v88|
	v_max3_f32 v130, v130, |v114|, |v118|
	ds_write_b16 v241, v199
	ds_write_b16_d16_hi v241, v199 offset:4112
	ds_write_b16 v241, v202 offset:8224
	ds_write_b16_d16_hi v241, v202 offset:12336
	v_and_b32_e32 v202, 64, v205
	v_max3_f32 v131, |v95|, 0, |v3|
	v_max3_f32 v129, v129, |v61|, |v65|
	v_max3_f32 v128, v128, |v96|, |v100|
	s_waitcnt vmcnt(0)
	v_max3_f32 v199, v130, |v122|, |v126|
	v_xor_b32_e32 v130, 8, v205
	v_add_u32_e32 v202, 64, v202
	v_max3_f32 v131, v131, |v7|, |v11|
	v_max3_f32 v129, v129, |v69|, |v73|
	v_max3_f32 v128, v128, |v104|, |v108|
	v_cmp_lt_i32_e32 vcc, v130, v202
	v_max3_f32 v131, v131, |v15|, |v19|
	v_max3_f32 v129, v129, |v77|, |v81|
	v_max3_f32 v128, v128, |v112|, |v116|
	v_cndmask_b32_e32 v130, v205, v130, vcc
	v_max3_f32 v131, v131, |v23|, |v27|
	v_max3_f32 v129, v129, |v85|, |v89|
	v_max3_f32 v128, v128, |v120|, |v124|
	v_lshlrev_b32_e32 v130, 2, v130
	v_max3_f32 v131, v131, |v31|, |v35|
	v_max3_f32 v129, v129, |v97|, |v101|
	ds_bpermute_b32 v243, v130, v128
	v_max3_f32 v131, v131, |v39|, |v43|
	v_max3_f32 v129, v129, |v105|, |v109|
	v_xor_b32_e32 v203, 16, v205
	v_max3_f32 v131, v131, |v47|, |v51|
	v_max3_f32 v129, v129, |v113|, |v117|
	v_cmp_lt_i32_e32 vcc, v203, v202
	v_xor_b32_e32 v246, 32, v205
	v_max3_f32 v131, v131, |v55|, |v59|
	v_max3_f32 v129, v129, |v121|, |v125|
	v_cndmask_b32_e32 v203, v205, v203, vcc
	v_cmp_lt_i32_e32 vcc, v246, v202
	v_max3_f32 v131, v131, |v63|, |v67|
	v_max3_f32 v131, v131, |v71|, |v75|
	v_cndmask_b32_e32 v202, v205, v246, vcc
	ds_bpermute_b32 v246, v130, v129
	s_waitcnt lgkmcnt(0)
	v_max_f32_e32 v243, v243, v243
	v_max3_f32 v131, v131, |v79|, |v83|
	v_lshlrev_b32_e32 v203, 2, v203
	v_max_f32_e32 v128, v128, v243
	v_max3_f32 v131, v131, |v87|, |v91|
	ds_bpermute_b32 v243, v203, v128
	v_max3_f32 v131, v131, |v99|, |v103|
	v_max3_f32 v131, v131, |v107|, |v111|
	v_lshlrev_b32_e32 v247, 2, v202
	s_waitcnt lgkmcnt(1)
	v_max_f32_e32 v202, v246, v246
	v_max3_f32 v131, v131, |v115|, |v119|
	v_max_f32_e32 v202, v129, v202
	v_max3_f32 v131, v131, |v123|, |v127|
	ds_bpermute_b32 v246, v203, v202
	s_waitcnt lgkmcnt(1)
	v_max_f32_e32 v129, v243, v243
	ds_bpermute_b32 v243, v130, v199
	ds_bpermute_b32 v248, v130, v131
	v_max_f32_e32 v128, v128, v129
	s_waitcnt lgkmcnt(2)
	v_max_f32_e32 v246, v246, v246
	v_max_f32_e32 v130, v202, v246
	s_waitcnt lgkmcnt(1)
	v_max_f32_e32 v202, v243, v243
	s_waitcnt lgkmcnt(0)
	v_max_f32_e32 v243, v248, v248
	v_max_f32_e32 v199, v199, v202
	v_max_f32_e32 v243, v131, v243
	ds_bpermute_b32 v202, v203, v199
	ds_bpermute_b32 v203, v203, v243
	ds_bpermute_b32 v129, v247, v128
	ds_bpermute_b32 v131, v247, v130
	v_cvt_pk_bf16_f32 v244, v124, v125
	s_waitcnt lgkmcnt(3)
	v_max_f32_e32 v202, v202, v202
	s_waitcnt lgkmcnt(2)
	v_max_f32_e32 v203, v203, v203
	v_max_f32_e32 v199, v199, v202
	v_max_f32_e32 v203, v243, v203
	ds_bpermute_b32 v202, v247, v199
	ds_bpermute_b32 v243, v247, v203
	v_cvt_pk_bf16_f32 v245, v126, v127
	ds_write_b16 v242, v244
	ds_write_b16_d16_hi v242, v244 offset:4112
	ds_write_b16 v242, v245 offset:8224
	ds_write_b16_d16_hi v242, v245 offset:12336
	s_and_saveexec_b64 s[48:49], s[6:7]
	s_cbranch_execz .LBB0_1590
	s_waitcnt lgkmcnt(4)
	v_max_f32_e32 v243, v243, v243
	v_max_f32_e32 v203, v203, v203
	v_max_f32_e32 v202, v202, v202
	v_max_f32_e32 v199, v199, v199
	v_max_f32_e32 v131, v131, v131
	v_max_f32_e32 v130, v130, v130
	v_max_f32_e32 v129, v129, v129
	v_max_f32_e32 v128, v128, v128
	v_max_f32_e32 v247, v203, v243
	v_max_f32_e32 v246, v199, v202
	v_max_f32_e32 v245, v130, v131
	v_max_f32_e32 v244, v128, v129
	ds_write_b128 v208, v[244:247]
